# weight rows permuted inside 256-row tiles at conversion (W_in, W_out, FFN down) so a wave owns 64 consecutive output cols; hand-written EpiProj + residual epilogues with full 128B-line stores (DPP hal
# speedup vs baseline: 1.0058x; 1.0057x over previous
.LBB0_58:
	s_waitcnt vmcnt(0)
	v_bfe_u32 v0, v6, 16, 1
	s_movk_i32 s7, 0x7fff
	v_add3_u32 v0, v6, v0, s7
	ds_write_b16_d16_hi v78, v0
	v_bfe_u32 v0, v7, 16, 1
	v_add3_u32 v0, v7, v0, s7
	ds_write_b16_d16_hi v78, v0 offset:136
	v_bfe_u32 v0, v8, 16, 1
	v_add3_u32 v0, v8, v0, s7
	ds_write_b16_d16_hi v78, v0 offset:272
	v_bfe_u32 v0, v9, 16, 1
	v_add3_u32 v0, v9, v0, s7
	ds_write_b16_d16_hi v78, v0 offset:408
	v_bfe_u32 v0, v10, 16, 1
	v_add3_u32 v0, v10, v0, s7
	ds_write_b16_d16_hi v78, v0 offset:8
	v_bfe_u32 v0, v11, 16, 1
	v_add3_u32 v0, v11, v0, s7
	ds_write_b16_d16_hi v78, v0 offset:144
	v_bfe_u32 v0, v12, 16, 1
	v_add3_u32 v0, v12, v0, s7
	ds_write_b16_d16_hi v78, v0 offset:280
	v_bfe_u32 v0, v13, 16, 1
	v_add3_u32 v0, v13, v0, s7
	ds_write_b16_d16_hi v78, v0 offset:416
	v_bfe_u32 v0, v14, 16, 1
	v_add3_u32 v0, v14, v0, s7
	ds_write_b16_d16_hi v78, v0 offset:16
	v_bfe_u32 v0, v15, 16, 1
	v_add3_u32 v0, v15, v0, s7
	ds_write_b16_d16_hi v78, v0 offset:152
	v_bfe_u32 v0, v16, 16, 1
	v_add3_u32 v0, v16, v0, s7
	ds_write_b16_d16_hi v78, v0 offset:288
	v_bfe_u32 v0, v17, 16, 1
	v_add3_u32 v0, v17, v0, s7
	ds_write_b16_d16_hi v78, v0 offset:424
	v_bfe_u32 v0, v18, 16, 1
	v_add3_u32 v0, v18, v0, s7
	ds_write_b16_d16_hi v78, v0 offset:24
	v_bfe_u32 v0, v19, 16, 1
	v_add3_u32 v0, v19, v0, s7
	ds_write_b16_d16_hi v78, v0 offset:160
	v_bfe_u32 v0, v20, 16, 1
	v_add3_u32 v0, v20, v0, s7
	ds_write_b16_d16_hi v78, v0 offset:296
	v_bfe_u32 v0, v21, 16, 1
	v_add3_u32 v0, v21, v0, s7
	ds_write_b16_d16_hi v78, v0 offset:432
	v_bfe_u32 v0, v22, 16, 1
	v_add3_u32 v0, v22, v0, s7
	ds_write_b16_d16_hi v78, v0 offset:32
	v_bfe_u32 v0, v23, 16, 1
	v_add3_u32 v0, v23, v0, s7
	ds_write_b16_d16_hi v78, v0 offset:168
	v_bfe_u32 v0, v24, 16, 1
	v_add3_u32 v0, v24, v0, s7
	ds_write_b16_d16_hi v78, v0 offset:304
	v_bfe_u32 v0, v25, 16, 1
	v_add3_u32 v0, v25, v0, s7
	ds_write_b16_d16_hi v78, v0 offset:440
	v_bfe_u32 v0, v26, 16, 1
	v_add3_u32 v0, v26, v0, s7
	ds_write_b16_d16_hi v78, v0 offset:40
	v_bfe_u32 v0, v27, 16, 1
	v_add3_u32 v0, v27, v0, s7
	ds_write_b16_d16_hi v78, v0 offset:176
	v_bfe_u32 v0, v28, 16, 1
	v_add3_u32 v0, v28, v0, s7
	ds_write_b16_d16_hi v78, v0 offset:312
	v_bfe_u32 v0, v29, 16, 1
	v_add3_u32 v0, v29, v0, s7
	ds_write_b16_d16_hi v78, v0 offset:448
	v_bfe_u32 v0, v30, 16, 1
	v_add3_u32 v0, v30, v0, s7
	ds_write_b16_d16_hi v78, v0 offset:48
	v_bfe_u32 v0, v31, 16, 1
	v_add3_u32 v0, v31, v0, s7
	ds_write_b16_d16_hi v78, v0 offset:184
	v_bfe_u32 v0, v32, 16, 1
	v_add3_u32 v0, v32, v0, s7
	ds_write_b16_d16_hi v78, v0 offset:320
	v_bfe_u32 v0, v33, 16, 1
	v_add3_u32 v0, v33, v0, s7
	ds_write_b16_d16_hi v78, v0 offset:456
	v_bfe_u32 v0, v34, 16, 1
	v_add3_u32 v0, v34, v0, s7
	ds_write_b16_d16_hi v78, v0 offset:56
	v_bfe_u32 v0, v35, 16, 1
	v_add3_u32 v0, v35, v0, s7
	ds_write_b16_d16_hi v78, v0 offset:192
	v_bfe_u32 v0, v36, 16, 1
	v_add3_u32 v0, v36, v0, s7
	ds_write_b16_d16_hi v78, v0 offset:328
	v_bfe_u32 v0, v37, 16, 1
	v_add3_u32 v0, v37, v0, s7
	ds_write_b16_d16_hi v78, v0 offset:464
	v_bfe_u32 v0, v38, 16, 1
	v_add3_u32 v0, v38, v0, s7
	ds_write_b16_d16_hi v78, v0 offset:64
	v_bfe_u32 v0, v39, 16, 1
	v_add3_u32 v0, v39, v0, s7
	ds_write_b16_d16_hi v78, v0 offset:200
	v_bfe_u32 v0, v40, 16, 1
	v_add3_u32 v0, v40, v0, s7
	ds_write_b16_d16_hi v78, v0 offset:336
	v_bfe_u32 v0, v41, 16, 1
	v_add3_u32 v0, v41, v0, s7
	ds_write_b16_d16_hi v78, v0 offset:472
	v_bfe_u32 v0, v42, 16, 1
	v_add3_u32 v0, v42, v0, s7
	ds_write_b16_d16_hi v78, v0 offset:72
	v_bfe_u32 v0, v43, 16, 1
	v_add3_u32 v0, v43, v0, s7
	ds_write_b16_d16_hi v78, v0 offset:208
	v_bfe_u32 v0, v44, 16, 1
	v_add3_u32 v0, v44, v0, s7
	ds_write_b16_d16_hi v78, v0 offset:344
	v_bfe_u32 v0, v45, 16, 1
	v_add3_u32 v0, v45, v0, s7
	ds_write_b16_d16_hi v78, v0 offset:480
	v_bfe_u32 v0, v46, 16, 1
	v_add3_u32 v0, v46, v0, s7
	ds_write_b16_d16_hi v78, v0 offset:80
	v_bfe_u32 v0, v47, 16, 1
	v_add3_u32 v0, v47, v0, s7
	ds_write_b16_d16_hi v78, v0 offset:216
	v_bfe_u32 v0, v48, 16, 1
	v_add3_u32 v0, v48, v0, s7
	ds_write_b16_d16_hi v78, v0 offset:352
	v_bfe_u32 v0, v49, 16, 1
	v_add3_u32 v0, v49, v0, s7
	ds_write_b16_d16_hi v78, v0 offset:488
	v_bfe_u32 v0, v50, 16, 1
	v_add3_u32 v0, v50, v0, s7
	ds_write_b16_d16_hi v78, v0 offset:88
	v_bfe_u32 v0, v51, 16, 1
	v_add3_u32 v0, v51, v0, s7
	ds_write_b16_d16_hi v78, v0 offset:224
	v_bfe_u32 v0, v52, 16, 1
	v_add3_u32 v0, v52, v0, s7
	ds_write_b16_d16_hi v78, v0 offset:360
	v_bfe_u32 v0, v53, 16, 1
	v_add3_u32 v0, v53, v0, s7
	ds_write_b16_d16_hi v78, v0 offset:496
	v_bfe_u32 v0, v54, 16, 1
	v_add3_u32 v0, v54, v0, s7
	ds_write_b16_d16_hi v78, v0 offset:96
	v_bfe_u32 v0, v55, 16, 1
	v_add3_u32 v0, v55, v0, s7
	ds_write_b16_d16_hi v78, v0 offset:232
	v_bfe_u32 v0, v56, 16, 1
	v_add3_u32 v0, v56, v0, s7
	ds_write_b16_d16_hi v78, v0 offset:368
	v_bfe_u32 v0, v57, 16, 1
	v_add3_u32 v0, v57, v0, s7
	ds_write_b16_d16_hi v78, v0 offset:504
	v_bfe_u32 v0, v58, 16, 1
	v_add3_u32 v0, v58, v0, s7
	ds_write_b16_d16_hi v78, v0 offset:104
	v_bfe_u32 v0, v59, 16, 1
	v_add3_u32 v0, v59, v0, s7
	ds_write_b16_d16_hi v78, v0 offset:240
	v_bfe_u32 v0, v60, 16, 1
	v_add3_u32 v0, v60, v0, s7
	ds_write_b16_d16_hi v78, v0 offset:376
	v_bfe_u32 v0, v61, 16, 1
	v_add3_u32 v0, v61, v0, s7
	ds_write_b16_d16_hi v78, v0 offset:512
	v_bfe_u32 v0, v62, 16, 1
	v_add3_u32 v0, v62, v0, s7
	ds_write_b16_d16_hi v78, v0 offset:112
	v_bfe_u32 v0, v63, 16, 1
	v_add3_u32 v0, v63, v0, s7
	ds_write_b16_d16_hi v78, v0 offset:248
	v_bfe_u32 v0, v64, 16, 1
	v_add3_u32 v0, v64, v0, s7
	ds_write_b16_d16_hi v78, v0 offset:384
	v_bfe_u32 v0, v65, 16, 1
	v_add3_u32 v0, v65, v0, s7
	ds_write_b16_d16_hi v78, v0 offset:520
	v_bfe_u32 v0, v66, 16, 1
	v_add3_u32 v0, v66, v0, s7
	ds_write_b16_d16_hi v78, v0 offset:120
	v_bfe_u32 v0, v67, 16, 1
	v_add3_u32 v0, v67, v0, s7
	ds_write_b16_d16_hi v78, v0 offset:256
	v_bfe_u32 v0, v68, 16, 1
	v_add3_u32 v0, v68, v0, s7
	ds_write_b16_d16_hi v78, v0 offset:392
	v_bfe_u32 v0, v69, 16, 1
	v_add3_u32 v0, v69, v0, s7
	ds_write_b16_d16_hi v78, v0 offset:528
	s_waitcnt lgkmcnt(0)
	v_add_u32_e32 v0, s8, v70
	v_cmp_gt_i32_e32 vcc, s13, v0
	s_and_saveexec_b64 s[8:9], vcc
	s_cbranch_execz .LBB0_23
	s_movk_i32 s7, 0x78c
	v_add_u32_e32 v2, 0x74, v0
	v_cmp_gt_i32_e32 vcc, s7, v0
	ds_read2_b64 v[6:9], v80 offset1:1
	ds_read2_b64 v[10:13], v80 offset0:2 offset1:3
	v_cndmask_b32_e32 v2, v2, v0, vcc
	v_bfe_u32 v18, v2, 6, 2
	v_bfe_u32 v19, v2, 5, 1
	v_and_b32_e32 v2, 0xffffff1f, v2
	v_lshl_or_b32 v2, v18, 5, v2
	v_lshl_or_b32 v2, v19, 7, v2
	ds_read2_b64 v[14:17], v80 offset0:4 offset1:5
	v_ashrrev_i32_e32 v3, 31, v2
	v_lshlrev_b64 v[2:3], 11, v[2:3]
	v_lshl_add_u64 v[2:3], s[0:1], 0, v[2:3]
	s_ashr_i32 s7, s6, 31
	v_lshl_add_u64 v[2:3], s[6:7], 1, v[2:3]
	s_waitcnt lgkmcnt(2)
	global_store_dwordx4 v[2:3], v[6:9], off
	s_waitcnt lgkmcnt(1)
	global_store_dwordx4 v[2:3], v[10:13], off offset:16
	s_waitcnt lgkmcnt(0)
	global_store_dwordx4 v[2:3], v[14:17], off offset:32
	ds_read2_b64 v[6:9], v80 offset0:6 offset1:7
	ds_read2_b64 v[10:13], v80 offset0:8 offset1:9
	ds_read2_b64 v[14:17], v80 offset0:10 offset1:11
	ds_read2_b64 v[18:21], v80 offset0:12 offset1:13
	ds_read2_b64 v[22:25], v80 offset0:14 offset1:15
	s_waitcnt lgkmcnt(4)
	global_store_dwordx4 v[2:3], v[6:9], off offset:48
	s_waitcnt lgkmcnt(3)
	global_store_dwordx4 v[2:3], v[10:13], off offset:64
	s_waitcnt lgkmcnt(2)
	global_store_dwordx4 v[2:3], v[14:17], off offset:80
	s_waitcnt lgkmcnt(1)
	global_store_dwordx4 v[2:3], v[18:21], off offset:96
	s_waitcnt lgkmcnt(0)
	global_store_dwordx4 v[2:3], v[22:25], off offset:112
	s_branch .LBB0_23

.LBB0_62:
	v_ashrrev_i32_e32 v3, 31, v2
	v_lshrrev_b32_e32 v3, 25, v3
	v_add_u32_e32 v3, v2, v3
	v_ashrrev_i32_e32 v8, 7, v3
	v_ashrrev_i32_e32 v9, 31, v8
	v_lshlrev_b32_e32 v3, 10, v8
	v_add_u32_e32 v8, 0x78c, v8
	v_bfe_u32 v10, v8, 6, 2
	v_bfe_u32 v11, v8, 5, 1
	v_and_b32_e32 v8, 0xffffff1f, v8
	v_lshl_or_b32 v8, v10, 5, v8
	v_lshl_or_b32 v8, v11, 7, v8
	v_mov_b32_e32 v9, 0
	v_lshlrev_b64 v[8:9], 11, v[8:9]
	v_sub_u32_e32 v10, v0, v3
	v_add_u32_e32 v2, s6, v2
	s_movk_i32 s8, 0x39ff
	v_lshl_add_u64 v[8:9], s[0:1], 0, v[8:9]
	v_ashrrev_i32_e32 v11, 31, v10
	v_cmp_lt_i32_e32 vcc, s8, v2
	v_lshl_add_u64 v[8:9], v[10:11], 1, v[8:9]
	s_or_b64 s[4:5], vcc, s[4:5]
	v_add_co_u32_e32 v8, vcc, 0, v8
	v_add_u32_e32 v0, s7, v0
	s_nop 0
	v_addc_co_u32_e32 v9, vcc, 0, v9, vcc
	global_store_dwordx4 v[8:9], v[4:7], off
	s_andn2_b64 exec, exec, s[4:5]
	s_cbranch_execnz .LBB0_62

.LBB0_135:
	s_or_b64 exec, exec, s[10:11]
	s_waitcnt vmcnt(0)
	v_bfe_u32 v74, v10, 16, 1
	s_movk_i32 s2, 0x7fff
	v_add3_u32 v10, v10, v74, s2
	ds_write_b16_d16_hi v0, v10
	v_bfe_u32 v10, v11, 16, 1
	v_add3_u32 v10, v11, v10, s2
	ds_write_b16_d16_hi v0, v10 offset:136
	v_bfe_u32 v10, v12, 16, 1
	v_add3_u32 v10, v12, v10, s2
	ds_write_b16_d16_hi v0, v10 offset:272
	v_bfe_u32 v10, v13, 16, 1
	v_add3_u32 v10, v13, v10, s2
	ds_write_b16_d16_hi v0, v10 offset:408
	v_bfe_u32 v10, v6, 16, 1
	v_add3_u32 v6, v6, v10, s2
	ds_write_b16_d16_hi v0, v6 offset:8
	v_bfe_u32 v6, v7, 16, 1
	v_add3_u32 v6, v7, v6, s2
	ds_write_b16_d16_hi v0, v6 offset:144
	v_bfe_u32 v6, v8, 16, 1
	v_add3_u32 v6, v8, v6, s2
	ds_write_b16_d16_hi v0, v6 offset:280
	v_bfe_u32 v6, v9, 16, 1
	v_add3_u32 v6, v9, v6, s2
	ds_write_b16_d16_hi v0, v6 offset:416
	v_bfe_u32 v6, v18, 16, 1
	v_add3_u32 v6, v18, v6, s2
	ds_write_b16_d16_hi v0, v6 offset:16
	v_bfe_u32 v6, v19, 16, 1
	v_add3_u32 v6, v19, v6, s2
	ds_write_b16_d16_hi v0, v6 offset:152
	v_bfe_u32 v6, v20, 16, 1
	v_add3_u32 v6, v20, v6, s2
	ds_write_b16_d16_hi v0, v6 offset:288
	v_bfe_u32 v6, v21, 16, 1
	v_add3_u32 v6, v21, v6, s2
	ds_write_b16_d16_hi v0, v6 offset:424
	v_bfe_u32 v6, v14, 16, 1
	v_add3_u32 v6, v14, v6, s2
	ds_write_b16_d16_hi v0, v6 offset:24
	v_bfe_u32 v6, v15, 16, 1
	v_add3_u32 v6, v15, v6, s2
	ds_write_b16_d16_hi v0, v6 offset:160
	v_bfe_u32 v6, v16, 16, 1
	v_add3_u32 v6, v16, v6, s2
	ds_write_b16_d16_hi v0, v6 offset:296
	v_bfe_u32 v6, v17, 16, 1
	v_add3_u32 v6, v17, v6, s2
	ds_write_b16_d16_hi v0, v6 offset:432
	v_bfe_u32 v6, v26, 16, 1
	v_add3_u32 v6, v26, v6, s2
	ds_write_b16_d16_hi v0, v6 offset:32
	v_bfe_u32 v6, v27, 16, 1
	v_add3_u32 v6, v27, v6, s2
	ds_write_b16_d16_hi v0, v6 offset:168
	v_bfe_u32 v6, v28, 16, 1
	v_add3_u32 v6, v28, v6, s2
	ds_write_b16_d16_hi v0, v6 offset:304
	v_bfe_u32 v6, v29, 16, 1
	v_add3_u32 v6, v29, v6, s2
	ds_write_b16_d16_hi v0, v6 offset:440
	v_bfe_u32 v6, v22, 16, 1
	v_add3_u32 v6, v22, v6, s2
	ds_write_b16_d16_hi v0, v6 offset:40
	v_bfe_u32 v6, v23, 16, 1
	v_add3_u32 v6, v23, v6, s2
	ds_write_b16_d16_hi v0, v6 offset:176
	v_bfe_u32 v6, v24, 16, 1
	v_add3_u32 v6, v24, v6, s2
	ds_write_b16_d16_hi v0, v6 offset:312
	v_bfe_u32 v6, v25, 16, 1
	v_add3_u32 v6, v25, v6, s2
	ds_write_b16_d16_hi v0, v6 offset:448
	v_bfe_u32 v6, v34, 16, 1
	v_add3_u32 v6, v34, v6, s2
	ds_write_b16_d16_hi v0, v6 offset:48
	v_bfe_u32 v6, v35, 16, 1
	v_add3_u32 v6, v35, v6, s2
	ds_write_b16_d16_hi v0, v6 offset:184
	v_bfe_u32 v6, v36, 16, 1
	v_add3_u32 v6, v36, v6, s2
	ds_write_b16_d16_hi v0, v6 offset:320
	v_bfe_u32 v6, v37, 16, 1
	v_add3_u32 v6, v37, v6, s2
	ds_write_b16_d16_hi v0, v6 offset:456
	v_bfe_u32 v6, v30, 16, 1
	v_add3_u32 v6, v30, v6, s2
	ds_write_b16_d16_hi v0, v6 offset:56
	v_bfe_u32 v6, v31, 16, 1
	v_add3_u32 v6, v31, v6, s2
	ds_write_b16_d16_hi v0, v6 offset:192
	v_bfe_u32 v6, v32, 16, 1
	v_add3_u32 v6, v32, v6, s2
	ds_write_b16_d16_hi v0, v6 offset:328
	v_bfe_u32 v6, v33, 16, 1
	v_add3_u32 v6, v33, v6, s2
	ds_write_b16_d16_hi v0, v6 offset:464
	v_bfe_u32 v6, v42, 16, 1
	v_add3_u32 v6, v42, v6, s2
	ds_write_b16_d16_hi v0, v6 offset:64
	v_bfe_u32 v6, v43, 16, 1
	v_add3_u32 v6, v43, v6, s2
	ds_write_b16_d16_hi v0, v6 offset:200
	v_bfe_u32 v6, v44, 16, 1
	v_add3_u32 v6, v44, v6, s2
	ds_write_b16_d16_hi v0, v6 offset:336
	v_bfe_u32 v6, v45, 16, 1
	v_add3_u32 v6, v45, v6, s2
	ds_write_b16_d16_hi v0, v6 offset:472
	v_bfe_u32 v6, v38, 16, 1
	v_add3_u32 v6, v38, v6, s2
	ds_write_b16_d16_hi v0, v6 offset:72
	v_bfe_u32 v6, v39, 16, 1
	v_add3_u32 v6, v39, v6, s2
	ds_write_b16_d16_hi v0, v6 offset:208
	v_bfe_u32 v6, v40, 16, 1
	v_add3_u32 v6, v40, v6, s2
	ds_write_b16_d16_hi v0, v6 offset:344
	v_bfe_u32 v6, v41, 16, 1
	v_add3_u32 v6, v41, v6, s2
	ds_write_b16_d16_hi v0, v6 offset:480
	v_bfe_u32 v6, v50, 16, 1
	v_add3_u32 v6, v50, v6, s2
	ds_write_b16_d16_hi v0, v6 offset:80
	v_bfe_u32 v6, v51, 16, 1
	v_add3_u32 v6, v51, v6, s2
	ds_write_b16_d16_hi v0, v6 offset:216
	v_bfe_u32 v6, v52, 16, 1
	v_add3_u32 v6, v52, v6, s2
	ds_write_b16_d16_hi v0, v6 offset:352
	v_bfe_u32 v6, v53, 16, 1
	v_add3_u32 v6, v53, v6, s2
	ds_write_b16_d16_hi v0, v6 offset:488
	v_bfe_u32 v6, v46, 16, 1
	v_add3_u32 v6, v46, v6, s2
	ds_write_b16_d16_hi v0, v6 offset:88
	v_bfe_u32 v6, v47, 16, 1
	v_add3_u32 v6, v47, v6, s2
	ds_write_b16_d16_hi v0, v6 offset:224
	v_bfe_u32 v6, v48, 16, 1
	v_add3_u32 v6, v48, v6, s2
	ds_write_b16_d16_hi v0, v6 offset:360
	v_bfe_u32 v6, v49, 16, 1
	v_add3_u32 v6, v49, v6, s2
	ds_write_b16_d16_hi v0, v6 offset:496
	v_bfe_u32 v6, v58, 16, 1
	v_add3_u32 v6, v58, v6, s2
	ds_write_b16_d16_hi v0, v6 offset:96
	v_bfe_u32 v6, v59, 16, 1
	v_add3_u32 v6, v59, v6, s2
	ds_write_b16_d16_hi v0, v6 offset:232
	v_bfe_u32 v6, v60, 16, 1
	v_add3_u32 v6, v60, v6, s2
	ds_write_b16_d16_hi v0, v6 offset:368
	v_bfe_u32 v6, v61, 16, 1
	v_add3_u32 v6, v61, v6, s2
	ds_write_b16_d16_hi v0, v6 offset:504
	v_bfe_u32 v6, v54, 16, 1
	v_add3_u32 v6, v54, v6, s2
	ds_write_b16_d16_hi v0, v6 offset:104
	v_bfe_u32 v6, v55, 16, 1
	v_add3_u32 v6, v55, v6, s2
	ds_write_b16_d16_hi v0, v6 offset:240
	v_bfe_u32 v6, v56, 16, 1
	v_add3_u32 v6, v56, v6, s2
	ds_write_b16_d16_hi v0, v6 offset:376
	v_bfe_u32 v6, v57, 16, 1
	v_add3_u32 v6, v57, v6, s2
	ds_write_b16_d16_hi v0, v6 offset:512
	v_bfe_u32 v6, v66, 16, 1
	v_add3_u32 v6, v66, v6, s2
	ds_write_b16_d16_hi v0, v6 offset:112
	v_bfe_u32 v6, v67, 16, 1
	v_add3_u32 v6, v67, v6, s2
	ds_write_b16_d16_hi v0, v6 offset:248
	v_bfe_u32 v6, v68, 16, 1
	v_add3_u32 v6, v68, v6, s2
	ds_write_b16_d16_hi v0, v6 offset:384
	v_bfe_u32 v6, v69, 16, 1
	v_add3_u32 v6, v69, v6, s2
	ds_write_b16_d16_hi v0, v6 offset:520
	v_bfe_u32 v6, v62, 16, 1
	v_add3_u32 v6, v62, v6, s2
	ds_write_b16_d16_hi v0, v6 offset:120
	v_bfe_u32 v6, v63, 16, 1
	v_add3_u32 v6, v63, v6, s2
	ds_write_b16_d16_hi v0, v6 offset:256
	v_bfe_u32 v6, v64, 16, 1
	v_add3_u32 v6, v64, v6, s2
	ds_write_b16_d16_hi v0, v6 offset:392
	v_bfe_u32 v6, v65, 16, 1
	v_add3_u32 v6, v65, v6, s2
	ds_write_b16_d16_hi v0, v6 offset:528
	s_waitcnt lgkmcnt(0)
	v_add_u32_e32 v6, s8, v70
	s_movk_i32 s2, 0x400
	v_cmp_gt_i32_e32 vcc, s2, v6
	s_and_saveexec_b64 s[2:3], vcc
	s_cbranch_execz .LBB0_102
	v_bfe_u32 v8, v6, 6, 2
	v_bfe_u32 v9, v6, 5, 1
	v_and_b32_e32 v6, 0xffffff1f, v6
	v_lshl_or_b32 v6, v8, 5, v6
	v_lshl_or_b32 v6, v9, 7, v6
	v_ashrrev_i32_e32 v7, 31, v6
	v_lshlrev_b64 v[6:7], 11, v[6:7]
	v_lshl_add_u64 v[18:19], s[0:1], 0, v[6:7]
	ds_read2_b64 v[6:9], v80 offset1:1
	ds_read2_b64 v[10:13], v80 offset0:2 offset1:3
	ds_read2_b64 v[14:17], v80 offset0:4 offset1:5
	s_ashr_i32 s5, s4, 31
	v_lshl_add_u64 v[26:27], s[4:5], 1, v[18:19]
	s_waitcnt lgkmcnt(2)
	global_store_dwordx4 v[26:27], v[6:9], off
	s_waitcnt lgkmcnt(1)
	global_store_dwordx4 v[26:27], v[10:13], off offset:16
	s_waitcnt lgkmcnt(0)
	global_store_dwordx4 v[26:27], v[14:17], off offset:32
	ds_read2_b64 v[6:9], v80 offset0:6 offset1:7
	ds_read2_b64 v[10:13], v80 offset0:8 offset1:9
	ds_read2_b64 v[14:17], v80 offset0:10 offset1:11
	ds_read2_b64 v[18:21], v80 offset0:12 offset1:13
	ds_read2_b64 v[22:25], v80 offset0:14 offset1:15
	s_waitcnt lgkmcnt(4)
	global_store_dwordx4 v[26:27], v[6:9], off offset:48
	s_waitcnt lgkmcnt(3)
	global_store_dwordx4 v[26:27], v[10:13], off offset:64
	s_waitcnt lgkmcnt(2)
	global_store_dwordx4 v[26:27], v[14:17], off offset:80
	s_waitcnt lgkmcnt(1)
	global_store_dwordx4 v[26:27], v[18:21], off offset:96
	s_waitcnt lgkmcnt(0)
	global_store_dwordx4 v[26:27], v[22:25], off offset:112
	s_branch .LBB0_102

.LBB0_450:
	s_or_b64 exec, exec, s[12:13]
	s_waitcnt vmcnt(0)
	v_bfe_u32 v74, v10, 16, 1
	s_movk_i32 s4, 0x7fff
	v_add3_u32 v10, v10, v74, s4
	ds_write_b16_d16_hi v0, v10
	v_bfe_u32 v10, v11, 16, 1
	v_add3_u32 v10, v11, v10, s4
	ds_write_b16_d16_hi v0, v10 offset:136
	v_bfe_u32 v10, v12, 16, 1
	v_add3_u32 v10, v12, v10, s4
	ds_write_b16_d16_hi v0, v10 offset:272
	v_bfe_u32 v10, v13, 16, 1
	v_add3_u32 v10, v13, v10, s4
	ds_write_b16_d16_hi v0, v10 offset:408
	v_bfe_u32 v10, v6, 16, 1
	v_add3_u32 v6, v6, v10, s4
	ds_write_b16_d16_hi v0, v6 offset:8
	v_bfe_u32 v6, v7, 16, 1
	v_add3_u32 v6, v7, v6, s4
	ds_write_b16_d16_hi v0, v6 offset:144
	v_bfe_u32 v6, v8, 16, 1
	v_add3_u32 v6, v8, v6, s4
	ds_write_b16_d16_hi v0, v6 offset:280
	v_bfe_u32 v6, v9, 16, 1
	v_add3_u32 v6, v9, v6, s4
	ds_write_b16_d16_hi v0, v6 offset:416
	v_bfe_u32 v6, v18, 16, 1
	v_add3_u32 v6, v18, v6, s4
	ds_write_b16_d16_hi v0, v6 offset:16
	v_bfe_u32 v6, v19, 16, 1
	v_add3_u32 v6, v19, v6, s4
	ds_write_b16_d16_hi v0, v6 offset:152
	v_bfe_u32 v6, v20, 16, 1
	v_add3_u32 v6, v20, v6, s4
	ds_write_b16_d16_hi v0, v6 offset:288
	v_bfe_u32 v6, v21, 16, 1
	v_add3_u32 v6, v21, v6, s4
	ds_write_b16_d16_hi v0, v6 offset:424
	v_bfe_u32 v6, v14, 16, 1
	v_add3_u32 v6, v14, v6, s4
	ds_write_b16_d16_hi v0, v6 offset:24
	v_bfe_u32 v6, v15, 16, 1
	v_add3_u32 v6, v15, v6, s4
	ds_write_b16_d16_hi v0, v6 offset:160
	v_bfe_u32 v6, v16, 16, 1
	v_add3_u32 v6, v16, v6, s4
	ds_write_b16_d16_hi v0, v6 offset:296
	v_bfe_u32 v6, v17, 16, 1
	v_add3_u32 v6, v17, v6, s4
	ds_write_b16_d16_hi v0, v6 offset:432
	v_bfe_u32 v6, v26, 16, 1
	v_add3_u32 v6, v26, v6, s4
	ds_write_b16_d16_hi v0, v6 offset:32
	v_bfe_u32 v6, v27, 16, 1
	v_add3_u32 v6, v27, v6, s4
	ds_write_b16_d16_hi v0, v6 offset:168
	v_bfe_u32 v6, v28, 16, 1
	v_add3_u32 v6, v28, v6, s4
	ds_write_b16_d16_hi v0, v6 offset:304
	v_bfe_u32 v6, v29, 16, 1
	v_add3_u32 v6, v29, v6, s4
	ds_write_b16_d16_hi v0, v6 offset:440
	v_bfe_u32 v6, v22, 16, 1
	v_add3_u32 v6, v22, v6, s4
	ds_write_b16_d16_hi v0, v6 offset:40
	v_bfe_u32 v6, v23, 16, 1
	v_add3_u32 v6, v23, v6, s4
	ds_write_b16_d16_hi v0, v6 offset:176
	v_bfe_u32 v6, v24, 16, 1
	v_add3_u32 v6, v24, v6, s4
	ds_write_b16_d16_hi v0, v6 offset:312
	v_bfe_u32 v6, v25, 16, 1
	v_add3_u32 v6, v25, v6, s4
	ds_write_b16_d16_hi v0, v6 offset:448
	v_bfe_u32 v6, v34, 16, 1
	v_add3_u32 v6, v34, v6, s4
	ds_write_b16_d16_hi v0, v6 offset:48
	v_bfe_u32 v6, v35, 16, 1
	v_add3_u32 v6, v35, v6, s4
	ds_write_b16_d16_hi v0, v6 offset:184
	v_bfe_u32 v6, v36, 16, 1
	v_add3_u32 v6, v36, v6, s4
	ds_write_b16_d16_hi v0, v6 offset:320
	v_bfe_u32 v6, v37, 16, 1
	v_add3_u32 v6, v37, v6, s4
	ds_write_b16_d16_hi v0, v6 offset:456
	v_bfe_u32 v6, v30, 16, 1
	v_add3_u32 v6, v30, v6, s4
	ds_write_b16_d16_hi v0, v6 offset:56
	v_bfe_u32 v6, v31, 16, 1
	v_add3_u32 v6, v31, v6, s4
	ds_write_b16_d16_hi v0, v6 offset:192
	v_bfe_u32 v6, v32, 16, 1
	v_add3_u32 v6, v32, v6, s4
	ds_write_b16_d16_hi v0, v6 offset:328
	v_bfe_u32 v6, v33, 16, 1
	v_add3_u32 v6, v33, v6, s4
	ds_write_b16_d16_hi v0, v6 offset:464
	v_bfe_u32 v6, v42, 16, 1
	v_add3_u32 v6, v42, v6, s4
	ds_write_b16_d16_hi v0, v6 offset:64
	v_bfe_u32 v6, v43, 16, 1
	v_add3_u32 v6, v43, v6, s4
	ds_write_b16_d16_hi v0, v6 offset:200
	v_bfe_u32 v6, v44, 16, 1
	v_add3_u32 v6, v44, v6, s4
	ds_write_b16_d16_hi v0, v6 offset:336
	v_bfe_u32 v6, v45, 16, 1
	v_add3_u32 v6, v45, v6, s4
	ds_write_b16_d16_hi v0, v6 offset:472
	v_bfe_u32 v6, v38, 16, 1
	v_add3_u32 v6, v38, v6, s4
	ds_write_b16_d16_hi v0, v6 offset:72
	v_bfe_u32 v6, v39, 16, 1
	v_add3_u32 v6, v39, v6, s4
	ds_write_b16_d16_hi v0, v6 offset:208
	v_bfe_u32 v6, v40, 16, 1
	v_add3_u32 v6, v40, v6, s4
	ds_write_b16_d16_hi v0, v6 offset:344
	v_bfe_u32 v6, v41, 16, 1
	v_add3_u32 v6, v41, v6, s4
	ds_write_b16_d16_hi v0, v6 offset:480
	v_bfe_u32 v6, v50, 16, 1
	v_add3_u32 v6, v50, v6, s4
	ds_write_b16_d16_hi v0, v6 offset:80
	v_bfe_u32 v6, v51, 16, 1
	v_add3_u32 v6, v51, v6, s4
	ds_write_b16_d16_hi v0, v6 offset:216
	v_bfe_u32 v6, v52, 16, 1
	v_add3_u32 v6, v52, v6, s4
	ds_write_b16_d16_hi v0, v6 offset:352
	v_bfe_u32 v6, v53, 16, 1
	v_add3_u32 v6, v53, v6, s4
	ds_write_b16_d16_hi v0, v6 offset:488
	v_bfe_u32 v6, v46, 16, 1
	v_add3_u32 v6, v46, v6, s4
	ds_write_b16_d16_hi v0, v6 offset:88
	v_bfe_u32 v6, v47, 16, 1
	v_add3_u32 v6, v47, v6, s4
	ds_write_b16_d16_hi v0, v6 offset:224
	v_bfe_u32 v6, v48, 16, 1
	v_add3_u32 v6, v48, v6, s4
	ds_write_b16_d16_hi v0, v6 offset:360
	v_bfe_u32 v6, v49, 16, 1
	v_add3_u32 v6, v49, v6, s4
	ds_write_b16_d16_hi v0, v6 offset:496
	v_bfe_u32 v6, v58, 16, 1
	v_add3_u32 v6, v58, v6, s4
	ds_write_b16_d16_hi v0, v6 offset:96
	v_bfe_u32 v6, v59, 16, 1
	v_add3_u32 v6, v59, v6, s4
	ds_write_b16_d16_hi v0, v6 offset:232
	v_bfe_u32 v6, v60, 16, 1
	v_add3_u32 v6, v60, v6, s4
	ds_write_b16_d16_hi v0, v6 offset:368
	v_bfe_u32 v6, v61, 16, 1
	v_add3_u32 v6, v61, v6, s4
	ds_write_b16_d16_hi v0, v6 offset:504
	v_bfe_u32 v6, v54, 16, 1
	v_add3_u32 v6, v54, v6, s4
	ds_write_b16_d16_hi v0, v6 offset:104
	v_bfe_u32 v6, v55, 16, 1
	v_add3_u32 v6, v55, v6, s4
	ds_write_b16_d16_hi v0, v6 offset:240
	v_bfe_u32 v6, v56, 16, 1
	v_add3_u32 v6, v56, v6, s4
	ds_write_b16_d16_hi v0, v6 offset:376
	v_bfe_u32 v6, v57, 16, 1
	v_add3_u32 v6, v57, v6, s4
	ds_write_b16_d16_hi v0, v6 offset:512
	v_bfe_u32 v6, v66, 16, 1
	v_add3_u32 v6, v66, v6, s4
	ds_write_b16_d16_hi v0, v6 offset:112
	v_bfe_u32 v6, v67, 16, 1
	v_add3_u32 v6, v67, v6, s4
	ds_write_b16_d16_hi v0, v6 offset:248
	v_bfe_u32 v6, v68, 16, 1
	v_add3_u32 v6, v68, v6, s4
	ds_write_b16_d16_hi v0, v6 offset:384
	v_bfe_u32 v6, v69, 16, 1
	v_add3_u32 v6, v69, v6, s4
	ds_write_b16_d16_hi v0, v6 offset:520
	v_bfe_u32 v6, v62, 16, 1
	v_add3_u32 v6, v62, v6, s4
	ds_write_b16_d16_hi v0, v6 offset:120
	v_bfe_u32 v6, v63, 16, 1
	v_add3_u32 v6, v63, v6, s4
	ds_write_b16_d16_hi v0, v6 offset:256
	v_bfe_u32 v6, v64, 16, 1
	v_add3_u32 v6, v64, v6, s4
	ds_write_b16_d16_hi v0, v6 offset:392
	v_bfe_u32 v6, v65, 16, 1
	v_add3_u32 v6, v65, v6, s4
	ds_write_b16_d16_hi v0, v6 offset:528
	s_waitcnt lgkmcnt(0)
	v_add_u32_e32 v6, s10, v70
	s_movk_i32 s4, 0x400
	v_cmp_gt_i32_e32 vcc, s4, v6
	s_and_saveexec_b64 s[4:5], vcc
	s_cbranch_execz .LBB0_417
	v_bfe_u32 v10, v6, 6, 2
	v_bfe_u32 v11, v6, 5, 1
	v_and_b32_e32 v6, 0xffffff1f, v6
	v_lshl_or_b32 v6, v10, 5, v6
	v_lshl_or_b32 v6, v11, 7, v6
	v_mov_b64_e32 v[8:9], s[0:1]
	s_movk_i32 s9, 0x1600
	v_mad_i64_i32 v[18:19], s[10:11], v6, s9, v[8:9]
	ds_read2_b64 v[6:9], v80 offset1:1
	ds_read2_b64 v[10:13], v80 offset0:2 offset1:3
	ds_read2_b64 v[14:17], v80 offset0:4 offset1:5
	s_ashr_i32 s9, s8, 31
	v_lshl_add_u64 v[26:27], s[8:9], 1, v[18:19]
	s_waitcnt lgkmcnt(2)
	global_store_dwordx4 v[26:27], v[6:9], off
	s_waitcnt lgkmcnt(1)
	global_store_dwordx4 v[26:27], v[10:13], off offset:16
	s_waitcnt lgkmcnt(0)
	global_store_dwordx4 v[26:27], v[14:17], off offset:32
	ds_read2_b64 v[6:9], v80 offset0:6 offset1:7
	ds_read2_b64 v[10:13], v80 offset0:8 offset1:9
	ds_read2_b64 v[14:17], v80 offset0:10 offset1:11
	ds_read2_b64 v[18:21], v80 offset0:12 offset1:13
	ds_read2_b64 v[22:25], v80 offset0:14 offset1:15
	s_waitcnt lgkmcnt(4)
	global_store_dwordx4 v[26:27], v[6:9], off offset:48
	s_waitcnt lgkmcnt(3)
	global_store_dwordx4 v[26:27], v[10:13], off offset:64
	s_waitcnt lgkmcnt(2)
	global_store_dwordx4 v[26:27], v[14:17], off offset:80
	s_waitcnt lgkmcnt(1)
	global_store_dwordx4 v[26:27], v[18:21], off offset:96
	s_waitcnt lgkmcnt(0)
	global_store_dwordx4 v[26:27], v[22:25], off offset:112
	s_branch .LBB0_417

.LBB0_576:
	v_lshl_add_u32 v172, s70, 8, v154
	v_ashrrev_i32_e32 v173, 31, v172
	v_lshl_add_u64 v[180:181], v[172:173], 2, s[14:15]
	global_load_dword v136, v[180:181], off
	global_load_dword v137, v[180:181], off offset:64
	global_load_dword v138, v[180:181], off offset:128
	global_load_dword v139, v[180:181], off offset:192
	global_load_dword v140, v[180:181], off offset:512
	global_load_dword v141, v[180:181], off offset:576
	global_load_dword v142, v[180:181], off offset:640
	global_load_dword v143, v[180:181], off offset:704
	s_and_b64 vcc, exec, s[18:19]
	s_cbranch_vccz .Lpj_nobar
	s_barrier
.Lpj_nobar:
	s_lshl_b32 s30, s69, 8
	s_cmp_gt_i32 s69, 7
	s_cbranch_scc1 .Lpj_gt
	s_mov_b32 s24, 0x13a00000
	s_mov_b32 s22, 0x1000
	s_cmp_lt_i32 s69, 2
	s_cselect_b32 s23, 1, 0
	s_cmp_eq_u32 s69, 7
	s_cselect_b32 s26, 2, s23
	s_branch .Lpj_cm
.Lpj_gt:
	s_add_i32 s30, s30, 0xfffff800
	s_mov_b32 s24, 0x1ba00000
	s_mov_b32 s22, 0x1800
	s_mov_b32 s23, 2
	s_mov_b32 s26, 2
.Lpj_cm:
	s_mov_b32 s25, 0
	s_add_u32 s24, s34, s24
	s_addc_u32 s25, s35, s25
	v_readfirstlane_b32 s28, v156
	s_nop 3
	s_bfe_u32 s28, s28, 0x20005
	s_cmp_ge_u32 s28, 2
	s_cselect_b32 s23, s26, s23
	v_and_b32_e32 v172, -9, v154
	v_lshl_add_u32 v172, s70, 8, v172
	v_lshrrev_b32_e32 v174, 5, v156
	v_lshlrev_b32_e32 v174, 6, v174
	v_and_b32_e32 v144, 24, v156
	v_add_u32_e32 v174, v174, v144
	v_and_b32_e32 v144, 8, v154
	v_lshl_add_u32 v174, v144, 2, v174
	v_add_u32_e32 v174, s30, v174
	v_lshlrev_b32_e32 v174, 1, v174
	v_mov_b32_e32 v175, 0
	v_lshl_add_u64 v[176:177], s[24:25], 0, v[174:175]
	v_mad_u64_u32 v[178:179], vcc, v172, s22, v[176:177]
	v_mov_b32_e32 v184, 1.0
	v_mov_b32_e32 v185, 1.0
	v_mov_b32_e32 v186, 0xbfb8aa3b
	v_mov_b32_e32 v187, 0xbfb8aa3b
	v_mov_b32_e32 v188, 0x3d372713
	v_mov_b32_e32 v189, 0x3d372713
	v_mov_b32_e32 v190, 0x3fcc422a
	v_mov_b32_e32 v191, 0x3fcc422a
	s_mov_b32 s29, 0
	s_waitcnt vmcnt(0)
	s_cmp_eq_u32 s23, 1
	s_cbranch_scc1 .Lpj_gelu
	s_cmp_eq_u32 s23, 2
	s_cbranch_scc1 .Lpj_sigm
	v_pk_mul_f32 v[126:127], v[126:127], v[136:137] op_sel_hi:[1,0]
	v_pk_mul_f32 v[128:129], v[128:129], v[136:137] op_sel_hi:[1,0]
	v_pk_mul_f32 v[122:123], v[122:123], v[136:137] op_sel_hi:[1,0]
	v_pk_mul_f32 v[124:125], v[124:125], v[136:137] op_sel_hi:[1,0]
	v_cvt_pk_bf16_f32 v126, v126, v127
	v_cvt_pk_bf16_f32 v127, v128, v129
	v_cvt_pk_bf16_f32 v128, v122, v123
	v_cvt_pk_bf16_f32 v129, v124, v125
	v_pk_mul_f32 v[118:119], v[118:119], v[136:137] op_sel_hi:[1,0]
	v_pk_mul_f32 v[120:121], v[120:121], v[136:137] op_sel_hi:[1,0]
	v_pk_mul_f32 v[114:115], v[114:115], v[136:137] op_sel_hi:[1,0]
	v_pk_mul_f32 v[116:117], v[116:117], v[136:137] op_sel_hi:[1,0]
	v_cvt_pk_bf16_f32 v118, v118, v119
	v_cvt_pk_bf16_f32 v119, v120, v121
	v_cvt_pk_bf16_f32 v120, v114, v115
	v_cvt_pk_bf16_f32 v121, v116, v117
	v_mov_b32_e32 v158, v118
	v_mov_b32_e32 v159, v119
	v_mov_b32_e32 v160, v120
	v_mov_b32_e32 v161, v121
	v_mov_b32_dpp v118, v126 row_shl:8 row_mask:0xf bank_mask:0x3
	v_mov_b32_dpp v119, v127 row_shl:8 row_mask:0xf bank_mask:0x3
	v_mov_b32_dpp v120, v128 row_shl:8 row_mask:0xf bank_mask:0x3
	v_mov_b32_dpp v121, v129 row_shl:8 row_mask:0xf bank_mask:0x3
	v_mov_b32_dpp v126, v158 row_shr:8 row_mask:0xf bank_mask:0xc
	v_mov_b32_dpp v127, v159 row_shr:8 row_mask:0xf bank_mask:0xc
	v_mov_b32_dpp v128, v160 row_shr:8 row_mask:0xf bank_mask:0xc
	v_mov_b32_dpp v129, v161 row_shr:8 row_mask:0xf bank_mask:0xc
	s_mul_i32 s28, s22, 0
	v_lshl_add_u64 v[180:181], s[28:29], 0, v[178:179]
	global_store_dwordx4 v[180:181], v[126:129], off
	s_mul_i32 s28, s22, 8
	v_lshl_add_u64 v[180:181], s[28:29], 0, v[178:179]
	global_store_dwordx4 v[180:181], v[118:121], off
	v_pk_mul_f32 v[110:111], v[110:111], v[136:137] op_sel:[0,1] op_sel_hi:[1,1]
	v_pk_mul_f32 v[112:113], v[112:113], v[136:137] op_sel:[0,1] op_sel_hi:[1,1]
	v_pk_mul_f32 v[106:107], v[106:107], v[136:137] op_sel:[0,1] op_sel_hi:[1,1]
	v_pk_mul_f32 v[108:109], v[108:109], v[136:137] op_sel:[0,1] op_sel_hi:[1,1]
	v_cvt_pk_bf16_f32 v110, v110, v111
	v_cvt_pk_bf16_f32 v111, v112, v113
	v_cvt_pk_bf16_f32 v112, v106, v107
	v_cvt_pk_bf16_f32 v113, v108, v109
	v_pk_mul_f32 v[102:103], v[102:103], v[136:137] op_sel:[0,1] op_sel_hi:[1,1]
	v_pk_mul_f32 v[104:105], v[104:105], v[136:137] op_sel:[0,1] op_sel_hi:[1,1]
	v_pk_mul_f32 v[98:99], v[98:99], v[136:137] op_sel:[0,1] op_sel_hi:[1,1]
	v_pk_mul_f32 v[100:101], v[100:101], v[136:137] op_sel:[0,1] op_sel_hi:[1,1]
	v_cvt_pk_bf16_f32 v102, v102, v103
	v_cvt_pk_bf16_f32 v103, v104, v105
	v_cvt_pk_bf16_f32 v104, v98, v99
	v_cvt_pk_bf16_f32 v105, v100, v101
	v_mov_b32_e32 v158, v102
	v_mov_b32_e32 v159, v103
	v_mov_b32_e32 v160, v104
	v_mov_b32_e32 v161, v105
	v_mov_b32_dpp v102, v110 row_shl:8 row_mask:0xf bank_mask:0x3
	v_mov_b32_dpp v103, v111 row_shl:8 row_mask:0xf bank_mask:0x3
	v_mov_b32_dpp v104, v112 row_shl:8 row_mask:0xf bank_mask:0x3
	v_mov_b32_dpp v105, v113 row_shl:8 row_mask:0xf bank_mask:0x3
	v_mov_b32_dpp v110, v158 row_shr:8 row_mask:0xf bank_mask:0xc
	v_mov_b32_dpp v111, v159 row_shr:8 row_mask:0xf bank_mask:0xc
	v_mov_b32_dpp v112, v160 row_shr:8 row_mask:0xf bank_mask:0xc
	v_mov_b32_dpp v113, v161 row_shr:8 row_mask:0xf bank_mask:0xc
	s_mul_i32 s28, s22, 16
	v_lshl_add_u64 v[180:181], s[28:29], 0, v[178:179]
	global_store_dwordx4 v[180:181], v[110:113], off
	s_mul_i32 s28, s22, 24
	v_lshl_add_u64 v[180:181], s[28:29], 0, v[178:179]
	global_store_dwordx4 v[180:181], v[102:105], off
	v_pk_mul_f32 v[94:95], v[94:95], v[138:139] op_sel_hi:[1,0]
	v_pk_mul_f32 v[96:97], v[96:97], v[138:139] op_sel_hi:[1,0]
	v_pk_mul_f32 v[90:91], v[90:91], v[138:139] op_sel_hi:[1,0]
	v_pk_mul_f32 v[92:93], v[92:93], v[138:139] op_sel_hi:[1,0]
	v_cvt_pk_bf16_f32 v94, v94, v95
	v_cvt_pk_bf16_f32 v95, v96, v97
	v_cvt_pk_bf16_f32 v96, v90, v91
	v_cvt_pk_bf16_f32 v97, v92, v93
	v_pk_mul_f32 v[86:87], v[86:87], v[138:139] op_sel_hi:[1,0]
	v_pk_mul_f32 v[88:89], v[88:89], v[138:139] op_sel_hi:[1,0]
	v_pk_mul_f32 v[82:83], v[82:83], v[138:139] op_sel_hi:[1,0]
	v_pk_mul_f32 v[84:85], v[84:85], v[138:139] op_sel_hi:[1,0]
	v_cvt_pk_bf16_f32 v86, v86, v87
	v_cvt_pk_bf16_f32 v87, v88, v89
	v_cvt_pk_bf16_f32 v88, v82, v83
	v_cvt_pk_bf16_f32 v89, v84, v85
	v_mov_b32_e32 v158, v86
	v_mov_b32_e32 v159, v87
	v_mov_b32_e32 v160, v88
	v_mov_b32_e32 v161, v89
	v_mov_b32_dpp v86, v94 row_shl:8 row_mask:0xf bank_mask:0x3
	v_mov_b32_dpp v87, v95 row_shl:8 row_mask:0xf bank_mask:0x3
	v_mov_b32_dpp v88, v96 row_shl:8 row_mask:0xf bank_mask:0x3
	v_mov_b32_dpp v89, v97 row_shl:8 row_mask:0xf bank_mask:0x3
	v_mov_b32_dpp v94, v158 row_shr:8 row_mask:0xf bank_mask:0xc
	v_mov_b32_dpp v95, v159 row_shr:8 row_mask:0xf bank_mask:0xc
	v_mov_b32_dpp v96, v160 row_shr:8 row_mask:0xf bank_mask:0xc
	v_mov_b32_dpp v97, v161 row_shr:8 row_mask:0xf bank_mask:0xc
	s_mul_i32 s28, s22, 32
	v_lshl_add_u64 v[180:181], s[28:29], 0, v[178:179]
	global_store_dwordx4 v[180:181], v[94:97], off
	s_mul_i32 s28, s22, 40
	v_lshl_add_u64 v[180:181], s[28:29], 0, v[178:179]
	global_store_dwordx4 v[180:181], v[86:89], off
	v_pk_mul_f32 v[78:79], v[78:79], v[138:139] op_sel:[0,1] op_sel_hi:[1,1]
	v_pk_mul_f32 v[80:81], v[80:81], v[138:139] op_sel:[0,1] op_sel_hi:[1,1]
	v_pk_mul_f32 v[74:75], v[74:75], v[138:139] op_sel:[0,1] op_sel_hi:[1,1]
	v_pk_mul_f32 v[76:77], v[76:77], v[138:139] op_sel:[0,1] op_sel_hi:[1,1]
	v_cvt_pk_bf16_f32 v78, v78, v79
	v_cvt_pk_bf16_f32 v79, v80, v81
	v_cvt_pk_bf16_f32 v80, v74, v75
	v_cvt_pk_bf16_f32 v81, v76, v77
	v_pk_mul_f32 v[70:71], v[70:71], v[138:139] op_sel:[0,1] op_sel_hi:[1,1]
	v_pk_mul_f32 v[72:73], v[72:73], v[138:139] op_sel:[0,1] op_sel_hi:[1,1]
	v_pk_mul_f32 v[66:67], v[66:67], v[138:139] op_sel:[0,1] op_sel_hi:[1,1]
	v_pk_mul_f32 v[68:69], v[68:69], v[138:139] op_sel:[0,1] op_sel_hi:[1,1]
	v_cvt_pk_bf16_f32 v70, v70, v71
	v_cvt_pk_bf16_f32 v71, v72, v73
	v_cvt_pk_bf16_f32 v72, v66, v67
	v_cvt_pk_bf16_f32 v73, v68, v69
	v_mov_b32_e32 v158, v70
	v_mov_b32_e32 v159, v71
	v_mov_b32_e32 v160, v72
	v_mov_b32_e32 v161, v73
	v_mov_b32_dpp v70, v78 row_shl:8 row_mask:0xf bank_mask:0x3
	v_mov_b32_dpp v71, v79 row_shl:8 row_mask:0xf bank_mask:0x3
	v_mov_b32_dpp v72, v80 row_shl:8 row_mask:0xf bank_mask:0x3
	v_mov_b32_dpp v73, v81 row_shl:8 row_mask:0xf bank_mask:0x3
	v_mov_b32_dpp v78, v158 row_shr:8 row_mask:0xf bank_mask:0xc
	v_mov_b32_dpp v79, v159 row_shr:8 row_mask:0xf bank_mask:0xc
	v_mov_b32_dpp v80, v160 row_shr:8 row_mask:0xf bank_mask:0xc
	v_mov_b32_dpp v81, v161 row_shr:8 row_mask:0xf bank_mask:0xc
	s_mul_i32 s28, s22, 48
	v_lshl_add_u64 v[180:181], s[28:29], 0, v[178:179]
	global_store_dwordx4 v[180:181], v[78:81], off
	s_mul_i32 s28, s22, 56
	v_lshl_add_u64 v[180:181], s[28:29], 0, v[178:179]
	global_store_dwordx4 v[180:181], v[70:73], off
	v_pk_mul_f32 v[62:63], v[62:63], v[140:141] op_sel_hi:[1,0]
	v_pk_mul_f32 v[64:65], v[64:65], v[140:141] op_sel_hi:[1,0]
	v_pk_mul_f32 v[58:59], v[58:59], v[140:141] op_sel_hi:[1,0]
	v_pk_mul_f32 v[60:61], v[60:61], v[140:141] op_sel_hi:[1,0]
	v_cvt_pk_bf16_f32 v62, v62, v63
	v_cvt_pk_bf16_f32 v63, v64, v65
	v_cvt_pk_bf16_f32 v64, v58, v59
	v_cvt_pk_bf16_f32 v65, v60, v61
	v_pk_mul_f32 v[54:55], v[54:55], v[140:141] op_sel_hi:[1,0]
	v_pk_mul_f32 v[56:57], v[56:57], v[140:141] op_sel_hi:[1,0]
	v_pk_mul_f32 v[50:51], v[50:51], v[140:141] op_sel_hi:[1,0]
	v_pk_mul_f32 v[52:53], v[52:53], v[140:141] op_sel_hi:[1,0]
	v_cvt_pk_bf16_f32 v54, v54, v55
	v_cvt_pk_bf16_f32 v55, v56, v57
	v_cvt_pk_bf16_f32 v56, v50, v51
	v_cvt_pk_bf16_f32 v57, v52, v53
	v_mov_b32_e32 v158, v54
	v_mov_b32_e32 v159, v55
	v_mov_b32_e32 v160, v56
	v_mov_b32_e32 v161, v57
	v_mov_b32_dpp v54, v62 row_shl:8 row_mask:0xf bank_mask:0x3
	v_mov_b32_dpp v55, v63 row_shl:8 row_mask:0xf bank_mask:0x3
	v_mov_b32_dpp v56, v64 row_shl:8 row_mask:0xf bank_mask:0x3
	v_mov_b32_dpp v57, v65 row_shl:8 row_mask:0xf bank_mask:0x3
	v_mov_b32_dpp v62, v158 row_shr:8 row_mask:0xf bank_mask:0xc
	v_mov_b32_dpp v63, v159 row_shr:8 row_mask:0xf bank_mask:0xc
	v_mov_b32_dpp v64, v160 row_shr:8 row_mask:0xf bank_mask:0xc
	v_mov_b32_dpp v65, v161 row_shr:8 row_mask:0xf bank_mask:0xc
	s_mul_i32 s28, s22, 128
	v_lshl_add_u64 v[180:181], s[28:29], 0, v[178:179]
	global_store_dwordx4 v[180:181], v[62:65], off
	s_mul_i32 s28, s22, 136
	v_lshl_add_u64 v[180:181], s[28:29], 0, v[178:179]
	global_store_dwordx4 v[180:181], v[54:57], off
	v_pk_mul_f32 v[46:47], v[46:47], v[140:141] op_sel:[0,1] op_sel_hi:[1,1]
	v_pk_mul_f32 v[48:49], v[48:49], v[140:141] op_sel:[0,1] op_sel_hi:[1,1]
	v_pk_mul_f32 v[42:43], v[42:43], v[140:141] op_sel:[0,1] op_sel_hi:[1,1]
	v_pk_mul_f32 v[44:45], v[44:45], v[140:141] op_sel:[0,1] op_sel_hi:[1,1]
	v_cvt_pk_bf16_f32 v46, v46, v47
	v_cvt_pk_bf16_f32 v47, v48, v49
	v_cvt_pk_bf16_f32 v48, v42, v43
	v_cvt_pk_bf16_f32 v49, v44, v45
	v_pk_mul_f32 v[38:39], v[38:39], v[140:141] op_sel:[0,1] op_sel_hi:[1,1]
	v_pk_mul_f32 v[40:41], v[40:41], v[140:141] op_sel:[0,1] op_sel_hi:[1,1]
	v_pk_mul_f32 v[34:35], v[34:35], v[140:141] op_sel:[0,1] op_sel_hi:[1,1]
	v_pk_mul_f32 v[36:37], v[36:37], v[140:141] op_sel:[0,1] op_sel_hi:[1,1]
	v_cvt_pk_bf16_f32 v38, v38, v39
	v_cvt_pk_bf16_f32 v39, v40, v41
	v_cvt_pk_bf16_f32 v40, v34, v35
	v_cvt_pk_bf16_f32 v41, v36, v37
	v_mov_b32_e32 v158, v38
	v_mov_b32_e32 v159, v39
	v_mov_b32_e32 v160, v40
	v_mov_b32_e32 v161, v41
	v_mov_b32_dpp v38, v46 row_shl:8 row_mask:0xf bank_mask:0x3
	v_mov_b32_dpp v39, v47 row_shl:8 row_mask:0xf bank_mask:0x3
	v_mov_b32_dpp v40, v48 row_shl:8 row_mask:0xf bank_mask:0x3
	v_mov_b32_dpp v41, v49 row_shl:8 row_mask:0xf bank_mask:0x3
	v_mov_b32_dpp v46, v158 row_shr:8 row_mask:0xf bank_mask:0xc
	v_mov_b32_dpp v47, v159 row_shr:8 row_mask:0xf bank_mask:0xc
	v_mov_b32_dpp v48, v160 row_shr:8 row_mask:0xf bank_mask:0xc
	v_mov_b32_dpp v49, v161 row_shr:8 row_mask:0xf bank_mask:0xc
	s_mul_i32 s28, s22, 144
	v_lshl_add_u64 v[180:181], s[28:29], 0, v[178:179]
	global_store_dwordx4 v[180:181], v[46:49], off
	s_mul_i32 s28, s22, 152
	v_lshl_add_u64 v[180:181], s[28:29], 0, v[178:179]
	global_store_dwordx4 v[180:181], v[38:41], off
	v_pk_mul_f32 v[30:31], v[30:31], v[142:143] op_sel_hi:[1,0]
	v_pk_mul_f32 v[32:33], v[32:33], v[142:143] op_sel_hi:[1,0]
	v_pk_mul_f32 v[26:27], v[26:27], v[142:143] op_sel_hi:[1,0]
	v_pk_mul_f32 v[28:29], v[28:29], v[142:143] op_sel_hi:[1,0]
	v_cvt_pk_bf16_f32 v30, v30, v31
	v_cvt_pk_bf16_f32 v31, v32, v33
	v_cvt_pk_bf16_f32 v32, v26, v27
	v_cvt_pk_bf16_f32 v33, v28, v29
	v_pk_mul_f32 v[22:23], v[22:23], v[142:143] op_sel_hi:[1,0]
	v_pk_mul_f32 v[24:25], v[24:25], v[142:143] op_sel_hi:[1,0]
	v_pk_mul_f32 v[18:19], v[18:19], v[142:143] op_sel_hi:[1,0]
	v_pk_mul_f32 v[20:21], v[20:21], v[142:143] op_sel_hi:[1,0]
	v_cvt_pk_bf16_f32 v22, v22, v23
	v_cvt_pk_bf16_f32 v23, v24, v25
	v_cvt_pk_bf16_f32 v24, v18, v19
	v_cvt_pk_bf16_f32 v25, v20, v21
	v_mov_b32_e32 v158, v22
	v_mov_b32_e32 v159, v23
	v_mov_b32_e32 v160, v24
	v_mov_b32_e32 v161, v25
	v_mov_b32_dpp v22, v30 row_shl:8 row_mask:0xf bank_mask:0x3
	v_mov_b32_dpp v23, v31 row_shl:8 row_mask:0xf bank_mask:0x3
	v_mov_b32_dpp v24, v32 row_shl:8 row_mask:0xf bank_mask:0x3
	v_mov_b32_dpp v25, v33 row_shl:8 row_mask:0xf bank_mask:0x3
	v_mov_b32_dpp v30, v158 row_shr:8 row_mask:0xf bank_mask:0xc
	v_mov_b32_dpp v31, v159 row_shr:8 row_mask:0xf bank_mask:0xc
	v_mov_b32_dpp v32, v160 row_shr:8 row_mask:0xf bank_mask:0xc
	v_mov_b32_dpp v33, v161 row_shr:8 row_mask:0xf bank_mask:0xc
	s_mul_i32 s28, s22, 160
	v_lshl_add_u64 v[180:181], s[28:29], 0, v[178:179]
	global_store_dwordx4 v[180:181], v[30:33], off
	s_mul_i32 s28, s22, 168
	v_lshl_add_u64 v[180:181], s[28:29], 0, v[178:179]
	global_store_dwordx4 v[180:181], v[22:25], off
	v_pk_mul_f32 v[14:15], v[14:15], v[142:143] op_sel:[0,1] op_sel_hi:[1,1]
	v_pk_mul_f32 v[16:17], v[16:17], v[142:143] op_sel:[0,1] op_sel_hi:[1,1]
	v_pk_mul_f32 v[10:11], v[10:11], v[142:143] op_sel:[0,1] op_sel_hi:[1,1]
	v_pk_mul_f32 v[12:13], v[12:13], v[142:143] op_sel:[0,1] op_sel_hi:[1,1]
	v_cvt_pk_bf16_f32 v14, v14, v15
	v_cvt_pk_bf16_f32 v15, v16, v17
	v_cvt_pk_bf16_f32 v16, v10, v11
	v_cvt_pk_bf16_f32 v17, v12, v13
	v_pk_mul_f32 v[6:7], v[6:7], v[142:143] op_sel:[0,1] op_sel_hi:[1,1]
	v_pk_mul_f32 v[8:9], v[8:9], v[142:143] op_sel:[0,1] op_sel_hi:[1,1]
	v_pk_mul_f32 v[2:3], v[2:3], v[142:143] op_sel:[0,1] op_sel_hi:[1,1]
	v_pk_mul_f32 v[4:5], v[4:5], v[142:143] op_sel:[0,1] op_sel_hi:[1,1]
	v_cvt_pk_bf16_f32 v6, v6, v7
	v_cvt_pk_bf16_f32 v7, v8, v9
	v_cvt_pk_bf16_f32 v8, v2, v3
	v_cvt_pk_bf16_f32 v9, v4, v5
	v_mov_b32_e32 v158, v6
	v_mov_b32_e32 v159, v7
	v_mov_b32_e32 v160, v8
	v_mov_b32_e32 v161, v9
	v_mov_b32_dpp v6, v14 row_shl:8 row_mask:0xf bank_mask:0x3
	v_mov_b32_dpp v7, v15 row_shl:8 row_mask:0xf bank_mask:0x3
	v_mov_b32_dpp v8, v16 row_shl:8 row_mask:0xf bank_mask:0x3
	v_mov_b32_dpp v9, v17 row_shl:8 row_mask:0xf bank_mask:0x3
	v_mov_b32_dpp v14, v158 row_shr:8 row_mask:0xf bank_mask:0xc
	v_mov_b32_dpp v15, v159 row_shr:8 row_mask:0xf bank_mask:0xc
	v_mov_b32_dpp v16, v160 row_shr:8 row_mask:0xf bank_mask:0xc
	v_mov_b32_dpp v17, v161 row_shr:8 row_mask:0xf bank_mask:0xc
	s_mul_i32 s28, s22, 176
	v_lshl_add_u64 v[180:181], s[28:29], 0, v[178:179]
	global_store_dwordx4 v[180:181], v[14:17], off
	s_mul_i32 s28, s22, 184
	v_lshl_add_u64 v[180:181], s[28:29], 0, v[178:179]
	global_store_dwordx4 v[180:181], v[6:9], off
	s_branch .Lpj_done
.Lpj_gelu:
	v_pk_mul_f32 v[126:127], v[126:127], v[136:137] op_sel_hi:[1,0]
	v_pk_mul_f32 v[128:129], v[128:129], v[136:137] op_sel_hi:[1,0]
	v_pk_mul_f32 v[122:123], v[122:123], v[136:137] op_sel_hi:[1,0]
	v_pk_mul_f32 v[124:125], v[124:125], v[136:137] op_sel_hi:[1,0]
	v_pk_mul_f32 v[144:145], v[126:127], v[188:189]
	v_pk_mul_f32 v[146:147], v[128:129], v[188:189]
	v_pk_mul_f32 v[148:149], v[122:123], v[188:189]
	v_pk_mul_f32 v[150:151], v[124:125], v[188:189]
	v_pk_mul_f32 v[144:145], v[126:127], v[144:145]
	v_pk_mul_f32 v[146:147], v[128:129], v[146:147]
	v_pk_mul_f32 v[148:149], v[122:123], v[148:149]
	v_pk_mul_f32 v[150:151], v[124:125], v[150:151]
	v_pk_fma_f32 v[144:145], v[126:127], v[144:145], v[126:127]
	v_pk_fma_f32 v[146:147], v[128:129], v[146:147], v[128:129]
	v_pk_fma_f32 v[148:149], v[122:123], v[148:149], v[122:123]
	v_pk_fma_f32 v[150:151], v[124:125], v[150:151], v[124:125]
	v_pk_mul_f32 v[144:145], v[144:145], v[190:191]
	v_pk_mul_f32 v[146:147], v[146:147], v[190:191]
	v_pk_mul_f32 v[148:149], v[148:149], v[190:191]
	v_pk_mul_f32 v[150:151], v[150:151], v[190:191]
	v_pk_mul_f32 v[144:145], v[144:145], v[186:187]
	v_pk_mul_f32 v[146:147], v[146:147], v[186:187]
	v_pk_mul_f32 v[148:149], v[148:149], v[186:187]
	v_pk_mul_f32 v[150:151], v[150:151], v[186:187]
	v_exp_f32_e32 v144, v144
	v_exp_f32_e32 v145, v145
	v_exp_f32_e32 v146, v146
	v_exp_f32_e32 v147, v147
	v_exp_f32_e32 v148, v148
	v_exp_f32_e32 v149, v149
	v_exp_f32_e32 v150, v150
	v_exp_f32_e32 v151, v151
	s_nop 0
	v_pk_add_f32 v[144:145], v[144:145], v[184:185]
	v_pk_add_f32 v[146:147], v[146:147], v[184:185]
	v_pk_add_f32 v[148:149], v[148:149], v[184:185]
	v_pk_add_f32 v[150:151], v[150:151], v[184:185]
	v_rcp_f32_e32 v144, v144
	v_rcp_f32_e32 v145, v145
	v_rcp_f32_e32 v146, v146
	v_rcp_f32_e32 v147, v147
	v_rcp_f32_e32 v148, v148
	v_rcp_f32_e32 v149, v149
	v_rcp_f32_e32 v150, v150
	v_rcp_f32_e32 v151, v151
	s_nop 0
	v_pk_mul_f32 v[126:127], v[126:127], v[144:145]
	v_pk_mul_f32 v[128:129], v[128:129], v[146:147]
	v_pk_mul_f32 v[122:123], v[122:123], v[148:149]
	v_pk_mul_f32 v[124:125], v[124:125], v[150:151]
	v_cvt_pk_bf16_f32 v126, v126, v127
	v_cvt_pk_bf16_f32 v127, v128, v129
	v_cvt_pk_bf16_f32 v128, v122, v123
	v_cvt_pk_bf16_f32 v129, v124, v125
	v_pk_mul_f32 v[118:119], v[118:119], v[136:137] op_sel_hi:[1,0]
	v_pk_mul_f32 v[120:121], v[120:121], v[136:137] op_sel_hi:[1,0]
	v_pk_mul_f32 v[114:115], v[114:115], v[136:137] op_sel_hi:[1,0]
	v_pk_mul_f32 v[116:117], v[116:117], v[136:137] op_sel_hi:[1,0]
	v_pk_mul_f32 v[144:145], v[118:119], v[188:189]
	v_pk_mul_f32 v[146:147], v[120:121], v[188:189]
	v_pk_mul_f32 v[148:149], v[114:115], v[188:189]
	v_pk_mul_f32 v[150:151], v[116:117], v[188:189]
	v_pk_mul_f32 v[144:145], v[118:119], v[144:145]
	v_pk_mul_f32 v[146:147], v[120:121], v[146:147]
	v_pk_mul_f32 v[148:149], v[114:115], v[148:149]
	v_pk_mul_f32 v[150:151], v[116:117], v[150:151]
	v_pk_fma_f32 v[144:145], v[118:119], v[144:145], v[118:119]
	v_pk_fma_f32 v[146:147], v[120:121], v[146:147], v[120:121]
	v_pk_fma_f32 v[148:149], v[114:115], v[148:149], v[114:115]
	v_pk_fma_f32 v[150:151], v[116:117], v[150:151], v[116:117]
	v_pk_mul_f32 v[144:145], v[144:145], v[190:191]
	v_pk_mul_f32 v[146:147], v[146:147], v[190:191]
	v_pk_mul_f32 v[148:149], v[148:149], v[190:191]
	v_pk_mul_f32 v[150:151], v[150:151], v[190:191]
	v_pk_mul_f32 v[144:145], v[144:145], v[186:187]
	v_pk_mul_f32 v[146:147], v[146:147], v[186:187]
	v_pk_mul_f32 v[148:149], v[148:149], v[186:187]
	v_pk_mul_f32 v[150:151], v[150:151], v[186:187]
	v_exp_f32_e32 v144, v144
	v_exp_f32_e32 v145, v145
	v_exp_f32_e32 v146, v146
	v_exp_f32_e32 v147, v147
	v_exp_f32_e32 v148, v148
	v_exp_f32_e32 v149, v149
	v_exp_f32_e32 v150, v150
	v_exp_f32_e32 v151, v151
	s_nop 0
	v_pk_add_f32 v[144:145], v[144:145], v[184:185]
	v_pk_add_f32 v[146:147], v[146:147], v[184:185]
	v_pk_add_f32 v[148:149], v[148:149], v[184:185]
	v_pk_add_f32 v[150:151], v[150:151], v[184:185]
	v_rcp_f32_e32 v144, v144
	v_rcp_f32_e32 v145, v145
	v_rcp_f32_e32 v146, v146
	v_rcp_f32_e32 v147, v147
	v_rcp_f32_e32 v148, v148
	v_rcp_f32_e32 v149, v149
	v_rcp_f32_e32 v150, v150
	v_rcp_f32_e32 v151, v151
	s_nop 0
	v_pk_mul_f32 v[118:119], v[118:119], v[144:145]
	v_pk_mul_f32 v[120:121], v[120:121], v[146:147]
	v_pk_mul_f32 v[114:115], v[114:115], v[148:149]
	v_pk_mul_f32 v[116:117], v[116:117], v[150:151]
	v_cvt_pk_bf16_f32 v118, v118, v119
	v_cvt_pk_bf16_f32 v119, v120, v121
	v_cvt_pk_bf16_f32 v120, v114, v115
	v_cvt_pk_bf16_f32 v121, v116, v117
	v_mov_b32_e32 v158, v118
	v_mov_b32_e32 v159, v119
	v_mov_b32_e32 v160, v120
	v_mov_b32_e32 v161, v121
	v_mov_b32_dpp v118, v126 row_shl:8 row_mask:0xf bank_mask:0x3
	v_mov_b32_dpp v119, v127 row_shl:8 row_mask:0xf bank_mask:0x3
	v_mov_b32_dpp v120, v128 row_shl:8 row_mask:0xf bank_mask:0x3
	v_mov_b32_dpp v121, v129 row_shl:8 row_mask:0xf bank_mask:0x3
	v_mov_b32_dpp v126, v158 row_shr:8 row_mask:0xf bank_mask:0xc
	v_mov_b32_dpp v127, v159 row_shr:8 row_mask:0xf bank_mask:0xc
	v_mov_b32_dpp v128, v160 row_shr:8 row_mask:0xf bank_mask:0xc
	v_mov_b32_dpp v129, v161 row_shr:8 row_mask:0xf bank_mask:0xc
	s_mul_i32 s28, s22, 0
	v_lshl_add_u64 v[180:181], s[28:29], 0, v[178:179]
	global_store_dwordx4 v[180:181], v[126:129], off
	s_mul_i32 s28, s22, 8
	v_lshl_add_u64 v[180:181], s[28:29], 0, v[178:179]
	global_store_dwordx4 v[180:181], v[118:121], off
	v_pk_mul_f32 v[110:111], v[110:111], v[136:137] op_sel:[0,1] op_sel_hi:[1,1]
	v_pk_mul_f32 v[112:113], v[112:113], v[136:137] op_sel:[0,1] op_sel_hi:[1,1]
	v_pk_mul_f32 v[106:107], v[106:107], v[136:137] op_sel:[0,1] op_sel_hi:[1,1]
	v_pk_mul_f32 v[108:109], v[108:109], v[136:137] op_sel:[0,1] op_sel_hi:[1,1]
	v_pk_mul_f32 v[144:145], v[110:111], v[188:189]
	v_pk_mul_f32 v[146:147], v[112:113], v[188:189]
	v_pk_mul_f32 v[148:149], v[106:107], v[188:189]
	v_pk_mul_f32 v[150:151], v[108:109], v[188:189]
	v_pk_mul_f32 v[144:145], v[110:111], v[144:145]
	v_pk_mul_f32 v[146:147], v[112:113], v[146:147]
	v_pk_mul_f32 v[148:149], v[106:107], v[148:149]
	v_pk_mul_f32 v[150:151], v[108:109], v[150:151]
	v_pk_fma_f32 v[144:145], v[110:111], v[144:145], v[110:111]
	v_pk_fma_f32 v[146:147], v[112:113], v[146:147], v[112:113]
	v_pk_fma_f32 v[148:149], v[106:107], v[148:149], v[106:107]
	v_pk_fma_f32 v[150:151], v[108:109], v[150:151], v[108:109]
	v_pk_mul_f32 v[144:145], v[144:145], v[190:191]
	v_pk_mul_f32 v[146:147], v[146:147], v[190:191]
	v_pk_mul_f32 v[148:149], v[148:149], v[190:191]
	v_pk_mul_f32 v[150:151], v[150:151], v[190:191]
	v_pk_mul_f32 v[144:145], v[144:145], v[186:187]
	v_pk_mul_f32 v[146:147], v[146:147], v[186:187]
	v_pk_mul_f32 v[148:149], v[148:149], v[186:187]
	v_pk_mul_f32 v[150:151], v[150:151], v[186:187]
	v_exp_f32_e32 v144, v144
	v_exp_f32_e32 v145, v145
	v_exp_f32_e32 v146, v146
	v_exp_f32_e32 v147, v147
	v_exp_f32_e32 v148, v148
	v_exp_f32_e32 v149, v149
	v_exp_f32_e32 v150, v150
	v_exp_f32_e32 v151, v151
	s_nop 0
	v_pk_add_f32 v[144:145], v[144:145], v[184:185]
	v_pk_add_f32 v[146:147], v[146:147], v[184:185]
	v_pk_add_f32 v[148:149], v[148:149], v[184:185]
	v_pk_add_f32 v[150:151], v[150:151], v[184:185]
	v_rcp_f32_e32 v144, v144
	v_rcp_f32_e32 v145, v145
	v_rcp_f32_e32 v146, v146
	v_rcp_f32_e32 v147, v147
	v_rcp_f32_e32 v148, v148
	v_rcp_f32_e32 v149, v149
	v_rcp_f32_e32 v150, v150
	v_rcp_f32_e32 v151, v151
	s_nop 0
	v_pk_mul_f32 v[110:111], v[110:111], v[144:145]
	v_pk_mul_f32 v[112:113], v[112:113], v[146:147]
	v_pk_mul_f32 v[106:107], v[106:107], v[148:149]
	v_pk_mul_f32 v[108:109], v[108:109], v[150:151]
	v_cvt_pk_bf16_f32 v110, v110, v111
	v_cvt_pk_bf16_f32 v111, v112, v113
	v_cvt_pk_bf16_f32 v112, v106, v107
	v_cvt_pk_bf16_f32 v113, v108, v109
	v_pk_mul_f32 v[102:103], v[102:103], v[136:137] op_sel:[0,1] op_sel_hi:[1,1]
	v_pk_mul_f32 v[104:105], v[104:105], v[136:137] op_sel:[0,1] op_sel_hi:[1,1]
	v_pk_mul_f32 v[98:99], v[98:99], v[136:137] op_sel:[0,1] op_sel_hi:[1,1]
	v_pk_mul_f32 v[100:101], v[100:101], v[136:137] op_sel:[0,1] op_sel_hi:[1,1]
	v_pk_mul_f32 v[144:145], v[102:103], v[188:189]
	v_pk_mul_f32 v[146:147], v[104:105], v[188:189]
	v_pk_mul_f32 v[148:149], v[98:99], v[188:189]
	v_pk_mul_f32 v[150:151], v[100:101], v[188:189]
	v_pk_mul_f32 v[144:145], v[102:103], v[144:145]
	v_pk_mul_f32 v[146:147], v[104:105], v[146:147]
	v_pk_mul_f32 v[148:149], v[98:99], v[148:149]
	v_pk_mul_f32 v[150:151], v[100:101], v[150:151]
	v_pk_fma_f32 v[144:145], v[102:103], v[144:145], v[102:103]
	v_pk_fma_f32 v[146:147], v[104:105], v[146:147], v[104:105]
	v_pk_fma_f32 v[148:149], v[98:99], v[148:149], v[98:99]
	v_pk_fma_f32 v[150:151], v[100:101], v[150:151], v[100:101]
	v_pk_mul_f32 v[144:145], v[144:145], v[190:191]
	v_pk_mul_f32 v[146:147], v[146:147], v[190:191]
	v_pk_mul_f32 v[148:149], v[148:149], v[190:191]
	v_pk_mul_f32 v[150:151], v[150:151], v[190:191]
	v_pk_mul_f32 v[144:145], v[144:145], v[186:187]
	v_pk_mul_f32 v[146:147], v[146:147], v[186:187]
	v_pk_mul_f32 v[148:149], v[148:149], v[186:187]
	v_pk_mul_f32 v[150:151], v[150:151], v[186:187]
	v_exp_f32_e32 v144, v144
	v_exp_f32_e32 v145, v145
	v_exp_f32_e32 v146, v146
	v_exp_f32_e32 v147, v147
	v_exp_f32_e32 v148, v148
	v_exp_f32_e32 v149, v149
	v_exp_f32_e32 v150, v150
	v_exp_f32_e32 v151, v151
	s_nop 0
	v_pk_add_f32 v[144:145], v[144:145], v[184:185]
	v_pk_add_f32 v[146:147], v[146:147], v[184:185]
	v_pk_add_f32 v[148:149], v[148:149], v[184:185]
	v_pk_add_f32 v[150:151], v[150:151], v[184:185]
	v_rcp_f32_e32 v144, v144
	v_rcp_f32_e32 v145, v145
	v_rcp_f32_e32 v146, v146
	v_rcp_f32_e32 v147, v147
	v_rcp_f32_e32 v148, v148
	v_rcp_f32_e32 v149, v149
	v_rcp_f32_e32 v150, v150
	v_rcp_f32_e32 v151, v151
	s_nop 0
	v_pk_mul_f32 v[102:103], v[102:103], v[144:145]
	v_pk_mul_f32 v[104:105], v[104:105], v[146:147]
	v_pk_mul_f32 v[98:99], v[98:99], v[148:149]
	v_pk_mul_f32 v[100:101], v[100:101], v[150:151]
	v_cvt_pk_bf16_f32 v102, v102, v103
	v_cvt_pk_bf16_f32 v103, v104, v105
	v_cvt_pk_bf16_f32 v104, v98, v99
	v_cvt_pk_bf16_f32 v105, v100, v101
	v_mov_b32_e32 v158, v102
	v_mov_b32_e32 v159, v103
	v_mov_b32_e32 v160, v104
	v_mov_b32_e32 v161, v105
	v_mov_b32_dpp v102, v110 row_shl:8 row_mask:0xf bank_mask:0x3
	v_mov_b32_dpp v103, v111 row_shl:8 row_mask:0xf bank_mask:0x3
	v_mov_b32_dpp v104, v112 row_shl:8 row_mask:0xf bank_mask:0x3
	v_mov_b32_dpp v105, v113 row_shl:8 row_mask:0xf bank_mask:0x3
	v_mov_b32_dpp v110, v158 row_shr:8 row_mask:0xf bank_mask:0xc
	v_mov_b32_dpp v111, v159 row_shr:8 row_mask:0xf bank_mask:0xc
	v_mov_b32_dpp v112, v160 row_shr:8 row_mask:0xf bank_mask:0xc
	v_mov_b32_dpp v113, v161 row_shr:8 row_mask:0xf bank_mask:0xc
	s_mul_i32 s28, s22, 16
	v_lshl_add_u64 v[180:181], s[28:29], 0, v[178:179]
	global_store_dwordx4 v[180:181], v[110:113], off
	s_mul_i32 s28, s22, 24
	v_lshl_add_u64 v[180:181], s[28:29], 0, v[178:179]
	global_store_dwordx4 v[180:181], v[102:105], off
	v_pk_mul_f32 v[94:95], v[94:95], v[138:139] op_sel_hi:[1,0]
	v_pk_mul_f32 v[96:97], v[96:97], v[138:139] op_sel_hi:[1,0]
	v_pk_mul_f32 v[90:91], v[90:91], v[138:139] op_sel_hi:[1,0]
	v_pk_mul_f32 v[92:93], v[92:93], v[138:139] op_sel_hi:[1,0]
	v_pk_mul_f32 v[144:145], v[94:95], v[188:189]
	v_pk_mul_f32 v[146:147], v[96:97], v[188:189]
	v_pk_mul_f32 v[148:149], v[90:91], v[188:189]
	v_pk_mul_f32 v[150:151], v[92:93], v[188:189]
	v_pk_mul_f32 v[144:145], v[94:95], v[144:145]
	v_pk_mul_f32 v[146:147], v[96:97], v[146:147]
	v_pk_mul_f32 v[148:149], v[90:91], v[148:149]
	v_pk_mul_f32 v[150:151], v[92:93], v[150:151]
	v_pk_fma_f32 v[144:145], v[94:95], v[144:145], v[94:95]
	v_pk_fma_f32 v[146:147], v[96:97], v[146:147], v[96:97]
	v_pk_fma_f32 v[148:149], v[90:91], v[148:149], v[90:91]
	v_pk_fma_f32 v[150:151], v[92:93], v[150:151], v[92:93]
	v_pk_mul_f32 v[144:145], v[144:145], v[190:191]
	v_pk_mul_f32 v[146:147], v[146:147], v[190:191]
	v_pk_mul_f32 v[148:149], v[148:149], v[190:191]
	v_pk_mul_f32 v[150:151], v[150:151], v[190:191]
	v_pk_mul_f32 v[144:145], v[144:145], v[186:187]
	v_pk_mul_f32 v[146:147], v[146:147], v[186:187]
	v_pk_mul_f32 v[148:149], v[148:149], v[186:187]
	v_pk_mul_f32 v[150:151], v[150:151], v[186:187]
	v_exp_f32_e32 v144, v144
	v_exp_f32_e32 v145, v145
	v_exp_f32_e32 v146, v146
	v_exp_f32_e32 v147, v147
	v_exp_f32_e32 v148, v148
	v_exp_f32_e32 v149, v149
	v_exp_f32_e32 v150, v150
	v_exp_f32_e32 v151, v151
	s_nop 0
	v_pk_add_f32 v[144:145], v[144:145], v[184:185]
	v_pk_add_f32 v[146:147], v[146:147], v[184:185]
	v_pk_add_f32 v[148:149], v[148:149], v[184:185]
	v_pk_add_f32 v[150:151], v[150:151], v[184:185]
	v_rcp_f32_e32 v144, v144
	v_rcp_f32_e32 v145, v145
	v_rcp_f32_e32 v146, v146
	v_rcp_f32_e32 v147, v147
	v_rcp_f32_e32 v148, v148
	v_rcp_f32_e32 v149, v149
	v_rcp_f32_e32 v150, v150
	v_rcp_f32_e32 v151, v151
	s_nop 0
	v_pk_mul_f32 v[94:95], v[94:95], v[144:145]
	v_pk_mul_f32 v[96:97], v[96:97], v[146:147]
	v_pk_mul_f32 v[90:91], v[90:91], v[148:149]
	v_pk_mul_f32 v[92:93], v[92:93], v[150:151]
	v_cvt_pk_bf16_f32 v94, v94, v95
	v_cvt_pk_bf16_f32 v95, v96, v97
	v_cvt_pk_bf16_f32 v96, v90, v91
	v_cvt_pk_bf16_f32 v97, v92, v93
	v_pk_mul_f32 v[86:87], v[86:87], v[138:139] op_sel_hi:[1,0]
	v_pk_mul_f32 v[88:89], v[88:89], v[138:139] op_sel_hi:[1,0]
	v_pk_mul_f32 v[82:83], v[82:83], v[138:139] op_sel_hi:[1,0]
	v_pk_mul_f32 v[84:85], v[84:85], v[138:139] op_sel_hi:[1,0]
	v_pk_mul_f32 v[144:145], v[86:87], v[188:189]
	v_pk_mul_f32 v[146:147], v[88:89], v[188:189]
	v_pk_mul_f32 v[148:149], v[82:83], v[188:189]
	v_pk_mul_f32 v[150:151], v[84:85], v[188:189]
	v_pk_mul_f32 v[144:145], v[86:87], v[144:145]
	v_pk_mul_f32 v[146:147], v[88:89], v[146:147]
	v_pk_mul_f32 v[148:149], v[82:83], v[148:149]
	v_pk_mul_f32 v[150:151], v[84:85], v[150:151]
	v_pk_fma_f32 v[144:145], v[86:87], v[144:145], v[86:87]
	v_pk_fma_f32 v[146:147], v[88:89], v[146:147], v[88:89]
	v_pk_fma_f32 v[148:149], v[82:83], v[148:149], v[82:83]
	v_pk_fma_f32 v[150:151], v[84:85], v[150:151], v[84:85]
	v_pk_mul_f32 v[144:145], v[144:145], v[190:191]
	v_pk_mul_f32 v[146:147], v[146:147], v[190:191]
	v_pk_mul_f32 v[148:149], v[148:149], v[190:191]
	v_pk_mul_f32 v[150:151], v[150:151], v[190:191]
	v_pk_mul_f32 v[144:145], v[144:145], v[186:187]
	v_pk_mul_f32 v[146:147], v[146:147], v[186:187]
	v_pk_mul_f32 v[148:149], v[148:149], v[186:187]
	v_pk_mul_f32 v[150:151], v[150:151], v[186:187]
	v_exp_f32_e32 v144, v144
	v_exp_f32_e32 v145, v145
	v_exp_f32_e32 v146, v146
	v_exp_f32_e32 v147, v147
	v_exp_f32_e32 v148, v148
	v_exp_f32_e32 v149, v149
	v_exp_f32_e32 v150, v150
	v_exp_f32_e32 v151, v151
	s_nop 0
	v_pk_add_f32 v[144:145], v[144:145], v[184:185]
	v_pk_add_f32 v[146:147], v[146:147], v[184:185]
	v_pk_add_f32 v[148:149], v[148:149], v[184:185]
	v_pk_add_f32 v[150:151], v[150:151], v[184:185]
	v_rcp_f32_e32 v144, v144
	v_rcp_f32_e32 v145, v145
	v_rcp_f32_e32 v146, v146
	v_rcp_f32_e32 v147, v147
	v_rcp_f32_e32 v148, v148
	v_rcp_f32_e32 v149, v149
	v_rcp_f32_e32 v150, v150
	v_rcp_f32_e32 v151, v151
	s_nop 0
	v_pk_mul_f32 v[86:87], v[86:87], v[144:145]
	v_pk_mul_f32 v[88:89], v[88:89], v[146:147]
	v_pk_mul_f32 v[82:83], v[82:83], v[148:149]
	v_pk_mul_f32 v[84:85], v[84:85], v[150:151]
	v_cvt_pk_bf16_f32 v86, v86, v87
	v_cvt_pk_bf16_f32 v87, v88, v89
	v_cvt_pk_bf16_f32 v88, v82, v83
	v_cvt_pk_bf16_f32 v89, v84, v85
	v_mov_b32_e32 v158, v86
	v_mov_b32_e32 v159, v87
	v_mov_b32_e32 v160, v88
	v_mov_b32_e32 v161, v89
	v_mov_b32_dpp v86, v94 row_shl:8 row_mask:0xf bank_mask:0x3
	v_mov_b32_dpp v87, v95 row_shl:8 row_mask:0xf bank_mask:0x3
	v_mov_b32_dpp v88, v96 row_shl:8 row_mask:0xf bank_mask:0x3
	v_mov_b32_dpp v89, v97 row_shl:8 row_mask:0xf bank_mask:0x3
	v_mov_b32_dpp v94, v158 row_shr:8 row_mask:0xf bank_mask:0xc
	v_mov_b32_dpp v95, v159 row_shr:8 row_mask:0xf bank_mask:0xc
	v_mov_b32_dpp v96, v160 row_shr:8 row_mask:0xf bank_mask:0xc
	v_mov_b32_dpp v97, v161 row_shr:8 row_mask:0xf bank_mask:0xc
	s_mul_i32 s28, s22, 32
	v_lshl_add_u64 v[180:181], s[28:29], 0, v[178:179]
	global_store_dwordx4 v[180:181], v[94:97], off
	s_mul_i32 s28, s22, 40
	v_lshl_add_u64 v[180:181], s[28:29], 0, v[178:179]
	global_store_dwordx4 v[180:181], v[86:89], off
	v_pk_mul_f32 v[78:79], v[78:79], v[138:139] op_sel:[0,1] op_sel_hi:[1,1]
	v_pk_mul_f32 v[80:81], v[80:81], v[138:139] op_sel:[0,1] op_sel_hi:[1,1]
	v_pk_mul_f32 v[74:75], v[74:75], v[138:139] op_sel:[0,1] op_sel_hi:[1,1]
	v_pk_mul_f32 v[76:77], v[76:77], v[138:139] op_sel:[0,1] op_sel_hi:[1,1]
	v_pk_mul_f32 v[144:145], v[78:79], v[188:189]
	v_pk_mul_f32 v[146:147], v[80:81], v[188:189]
	v_pk_mul_f32 v[148:149], v[74:75], v[188:189]
	v_pk_mul_f32 v[150:151], v[76:77], v[188:189]
	v_pk_mul_f32 v[144:145], v[78:79], v[144:145]
	v_pk_mul_f32 v[146:147], v[80:81], v[146:147]
	v_pk_mul_f32 v[148:149], v[74:75], v[148:149]
	v_pk_mul_f32 v[150:151], v[76:77], v[150:151]
	v_pk_fma_f32 v[144:145], v[78:79], v[144:145], v[78:79]
	v_pk_fma_f32 v[146:147], v[80:81], v[146:147], v[80:81]
	v_pk_fma_f32 v[148:149], v[74:75], v[148:149], v[74:75]
	v_pk_fma_f32 v[150:151], v[76:77], v[150:151], v[76:77]
	v_pk_mul_f32 v[144:145], v[144:145], v[190:191]
	v_pk_mul_f32 v[146:147], v[146:147], v[190:191]
	v_pk_mul_f32 v[148:149], v[148:149], v[190:191]
	v_pk_mul_f32 v[150:151], v[150:151], v[190:191]
	v_pk_mul_f32 v[144:145], v[144:145], v[186:187]
	v_pk_mul_f32 v[146:147], v[146:147], v[186:187]
	v_pk_mul_f32 v[148:149], v[148:149], v[186:187]
	v_pk_mul_f32 v[150:151], v[150:151], v[186:187]
	v_exp_f32_e32 v144, v144
	v_exp_f32_e32 v145, v145
	v_exp_f32_e32 v146, v146
	v_exp_f32_e32 v147, v147
	v_exp_f32_e32 v148, v148
	v_exp_f32_e32 v149, v149
	v_exp_f32_e32 v150, v150
	v_exp_f32_e32 v151, v151
	s_nop 0
	v_pk_add_f32 v[144:145], v[144:145], v[184:185]
	v_pk_add_f32 v[146:147], v[146:147], v[184:185]
	v_pk_add_f32 v[148:149], v[148:149], v[184:185]
	v_pk_add_f32 v[150:151], v[150:151], v[184:185]
	v_rcp_f32_e32 v144, v144
	v_rcp_f32_e32 v145, v145
	v_rcp_f32_e32 v146, v146
	v_rcp_f32_e32 v147, v147
	v_rcp_f32_e32 v148, v148
	v_rcp_f32_e32 v149, v149
	v_rcp_f32_e32 v150, v150
	v_rcp_f32_e32 v151, v151
	s_nop 0
	v_pk_mul_f32 v[78:79], v[78:79], v[144:145]
	v_pk_mul_f32 v[80:81], v[80:81], v[146:147]
	v_pk_mul_f32 v[74:75], v[74:75], v[148:149]
	v_pk_mul_f32 v[76:77], v[76:77], v[150:151]
	v_cvt_pk_bf16_f32 v78, v78, v79
	v_cvt_pk_bf16_f32 v79, v80, v81
	v_cvt_pk_bf16_f32 v80, v74, v75
	v_cvt_pk_bf16_f32 v81, v76, v77
	v_pk_mul_f32 v[70:71], v[70:71], v[138:139] op_sel:[0,1] op_sel_hi:[1,1]
	v_pk_mul_f32 v[72:73], v[72:73], v[138:139] op_sel:[0,1] op_sel_hi:[1,1]
	v_pk_mul_f32 v[66:67], v[66:67], v[138:139] op_sel:[0,1] op_sel_hi:[1,1]
	v_pk_mul_f32 v[68:69], v[68:69], v[138:139] op_sel:[0,1] op_sel_hi:[1,1]
	v_pk_mul_f32 v[144:145], v[70:71], v[188:189]
	v_pk_mul_f32 v[146:147], v[72:73], v[188:189]
	v_pk_mul_f32 v[148:149], v[66:67], v[188:189]
	v_pk_mul_f32 v[150:151], v[68:69], v[188:189]
	v_pk_mul_f32 v[144:145], v[70:71], v[144:145]
	v_pk_mul_f32 v[146:147], v[72:73], v[146:147]
	v_pk_mul_f32 v[148:149], v[66:67], v[148:149]
	v_pk_mul_f32 v[150:151], v[68:69], v[150:151]
	v_pk_fma_f32 v[144:145], v[70:71], v[144:145], v[70:71]
	v_pk_fma_f32 v[146:147], v[72:73], v[146:147], v[72:73]
	v_pk_fma_f32 v[148:149], v[66:67], v[148:149], v[66:67]
	v_pk_fma_f32 v[150:151], v[68:69], v[150:151], v[68:69]
	v_pk_mul_f32 v[144:145], v[144:145], v[190:191]
	v_pk_mul_f32 v[146:147], v[146:147], v[190:191]
	v_pk_mul_f32 v[148:149], v[148:149], v[190:191]
	v_pk_mul_f32 v[150:151], v[150:151], v[190:191]
	v_pk_mul_f32 v[144:145], v[144:145], v[186:187]
	v_pk_mul_f32 v[146:147], v[146:147], v[186:187]
	v_pk_mul_f32 v[148:149], v[148:149], v[186:187]
	v_pk_mul_f32 v[150:151], v[150:151], v[186:187]
	v_exp_f32_e32 v144, v144
	v_exp_f32_e32 v145, v145
	v_exp_f32_e32 v146, v146
	v_exp_f32_e32 v147, v147
	v_exp_f32_e32 v148, v148
	v_exp_f32_e32 v149, v149
	v_exp_f32_e32 v150, v150
	v_exp_f32_e32 v151, v151
	s_nop 0
	v_pk_add_f32 v[144:145], v[144:145], v[184:185]
	v_pk_add_f32 v[146:147], v[146:147], v[184:185]
	v_pk_add_f32 v[148:149], v[148:149], v[184:185]
	v_pk_add_f32 v[150:151], v[150:151], v[184:185]
	v_rcp_f32_e32 v144, v144
	v_rcp_f32_e32 v145, v145
	v_rcp_f32_e32 v146, v146
	v_rcp_f32_e32 v147, v147
	v_rcp_f32_e32 v148, v148
	v_rcp_f32_e32 v149, v149
	v_rcp_f32_e32 v150, v150
	v_rcp_f32_e32 v151, v151
	s_nop 0
	v_pk_mul_f32 v[70:71], v[70:71], v[144:145]
	v_pk_mul_f32 v[72:73], v[72:73], v[146:147]
	v_pk_mul_f32 v[66:67], v[66:67], v[148:149]
	v_pk_mul_f32 v[68:69], v[68:69], v[150:151]
	v_cvt_pk_bf16_f32 v70, v70, v71
	v_cvt_pk_bf16_f32 v71, v72, v73
	v_cvt_pk_bf16_f32 v72, v66, v67
	v_cvt_pk_bf16_f32 v73, v68, v69
	v_mov_b32_e32 v158, v70
	v_mov_b32_e32 v159, v71
	v_mov_b32_e32 v160, v72
	v_mov_b32_e32 v161, v73
	v_mov_b32_dpp v70, v78 row_shl:8 row_mask:0xf bank_mask:0x3
	v_mov_b32_dpp v71, v79 row_shl:8 row_mask:0xf bank_mask:0x3
	v_mov_b32_dpp v72, v80 row_shl:8 row_mask:0xf bank_mask:0x3
	v_mov_b32_dpp v73, v81 row_shl:8 row_mask:0xf bank_mask:0x3
	v_mov_b32_dpp v78, v158 row_shr:8 row_mask:0xf bank_mask:0xc
	v_mov_b32_dpp v79, v159 row_shr:8 row_mask:0xf bank_mask:0xc
	v_mov_b32_dpp v80, v160 row_shr:8 row_mask:0xf bank_mask:0xc
	v_mov_b32_dpp v81, v161 row_shr:8 row_mask:0xf bank_mask:0xc
	s_mul_i32 s28, s22, 48
	v_lshl_add_u64 v[180:181], s[28:29], 0, v[178:179]
	global_store_dwordx4 v[180:181], v[78:81], off
	s_mul_i32 s28, s22, 56
	v_lshl_add_u64 v[180:181], s[28:29], 0, v[178:179]
	global_store_dwordx4 v[180:181], v[70:73], off
	v_pk_mul_f32 v[62:63], v[62:63], v[140:141] op_sel_hi:[1,0]
	v_pk_mul_f32 v[64:65], v[64:65], v[140:141] op_sel_hi:[1,0]
	v_pk_mul_f32 v[58:59], v[58:59], v[140:141] op_sel_hi:[1,0]
	v_pk_mul_f32 v[60:61], v[60:61], v[140:141] op_sel_hi:[1,0]
	v_pk_mul_f32 v[144:145], v[62:63], v[188:189]
	v_pk_mul_f32 v[146:147], v[64:65], v[188:189]
	v_pk_mul_f32 v[148:149], v[58:59], v[188:189]
	v_pk_mul_f32 v[150:151], v[60:61], v[188:189]
	v_pk_mul_f32 v[144:145], v[62:63], v[144:145]
	v_pk_mul_f32 v[146:147], v[64:65], v[146:147]
	v_pk_mul_f32 v[148:149], v[58:59], v[148:149]
	v_pk_mul_f32 v[150:151], v[60:61], v[150:151]
	v_pk_fma_f32 v[144:145], v[62:63], v[144:145], v[62:63]
	v_pk_fma_f32 v[146:147], v[64:65], v[146:147], v[64:65]
	v_pk_fma_f32 v[148:149], v[58:59], v[148:149], v[58:59]
	v_pk_fma_f32 v[150:151], v[60:61], v[150:151], v[60:61]
	v_pk_mul_f32 v[144:145], v[144:145], v[190:191]
	v_pk_mul_f32 v[146:147], v[146:147], v[190:191]
	v_pk_mul_f32 v[148:149], v[148:149], v[190:191]
	v_pk_mul_f32 v[150:151], v[150:151], v[190:191]
	v_pk_mul_f32 v[144:145], v[144:145], v[186:187]
	v_pk_mul_f32 v[146:147], v[146:147], v[186:187]
	v_pk_mul_f32 v[148:149], v[148:149], v[186:187]
	v_pk_mul_f32 v[150:151], v[150:151], v[186:187]
	v_exp_f32_e32 v144, v144
	v_exp_f32_e32 v145, v145
	v_exp_f32_e32 v146, v146
	v_exp_f32_e32 v147, v147
	v_exp_f32_e32 v148, v148
	v_exp_f32_e32 v149, v149
	v_exp_f32_e32 v150, v150
	v_exp_f32_e32 v151, v151
	s_nop 0
	v_pk_add_f32 v[144:145], v[144:145], v[184:185]
	v_pk_add_f32 v[146:147], v[146:147], v[184:185]
	v_pk_add_f32 v[148:149], v[148:149], v[184:185]
	v_pk_add_f32 v[150:151], v[150:151], v[184:185]
	v_rcp_f32_e32 v144, v144
	v_rcp_f32_e32 v145, v145
	v_rcp_f32_e32 v146, v146
	v_rcp_f32_e32 v147, v147
	v_rcp_f32_e32 v148, v148
	v_rcp_f32_e32 v149, v149
	v_rcp_f32_e32 v150, v150
	v_rcp_f32_e32 v151, v151
	s_nop 0
	v_pk_mul_f32 v[62:63], v[62:63], v[144:145]
	v_pk_mul_f32 v[64:65], v[64:65], v[146:147]
	v_pk_mul_f32 v[58:59], v[58:59], v[148:149]
	v_pk_mul_f32 v[60:61], v[60:61], v[150:151]
	v_cvt_pk_bf16_f32 v62, v62, v63
	v_cvt_pk_bf16_f32 v63, v64, v65
	v_cvt_pk_bf16_f32 v64, v58, v59
	v_cvt_pk_bf16_f32 v65, v60, v61
	v_pk_mul_f32 v[54:55], v[54:55], v[140:141] op_sel_hi:[1,0]
	v_pk_mul_f32 v[56:57], v[56:57], v[140:141] op_sel_hi:[1,0]
	v_pk_mul_f32 v[50:51], v[50:51], v[140:141] op_sel_hi:[1,0]
	v_pk_mul_f32 v[52:53], v[52:53], v[140:141] op_sel_hi:[1,0]
	v_pk_mul_f32 v[144:145], v[54:55], v[188:189]
	v_pk_mul_f32 v[146:147], v[56:57], v[188:189]
	v_pk_mul_f32 v[148:149], v[50:51], v[188:189]
	v_pk_mul_f32 v[150:151], v[52:53], v[188:189]
	v_pk_mul_f32 v[144:145], v[54:55], v[144:145]
	v_pk_mul_f32 v[146:147], v[56:57], v[146:147]
	v_pk_mul_f32 v[148:149], v[50:51], v[148:149]
	v_pk_mul_f32 v[150:151], v[52:53], v[150:151]
	v_pk_fma_f32 v[144:145], v[54:55], v[144:145], v[54:55]
	v_pk_fma_f32 v[146:147], v[56:57], v[146:147], v[56:57]
	v_pk_fma_f32 v[148:149], v[50:51], v[148:149], v[50:51]
	v_pk_fma_f32 v[150:151], v[52:53], v[150:151], v[52:53]
	v_pk_mul_f32 v[144:145], v[144:145], v[190:191]
	v_pk_mul_f32 v[146:147], v[146:147], v[190:191]
	v_pk_mul_f32 v[148:149], v[148:149], v[190:191]
	v_pk_mul_f32 v[150:151], v[150:151], v[190:191]
	v_pk_mul_f32 v[144:145], v[144:145], v[186:187]
	v_pk_mul_f32 v[146:147], v[146:147], v[186:187]
	v_pk_mul_f32 v[148:149], v[148:149], v[186:187]
	v_pk_mul_f32 v[150:151], v[150:151], v[186:187]
	v_exp_f32_e32 v144, v144
	v_exp_f32_e32 v145, v145
	v_exp_f32_e32 v146, v146
	v_exp_f32_e32 v147, v147
	v_exp_f32_e32 v148, v148
	v_exp_f32_e32 v149, v149
	v_exp_f32_e32 v150, v150
	v_exp_f32_e32 v151, v151
	s_nop 0
	v_pk_add_f32 v[144:145], v[144:145], v[184:185]
	v_pk_add_f32 v[146:147], v[146:147], v[184:185]
	v_pk_add_f32 v[148:149], v[148:149], v[184:185]
	v_pk_add_f32 v[150:151], v[150:151], v[184:185]
	v_rcp_f32_e32 v144, v144
	v_rcp_f32_e32 v145, v145
	v_rcp_f32_e32 v146, v146
	v_rcp_f32_e32 v147, v147
	v_rcp_f32_e32 v148, v148
	v_rcp_f32_e32 v149, v149
	v_rcp_f32_e32 v150, v150
	v_rcp_f32_e32 v151, v151
	s_nop 0
	v_pk_mul_f32 v[54:55], v[54:55], v[144:145]
	v_pk_mul_f32 v[56:57], v[56:57], v[146:147]
	v_pk_mul_f32 v[50:51], v[50:51], v[148:149]
	v_pk_mul_f32 v[52:53], v[52:53], v[150:151]
	v_cvt_pk_bf16_f32 v54, v54, v55
	v_cvt_pk_bf16_f32 v55, v56, v57
	v_cvt_pk_bf16_f32 v56, v50, v51
	v_cvt_pk_bf16_f32 v57, v52, v53
	v_mov_b32_e32 v158, v54
	v_mov_b32_e32 v159, v55
	v_mov_b32_e32 v160, v56
	v_mov_b32_e32 v161, v57
	v_mov_b32_dpp v54, v62 row_shl:8 row_mask:0xf bank_mask:0x3
	v_mov_b32_dpp v55, v63 row_shl:8 row_mask:0xf bank_mask:0x3
	v_mov_b32_dpp v56, v64 row_shl:8 row_mask:0xf bank_mask:0x3
	v_mov_b32_dpp v57, v65 row_shl:8 row_mask:0xf bank_mask:0x3
	v_mov_b32_dpp v62, v158 row_shr:8 row_mask:0xf bank_mask:0xc
	v_mov_b32_dpp v63, v159 row_shr:8 row_mask:0xf bank_mask:0xc
	v_mov_b32_dpp v64, v160 row_shr:8 row_mask:0xf bank_mask:0xc
	v_mov_b32_dpp v65, v161 row_shr:8 row_mask:0xf bank_mask:0xc
	s_mul_i32 s28, s22, 128
	v_lshl_add_u64 v[180:181], s[28:29], 0, v[178:179]
	global_store_dwordx4 v[180:181], v[62:65], off
	s_mul_i32 s28, s22, 136
	v_lshl_add_u64 v[180:181], s[28:29], 0, v[178:179]
	global_store_dwordx4 v[180:181], v[54:57], off
	v_pk_mul_f32 v[46:47], v[46:47], v[140:141] op_sel:[0,1] op_sel_hi:[1,1]
	v_pk_mul_f32 v[48:49], v[48:49], v[140:141] op_sel:[0,1] op_sel_hi:[1,1]
	v_pk_mul_f32 v[42:43], v[42:43], v[140:141] op_sel:[0,1] op_sel_hi:[1,1]
	v_pk_mul_f32 v[44:45], v[44:45], v[140:141] op_sel:[0,1] op_sel_hi:[1,1]
	v_pk_mul_f32 v[144:145], v[46:47], v[188:189]
	v_pk_mul_f32 v[146:147], v[48:49], v[188:189]
	v_pk_mul_f32 v[148:149], v[42:43], v[188:189]
	v_pk_mul_f32 v[150:151], v[44:45], v[188:189]
	v_pk_mul_f32 v[144:145], v[46:47], v[144:145]
	v_pk_mul_f32 v[146:147], v[48:49], v[146:147]
	v_pk_mul_f32 v[148:149], v[42:43], v[148:149]
	v_pk_mul_f32 v[150:151], v[44:45], v[150:151]
	v_pk_fma_f32 v[144:145], v[46:47], v[144:145], v[46:47]
	v_pk_fma_f32 v[146:147], v[48:49], v[146:147], v[48:49]
	v_pk_fma_f32 v[148:149], v[42:43], v[148:149], v[42:43]
	v_pk_fma_f32 v[150:151], v[44:45], v[150:151], v[44:45]
	v_pk_mul_f32 v[144:145], v[144:145], v[190:191]
	v_pk_mul_f32 v[146:147], v[146:147], v[190:191]
	v_pk_mul_f32 v[148:149], v[148:149], v[190:191]
	v_pk_mul_f32 v[150:151], v[150:151], v[190:191]
	v_pk_mul_f32 v[144:145], v[144:145], v[186:187]
	v_pk_mul_f32 v[146:147], v[146:147], v[186:187]
	v_pk_mul_f32 v[148:149], v[148:149], v[186:187]
	v_pk_mul_f32 v[150:151], v[150:151], v[186:187]
	v_exp_f32_e32 v144, v144
	v_exp_f32_e32 v145, v145
	v_exp_f32_e32 v146, v146
	v_exp_f32_e32 v147, v147
	v_exp_f32_e32 v148, v148
	v_exp_f32_e32 v149, v149
	v_exp_f32_e32 v150, v150
	v_exp_f32_e32 v151, v151
	s_nop 0
	v_pk_add_f32 v[144:145], v[144:145], v[184:185]
	v_pk_add_f32 v[146:147], v[146:147], v[184:185]
	v_pk_add_f32 v[148:149], v[148:149], v[184:185]
	v_pk_add_f32 v[150:151], v[150:151], v[184:185]
	v_rcp_f32_e32 v144, v144
	v_rcp_f32_e32 v145, v145
	v_rcp_f32_e32 v146, v146
	v_rcp_f32_e32 v147, v147
	v_rcp_f32_e32 v148, v148
	v_rcp_f32_e32 v149, v149
	v_rcp_f32_e32 v150, v150
	v_rcp_f32_e32 v151, v151
	s_nop 0
	v_pk_mul_f32 v[46:47], v[46:47], v[144:145]
	v_pk_mul_f32 v[48:49], v[48:49], v[146:147]
	v_pk_mul_f32 v[42:43], v[42:43], v[148:149]
	v_pk_mul_f32 v[44:45], v[44:45], v[150:151]
	v_cvt_pk_bf16_f32 v46, v46, v47
	v_cvt_pk_bf16_f32 v47, v48, v49
	v_cvt_pk_bf16_f32 v48, v42, v43
	v_cvt_pk_bf16_f32 v49, v44, v45
	v_pk_mul_f32 v[38:39], v[38:39], v[140:141] op_sel:[0,1] op_sel_hi:[1,1]
	v_pk_mul_f32 v[40:41], v[40:41], v[140:141] op_sel:[0,1] op_sel_hi:[1,1]
	v_pk_mul_f32 v[34:35], v[34:35], v[140:141] op_sel:[0,1] op_sel_hi:[1,1]
	v_pk_mul_f32 v[36:37], v[36:37], v[140:141] op_sel:[0,1] op_sel_hi:[1,1]
	v_pk_mul_f32 v[144:145], v[38:39], v[188:189]
	v_pk_mul_f32 v[146:147], v[40:41], v[188:189]
	v_pk_mul_f32 v[148:149], v[34:35], v[188:189]
	v_pk_mul_f32 v[150:151], v[36:37], v[188:189]
	v_pk_mul_f32 v[144:145], v[38:39], v[144:145]
	v_pk_mul_f32 v[146:147], v[40:41], v[146:147]
	v_pk_mul_f32 v[148:149], v[34:35], v[148:149]
	v_pk_mul_f32 v[150:151], v[36:37], v[150:151]
	v_pk_fma_f32 v[144:145], v[38:39], v[144:145], v[38:39]
	v_pk_fma_f32 v[146:147], v[40:41], v[146:147], v[40:41]
	v_pk_fma_f32 v[148:149], v[34:35], v[148:149], v[34:35]
	v_pk_fma_f32 v[150:151], v[36:37], v[150:151], v[36:37]
	v_pk_mul_f32 v[144:145], v[144:145], v[190:191]
	v_pk_mul_f32 v[146:147], v[146:147], v[190:191]
	v_pk_mul_f32 v[148:149], v[148:149], v[190:191]
	v_pk_mul_f32 v[150:151], v[150:151], v[190:191]
	v_pk_mul_f32 v[144:145], v[144:145], v[186:187]
	v_pk_mul_f32 v[146:147], v[146:147], v[186:187]
	v_pk_mul_f32 v[148:149], v[148:149], v[186:187]
	v_pk_mul_f32 v[150:151], v[150:151], v[186:187]
	v_exp_f32_e32 v144, v144
	v_exp_f32_e32 v145, v145
	v_exp_f32_e32 v146, v146
	v_exp_f32_e32 v147, v147
	v_exp_f32_e32 v148, v148
	v_exp_f32_e32 v149, v149
	v_exp_f32_e32 v150, v150
	v_exp_f32_e32 v151, v151
	s_nop 0
	v_pk_add_f32 v[144:145], v[144:145], v[184:185]
	v_pk_add_f32 v[146:147], v[146:147], v[184:185]
	v_pk_add_f32 v[148:149], v[148:149], v[184:185]
	v_pk_add_f32 v[150:151], v[150:151], v[184:185]
	v_rcp_f32_e32 v144, v144
	v_rcp_f32_e32 v145, v145
	v_rcp_f32_e32 v146, v146
	v_rcp_f32_e32 v147, v147
	v_rcp_f32_e32 v148, v148
	v_rcp_f32_e32 v149, v149
	v_rcp_f32_e32 v150, v150
	v_rcp_f32_e32 v151, v151
	s_nop 0
	v_pk_mul_f32 v[38:39], v[38:39], v[144:145]
	v_pk_mul_f32 v[40:41], v[40:41], v[146:147]
	v_pk_mul_f32 v[34:35], v[34:35], v[148:149]
	v_pk_mul_f32 v[36:37], v[36:37], v[150:151]
	v_cvt_pk_bf16_f32 v38, v38, v39
	v_cvt_pk_bf16_f32 v39, v40, v41
	v_cvt_pk_bf16_f32 v40, v34, v35
	v_cvt_pk_bf16_f32 v41, v36, v37
	v_mov_b32_e32 v158, v38
	v_mov_b32_e32 v159, v39
	v_mov_b32_e32 v160, v40
	v_mov_b32_e32 v161, v41
	v_mov_b32_dpp v38, v46 row_shl:8 row_mask:0xf bank_mask:0x3
	v_mov_b32_dpp v39, v47 row_shl:8 row_mask:0xf bank_mask:0x3
	v_mov_b32_dpp v40, v48 row_shl:8 row_mask:0xf bank_mask:0x3
	v_mov_b32_dpp v41, v49 row_shl:8 row_mask:0xf bank_mask:0x3
	v_mov_b32_dpp v46, v158 row_shr:8 row_mask:0xf bank_mask:0xc
	v_mov_b32_dpp v47, v159 row_shr:8 row_mask:0xf bank_mask:0xc
	v_mov_b32_dpp v48, v160 row_shr:8 row_mask:0xf bank_mask:0xc
	v_mov_b32_dpp v49, v161 row_shr:8 row_mask:0xf bank_mask:0xc
	s_mul_i32 s28, s22, 144
	v_lshl_add_u64 v[180:181], s[28:29], 0, v[178:179]
	global_store_dwordx4 v[180:181], v[46:49], off
	s_mul_i32 s28, s22, 152
	v_lshl_add_u64 v[180:181], s[28:29], 0, v[178:179]
	global_store_dwordx4 v[180:181], v[38:41], off
	v_pk_mul_f32 v[30:31], v[30:31], v[142:143] op_sel_hi:[1,0]
	v_pk_mul_f32 v[32:33], v[32:33], v[142:143] op_sel_hi:[1,0]
	v_pk_mul_f32 v[26:27], v[26:27], v[142:143] op_sel_hi:[1,0]
	v_pk_mul_f32 v[28:29], v[28:29], v[142:143] op_sel_hi:[1,0]
	v_pk_mul_f32 v[144:145], v[30:31], v[188:189]
	v_pk_mul_f32 v[146:147], v[32:33], v[188:189]
	v_pk_mul_f32 v[148:149], v[26:27], v[188:189]
	v_pk_mul_f32 v[150:151], v[28:29], v[188:189]
	v_pk_mul_f32 v[144:145], v[30:31], v[144:145]
	v_pk_mul_f32 v[146:147], v[32:33], v[146:147]
	v_pk_mul_f32 v[148:149], v[26:27], v[148:149]
	v_pk_mul_f32 v[150:151], v[28:29], v[150:151]
	v_pk_fma_f32 v[144:145], v[30:31], v[144:145], v[30:31]
	v_pk_fma_f32 v[146:147], v[32:33], v[146:147], v[32:33]
	v_pk_fma_f32 v[148:149], v[26:27], v[148:149], v[26:27]
	v_pk_fma_f32 v[150:151], v[28:29], v[150:151], v[28:29]
	v_pk_mul_f32 v[144:145], v[144:145], v[190:191]
	v_pk_mul_f32 v[146:147], v[146:147], v[190:191]
	v_pk_mul_f32 v[148:149], v[148:149], v[190:191]
	v_pk_mul_f32 v[150:151], v[150:151], v[190:191]
	v_pk_mul_f32 v[144:145], v[144:145], v[186:187]
	v_pk_mul_f32 v[146:147], v[146:147], v[186:187]
	v_pk_mul_f32 v[148:149], v[148:149], v[186:187]
	v_pk_mul_f32 v[150:151], v[150:151], v[186:187]
	v_exp_f32_e32 v144, v144
	v_exp_f32_e32 v145, v145
	v_exp_f32_e32 v146, v146
	v_exp_f32_e32 v147, v147
	v_exp_f32_e32 v148, v148
	v_exp_f32_e32 v149, v149
	v_exp_f32_e32 v150, v150
	v_exp_f32_e32 v151, v151
	s_nop 0
	v_pk_add_f32 v[144:145], v[144:145], v[184:185]
	v_pk_add_f32 v[146:147], v[146:147], v[184:185]
	v_pk_add_f32 v[148:149], v[148:149], v[184:185]
	v_pk_add_f32 v[150:151], v[150:151], v[184:185]
	v_rcp_f32_e32 v144, v144
	v_rcp_f32_e32 v145, v145
	v_rcp_f32_e32 v146, v146
	v_rcp_f32_e32 v147, v147
	v_rcp_f32_e32 v148, v148
	v_rcp_f32_e32 v149, v149
	v_rcp_f32_e32 v150, v150
	v_rcp_f32_e32 v151, v151
	s_nop 0
	v_pk_mul_f32 v[30:31], v[30:31], v[144:145]
	v_pk_mul_f32 v[32:33], v[32:33], v[146:147]
	v_pk_mul_f32 v[26:27], v[26:27], v[148:149]
	v_pk_mul_f32 v[28:29], v[28:29], v[150:151]
	v_cvt_pk_bf16_f32 v30, v30, v31
	v_cvt_pk_bf16_f32 v31, v32, v33
	v_cvt_pk_bf16_f32 v32, v26, v27
	v_cvt_pk_bf16_f32 v33, v28, v29
	v_pk_mul_f32 v[22:23], v[22:23], v[142:143] op_sel_hi:[1,0]
	v_pk_mul_f32 v[24:25], v[24:25], v[142:143] op_sel_hi:[1,0]
	v_pk_mul_f32 v[18:19], v[18:19], v[142:143] op_sel_hi:[1,0]
	v_pk_mul_f32 v[20:21], v[20:21], v[142:143] op_sel_hi:[1,0]
	v_pk_mul_f32 v[144:145], v[22:23], v[188:189]
	v_pk_mul_f32 v[146:147], v[24:25], v[188:189]
	v_pk_mul_f32 v[148:149], v[18:19], v[188:189]
	v_pk_mul_f32 v[150:151], v[20:21], v[188:189]
	v_pk_mul_f32 v[144:145], v[22:23], v[144:145]
	v_pk_mul_f32 v[146:147], v[24:25], v[146:147]
	v_pk_mul_f32 v[148:149], v[18:19], v[148:149]
	v_pk_mul_f32 v[150:151], v[20:21], v[150:151]
	v_pk_fma_f32 v[144:145], v[22:23], v[144:145], v[22:23]
	v_pk_fma_f32 v[146:147], v[24:25], v[146:147], v[24:25]
	v_pk_fma_f32 v[148:149], v[18:19], v[148:149], v[18:19]
	v_pk_fma_f32 v[150:151], v[20:21], v[150:151], v[20:21]
	v_pk_mul_f32 v[144:145], v[144:145], v[190:191]
	v_pk_mul_f32 v[146:147], v[146:147], v[190:191]
	v_pk_mul_f32 v[148:149], v[148:149], v[190:191]
	v_pk_mul_f32 v[150:151], v[150:151], v[190:191]
	v_pk_mul_f32 v[144:145], v[144:145], v[186:187]
	v_pk_mul_f32 v[146:147], v[146:147], v[186:187]
	v_pk_mul_f32 v[148:149], v[148:149], v[186:187]
	v_pk_mul_f32 v[150:151], v[150:151], v[186:187]
	v_exp_f32_e32 v144, v144
	v_exp_f32_e32 v145, v145
	v_exp_f32_e32 v146, v146
	v_exp_f32_e32 v147, v147
	v_exp_f32_e32 v148, v148
	v_exp_f32_e32 v149, v149
	v_exp_f32_e32 v150, v150
	v_exp_f32_e32 v151, v151
	s_nop 0
	v_pk_add_f32 v[144:145], v[144:145], v[184:185]
	v_pk_add_f32 v[146:147], v[146:147], v[184:185]
	v_pk_add_f32 v[148:149], v[148:149], v[184:185]
	v_pk_add_f32 v[150:151], v[150:151], v[184:185]
	v_rcp_f32_e32 v144, v144
	v_rcp_f32_e32 v145, v145
	v_rcp_f32_e32 v146, v146
	v_rcp_f32_e32 v147, v147
	v_rcp_f32_e32 v148, v148
	v_rcp_f32_e32 v149, v149
	v_rcp_f32_e32 v150, v150
	v_rcp_f32_e32 v151, v151
	s_nop 0
	v_pk_mul_f32 v[22:23], v[22:23], v[144:145]
	v_pk_mul_f32 v[24:25], v[24:25], v[146:147]
	v_pk_mul_f32 v[18:19], v[18:19], v[148:149]
	v_pk_mul_f32 v[20:21], v[20:21], v[150:151]
	v_cvt_pk_bf16_f32 v22, v22, v23
	v_cvt_pk_bf16_f32 v23, v24, v25
	v_cvt_pk_bf16_f32 v24, v18, v19
	v_cvt_pk_bf16_f32 v25, v20, v21
	v_mov_b32_e32 v158, v22
	v_mov_b32_e32 v159, v23
	v_mov_b32_e32 v160, v24
	v_mov_b32_e32 v161, v25
	v_mov_b32_dpp v22, v30 row_shl:8 row_mask:0xf bank_mask:0x3
	v_mov_b32_dpp v23, v31 row_shl:8 row_mask:0xf bank_mask:0x3
	v_mov_b32_dpp v24, v32 row_shl:8 row_mask:0xf bank_mask:0x3
	v_mov_b32_dpp v25, v33 row_shl:8 row_mask:0xf bank_mask:0x3
	v_mov_b32_dpp v30, v158 row_shr:8 row_mask:0xf bank_mask:0xc
	v_mov_b32_dpp v31, v159 row_shr:8 row_mask:0xf bank_mask:0xc
	v_mov_b32_dpp v32, v160 row_shr:8 row_mask:0xf bank_mask:0xc
	v_mov_b32_dpp v33, v161 row_shr:8 row_mask:0xf bank_mask:0xc
	s_mul_i32 s28, s22, 160
	v_lshl_add_u64 v[180:181], s[28:29], 0, v[178:179]
	global_store_dwordx4 v[180:181], v[30:33], off
	s_mul_i32 s28, s22, 168
	v_lshl_add_u64 v[180:181], s[28:29], 0, v[178:179]
	global_store_dwordx4 v[180:181], v[22:25], off
	v_pk_mul_f32 v[14:15], v[14:15], v[142:143] op_sel:[0,1] op_sel_hi:[1,1]
	v_pk_mul_f32 v[16:17], v[16:17], v[142:143] op_sel:[0,1] op_sel_hi:[1,1]
	v_pk_mul_f32 v[10:11], v[10:11], v[142:143] op_sel:[0,1] op_sel_hi:[1,1]
	v_pk_mul_f32 v[12:13], v[12:13], v[142:143] op_sel:[0,1] op_sel_hi:[1,1]
	v_pk_mul_f32 v[144:145], v[14:15], v[188:189]
	v_pk_mul_f32 v[146:147], v[16:17], v[188:189]
	v_pk_mul_f32 v[148:149], v[10:11], v[188:189]
	v_pk_mul_f32 v[150:151], v[12:13], v[188:189]
	v_pk_mul_f32 v[144:145], v[14:15], v[144:145]
	v_pk_mul_f32 v[146:147], v[16:17], v[146:147]
	v_pk_mul_f32 v[148:149], v[10:11], v[148:149]
	v_pk_mul_f32 v[150:151], v[12:13], v[150:151]
	v_pk_fma_f32 v[144:145], v[14:15], v[144:145], v[14:15]
	v_pk_fma_f32 v[146:147], v[16:17], v[146:147], v[16:17]
	v_pk_fma_f32 v[148:149], v[10:11], v[148:149], v[10:11]
	v_pk_fma_f32 v[150:151], v[12:13], v[150:151], v[12:13]
	v_pk_mul_f32 v[144:145], v[144:145], v[190:191]
	v_pk_mul_f32 v[146:147], v[146:147], v[190:191]
	v_pk_mul_f32 v[148:149], v[148:149], v[190:191]
	v_pk_mul_f32 v[150:151], v[150:151], v[190:191]
	v_pk_mul_f32 v[144:145], v[144:145], v[186:187]
	v_pk_mul_f32 v[146:147], v[146:147], v[186:187]
	v_pk_mul_f32 v[148:149], v[148:149], v[186:187]
	v_pk_mul_f32 v[150:151], v[150:151], v[186:187]
	v_exp_f32_e32 v144, v144
	v_exp_f32_e32 v145, v145
	v_exp_f32_e32 v146, v146
	v_exp_f32_e32 v147, v147
	v_exp_f32_e32 v148, v148
	v_exp_f32_e32 v149, v149
	v_exp_f32_e32 v150, v150
	v_exp_f32_e32 v151, v151
	s_nop 0
	v_pk_add_f32 v[144:145], v[144:145], v[184:185]
	v_pk_add_f32 v[146:147], v[146:147], v[184:185]
	v_pk_add_f32 v[148:149], v[148:149], v[184:185]
	v_pk_add_f32 v[150:151], v[150:151], v[184:185]
	v_rcp_f32_e32 v144, v144
	v_rcp_f32_e32 v145, v145
	v_rcp_f32_e32 v146, v146
	v_rcp_f32_e32 v147, v147
	v_rcp_f32_e32 v148, v148
	v_rcp_f32_e32 v149, v149
	v_rcp_f32_e32 v150, v150
	v_rcp_f32_e32 v151, v151
	s_nop 0
	v_pk_mul_f32 v[14:15], v[14:15], v[144:145]
	v_pk_mul_f32 v[16:17], v[16:17], v[146:147]
	v_pk_mul_f32 v[10:11], v[10:11], v[148:149]
	v_pk_mul_f32 v[12:13], v[12:13], v[150:151]
	v_cvt_pk_bf16_f32 v14, v14, v15
	v_cvt_pk_bf16_f32 v15, v16, v17
	v_cvt_pk_bf16_f32 v16, v10, v11
	v_cvt_pk_bf16_f32 v17, v12, v13
	v_pk_mul_f32 v[6:7], v[6:7], v[142:143] op_sel:[0,1] op_sel_hi:[1,1]
	v_pk_mul_f32 v[8:9], v[8:9], v[142:143] op_sel:[0,1] op_sel_hi:[1,1]
	v_pk_mul_f32 v[2:3], v[2:3], v[142:143] op_sel:[0,1] op_sel_hi:[1,1]
	v_pk_mul_f32 v[4:5], v[4:5], v[142:143] op_sel:[0,1] op_sel_hi:[1,1]
	v_pk_mul_f32 v[144:145], v[6:7], v[188:189]
	v_pk_mul_f32 v[146:147], v[8:9], v[188:189]
	v_pk_mul_f32 v[148:149], v[2:3], v[188:189]
	v_pk_mul_f32 v[150:151], v[4:5], v[188:189]
	v_pk_mul_f32 v[144:145], v[6:7], v[144:145]
	v_pk_mul_f32 v[146:147], v[8:9], v[146:147]
	v_pk_mul_f32 v[148:149], v[2:3], v[148:149]
	v_pk_mul_f32 v[150:151], v[4:5], v[150:151]
	v_pk_fma_f32 v[144:145], v[6:7], v[144:145], v[6:7]
	v_pk_fma_f32 v[146:147], v[8:9], v[146:147], v[8:9]
	v_pk_fma_f32 v[148:149], v[2:3], v[148:149], v[2:3]
	v_pk_fma_f32 v[150:151], v[4:5], v[150:151], v[4:5]
	v_pk_mul_f32 v[144:145], v[144:145], v[190:191]
	v_pk_mul_f32 v[146:147], v[146:147], v[190:191]
	v_pk_mul_f32 v[148:149], v[148:149], v[190:191]
	v_pk_mul_f32 v[150:151], v[150:151], v[190:191]
	v_pk_mul_f32 v[144:145], v[144:145], v[186:187]
	v_pk_mul_f32 v[146:147], v[146:147], v[186:187]
	v_pk_mul_f32 v[148:149], v[148:149], v[186:187]
	v_pk_mul_f32 v[150:151], v[150:151], v[186:187]
	v_exp_f32_e32 v144, v144
	v_exp_f32_e32 v145, v145
	v_exp_f32_e32 v146, v146
	v_exp_f32_e32 v147, v147
	v_exp_f32_e32 v148, v148
	v_exp_f32_e32 v149, v149
	v_exp_f32_e32 v150, v150
	v_exp_f32_e32 v151, v151
	s_nop 0
	v_pk_add_f32 v[144:145], v[144:145], v[184:185]
	v_pk_add_f32 v[146:147], v[146:147], v[184:185]
	v_pk_add_f32 v[148:149], v[148:149], v[184:185]
	v_pk_add_f32 v[150:151], v[150:151], v[184:185]
	v_rcp_f32_e32 v144, v144
	v_rcp_f32_e32 v145, v145
	v_rcp_f32_e32 v146, v146
	v_rcp_f32_e32 v147, v147
	v_rcp_f32_e32 v148, v148
	v_rcp_f32_e32 v149, v149
	v_rcp_f32_e32 v150, v150
	v_rcp_f32_e32 v151, v151
	s_nop 0
	v_pk_mul_f32 v[6:7], v[6:7], v[144:145]
	v_pk_mul_f32 v[8:9], v[8:9], v[146:147]
	v_pk_mul_f32 v[2:3], v[2:3], v[148:149]
	v_pk_mul_f32 v[4:5], v[4:5], v[150:151]
	v_cvt_pk_bf16_f32 v6, v6, v7
	v_cvt_pk_bf16_f32 v7, v8, v9
	v_cvt_pk_bf16_f32 v8, v2, v3
	v_cvt_pk_bf16_f32 v9, v4, v5
	v_mov_b32_e32 v158, v6
	v_mov_b32_e32 v159, v7
	v_mov_b32_e32 v160, v8
	v_mov_b32_e32 v161, v9
	v_mov_b32_dpp v6, v14 row_shl:8 row_mask:0xf bank_mask:0x3
	v_mov_b32_dpp v7, v15 row_shl:8 row_mask:0xf bank_mask:0x3
	v_mov_b32_dpp v8, v16 row_shl:8 row_mask:0xf bank_mask:0x3
	v_mov_b32_dpp v9, v17 row_shl:8 row_mask:0xf bank_mask:0x3
	v_mov_b32_dpp v14, v158 row_shr:8 row_mask:0xf bank_mask:0xc
	v_mov_b32_dpp v15, v159 row_shr:8 row_mask:0xf bank_mask:0xc
	v_mov_b32_dpp v16, v160 row_shr:8 row_mask:0xf bank_mask:0xc
	v_mov_b32_dpp v17, v161 row_shr:8 row_mask:0xf bank_mask:0xc
	s_mul_i32 s28, s22, 176
	v_lshl_add_u64 v[180:181], s[28:29], 0, v[178:179]
	global_store_dwordx4 v[180:181], v[14:17], off
	s_mul_i32 s28, s22, 184
	v_lshl_add_u64 v[180:181], s[28:29], 0, v[178:179]
	global_store_dwordx4 v[180:181], v[6:9], off
	s_branch .Lpj_done
.Lpj_sigm:
	v_pk_mul_f32 v[126:127], v[126:127], v[136:137] op_sel_hi:[1,0]
	v_pk_mul_f32 v[128:129], v[128:129], v[136:137] op_sel_hi:[1,0]
	v_pk_mul_f32 v[122:123], v[122:123], v[136:137] op_sel_hi:[1,0]
	v_pk_mul_f32 v[124:125], v[124:125], v[136:137] op_sel_hi:[1,0]
	v_pk_mul_f32 v[144:145], v[126:127], v[186:187]
	v_pk_mul_f32 v[146:147], v[128:129], v[186:187]
	v_pk_mul_f32 v[148:149], v[122:123], v[186:187]
	v_pk_mul_f32 v[150:151], v[124:125], v[186:187]
	v_exp_f32_e32 v144, v144
	v_exp_f32_e32 v145, v145
	v_exp_f32_e32 v146, v146
	v_exp_f32_e32 v147, v147
	v_exp_f32_e32 v148, v148
	v_exp_f32_e32 v149, v149
	v_exp_f32_e32 v150, v150
	v_exp_f32_e32 v151, v151
	s_nop 0
	v_pk_add_f32 v[144:145], v[144:145], v[184:185]
	v_pk_add_f32 v[146:147], v[146:147], v[184:185]
	v_pk_add_f32 v[148:149], v[148:149], v[184:185]
	v_pk_add_f32 v[150:151], v[150:151], v[184:185]
	v_rcp_f32_e32 v144, v144
	v_rcp_f32_e32 v145, v145
	v_rcp_f32_e32 v146, v146
	v_rcp_f32_e32 v147, v147
	v_rcp_f32_e32 v148, v148
	v_rcp_f32_e32 v149, v149
	v_rcp_f32_e32 v150, v150
	v_rcp_f32_e32 v151, v151
	s_nop 0
	v_cvt_pk_bf16_f32 v126, v144, v145
	v_cvt_pk_bf16_f32 v127, v146, v147
	v_cvt_pk_bf16_f32 v128, v148, v149
	v_cvt_pk_bf16_f32 v129, v150, v151
	v_pk_mul_f32 v[118:119], v[118:119], v[136:137] op_sel_hi:[1,0]
	v_pk_mul_f32 v[120:121], v[120:121], v[136:137] op_sel_hi:[1,0]
	v_pk_mul_f32 v[114:115], v[114:115], v[136:137] op_sel_hi:[1,0]
	v_pk_mul_f32 v[116:117], v[116:117], v[136:137] op_sel_hi:[1,0]
	v_pk_mul_f32 v[144:145], v[118:119], v[186:187]
	v_pk_mul_f32 v[146:147], v[120:121], v[186:187]
	v_pk_mul_f32 v[148:149], v[114:115], v[186:187]
	v_pk_mul_f32 v[150:151], v[116:117], v[186:187]
	v_exp_f32_e32 v144, v144
	v_exp_f32_e32 v145, v145
	v_exp_f32_e32 v146, v146
	v_exp_f32_e32 v147, v147
	v_exp_f32_e32 v148, v148
	v_exp_f32_e32 v149, v149
	v_exp_f32_e32 v150, v150
	v_exp_f32_e32 v151, v151
	s_nop 0
	v_pk_add_f32 v[144:145], v[144:145], v[184:185]
	v_pk_add_f32 v[146:147], v[146:147], v[184:185]
	v_pk_add_f32 v[148:149], v[148:149], v[184:185]
	v_pk_add_f32 v[150:151], v[150:151], v[184:185]
	v_rcp_f32_e32 v144, v144
	v_rcp_f32_e32 v145, v145
	v_rcp_f32_e32 v146, v146
	v_rcp_f32_e32 v147, v147
	v_rcp_f32_e32 v148, v148
	v_rcp_f32_e32 v149, v149
	v_rcp_f32_e32 v150, v150
	v_rcp_f32_e32 v151, v151
	s_nop 0
	v_cvt_pk_bf16_f32 v118, v144, v145
	v_cvt_pk_bf16_f32 v119, v146, v147
	v_cvt_pk_bf16_f32 v120, v148, v149
	v_cvt_pk_bf16_f32 v121, v150, v151
	v_mov_b32_e32 v158, v118
	v_mov_b32_e32 v159, v119
	v_mov_b32_e32 v160, v120
	v_mov_b32_e32 v161, v121
	v_mov_b32_dpp v118, v126 row_shl:8 row_mask:0xf bank_mask:0x3
	v_mov_b32_dpp v119, v127 row_shl:8 row_mask:0xf bank_mask:0x3
	v_mov_b32_dpp v120, v128 row_shl:8 row_mask:0xf bank_mask:0x3
	v_mov_b32_dpp v121, v129 row_shl:8 row_mask:0xf bank_mask:0x3
	v_mov_b32_dpp v126, v158 row_shr:8 row_mask:0xf bank_mask:0xc
	v_mov_b32_dpp v127, v159 row_shr:8 row_mask:0xf bank_mask:0xc
	v_mov_b32_dpp v128, v160 row_shr:8 row_mask:0xf bank_mask:0xc
	v_mov_b32_dpp v129, v161 row_shr:8 row_mask:0xf bank_mask:0xc
	s_mul_i32 s28, s22, 0
	v_lshl_add_u64 v[180:181], s[28:29], 0, v[178:179]
	global_store_dwordx4 v[180:181], v[126:129], off
	s_mul_i32 s28, s22, 8
	v_lshl_add_u64 v[180:181], s[28:29], 0, v[178:179]
	global_store_dwordx4 v[180:181], v[118:121], off
	v_pk_mul_f32 v[110:111], v[110:111], v[136:137] op_sel:[0,1] op_sel_hi:[1,1]
	v_pk_mul_f32 v[112:113], v[112:113], v[136:137] op_sel:[0,1] op_sel_hi:[1,1]
	v_pk_mul_f32 v[106:107], v[106:107], v[136:137] op_sel:[0,1] op_sel_hi:[1,1]
	v_pk_mul_f32 v[108:109], v[108:109], v[136:137] op_sel:[0,1] op_sel_hi:[1,1]
	v_pk_mul_f32 v[144:145], v[110:111], v[186:187]
	v_pk_mul_f32 v[146:147], v[112:113], v[186:187]
	v_pk_mul_f32 v[148:149], v[106:107], v[186:187]
	v_pk_mul_f32 v[150:151], v[108:109], v[186:187]
	v_exp_f32_e32 v144, v144
	v_exp_f32_e32 v145, v145
	v_exp_f32_e32 v146, v146
	v_exp_f32_e32 v147, v147
	v_exp_f32_e32 v148, v148
	v_exp_f32_e32 v149, v149
	v_exp_f32_e32 v150, v150
	v_exp_f32_e32 v151, v151
	s_nop 0
	v_pk_add_f32 v[144:145], v[144:145], v[184:185]
	v_pk_add_f32 v[146:147], v[146:147], v[184:185]
	v_pk_add_f32 v[148:149], v[148:149], v[184:185]
	v_pk_add_f32 v[150:151], v[150:151], v[184:185]
	v_rcp_f32_e32 v144, v144
	v_rcp_f32_e32 v145, v145
	v_rcp_f32_e32 v146, v146
	v_rcp_f32_e32 v147, v147
	v_rcp_f32_e32 v148, v148
	v_rcp_f32_e32 v149, v149
	v_rcp_f32_e32 v150, v150
	v_rcp_f32_e32 v151, v151
	s_nop 0
	v_cvt_pk_bf16_f32 v110, v144, v145
	v_cvt_pk_bf16_f32 v111, v146, v147
	v_cvt_pk_bf16_f32 v112, v148, v149
	v_cvt_pk_bf16_f32 v113, v150, v151
	v_pk_mul_f32 v[102:103], v[102:103], v[136:137] op_sel:[0,1] op_sel_hi:[1,1]
	v_pk_mul_f32 v[104:105], v[104:105], v[136:137] op_sel:[0,1] op_sel_hi:[1,1]
	v_pk_mul_f32 v[98:99], v[98:99], v[136:137] op_sel:[0,1] op_sel_hi:[1,1]
	v_pk_mul_f32 v[100:101], v[100:101], v[136:137] op_sel:[0,1] op_sel_hi:[1,1]
	v_pk_mul_f32 v[144:145], v[102:103], v[186:187]
	v_pk_mul_f32 v[146:147], v[104:105], v[186:187]
	v_pk_mul_f32 v[148:149], v[98:99], v[186:187]
	v_pk_mul_f32 v[150:151], v[100:101], v[186:187]
	v_exp_f32_e32 v144, v144
	v_exp_f32_e32 v145, v145
	v_exp_f32_e32 v146, v146
	v_exp_f32_e32 v147, v147
	v_exp_f32_e32 v148, v148
	v_exp_f32_e32 v149, v149
	v_exp_f32_e32 v150, v150
	v_exp_f32_e32 v151, v151
	s_nop 0
	v_pk_add_f32 v[144:145], v[144:145], v[184:185]
	v_pk_add_f32 v[146:147], v[146:147], v[184:185]
	v_pk_add_f32 v[148:149], v[148:149], v[184:185]
	v_pk_add_f32 v[150:151], v[150:151], v[184:185]
	v_rcp_f32_e32 v144, v144
	v_rcp_f32_e32 v145, v145
	v_rcp_f32_e32 v146, v146
	v_rcp_f32_e32 v147, v147
	v_rcp_f32_e32 v148, v148
	v_rcp_f32_e32 v149, v149
	v_rcp_f32_e32 v150, v150
	v_rcp_f32_e32 v151, v151
	s_nop 0
	v_cvt_pk_bf16_f32 v102, v144, v145
	v_cvt_pk_bf16_f32 v103, v146, v147
	v_cvt_pk_bf16_f32 v104, v148, v149
	v_cvt_pk_bf16_f32 v105, v150, v151
	v_mov_b32_e32 v158, v102
	v_mov_b32_e32 v159, v103
	v_mov_b32_e32 v160, v104
	v_mov_b32_e32 v161, v105
	v_mov_b32_dpp v102, v110 row_shl:8 row_mask:0xf bank_mask:0x3
	v_mov_b32_dpp v103, v111 row_shl:8 row_mask:0xf bank_mask:0x3
	v_mov_b32_dpp v104, v112 row_shl:8 row_mask:0xf bank_mask:0x3
	v_mov_b32_dpp v105, v113 row_shl:8 row_mask:0xf bank_mask:0x3
	v_mov_b32_dpp v110, v158 row_shr:8 row_mask:0xf bank_mask:0xc
	v_mov_b32_dpp v111, v159 row_shr:8 row_mask:0xf bank_mask:0xc
	v_mov_b32_dpp v112, v160 row_shr:8 row_mask:0xf bank_mask:0xc
	v_mov_b32_dpp v113, v161 row_shr:8 row_mask:0xf bank_mask:0xc
	s_mul_i32 s28, s22, 16
	v_lshl_add_u64 v[180:181], s[28:29], 0, v[178:179]
	global_store_dwordx4 v[180:181], v[110:113], off
	s_mul_i32 s28, s22, 24
	v_lshl_add_u64 v[180:181], s[28:29], 0, v[178:179]
	global_store_dwordx4 v[180:181], v[102:105], off
	v_pk_mul_f32 v[94:95], v[94:95], v[138:139] op_sel_hi:[1,0]
	v_pk_mul_f32 v[96:97], v[96:97], v[138:139] op_sel_hi:[1,0]
	v_pk_mul_f32 v[90:91], v[90:91], v[138:139] op_sel_hi:[1,0]
	v_pk_mul_f32 v[92:93], v[92:93], v[138:139] op_sel_hi:[1,0]
	v_pk_mul_f32 v[144:145], v[94:95], v[186:187]
	v_pk_mul_f32 v[146:147], v[96:97], v[186:187]
	v_pk_mul_f32 v[148:149], v[90:91], v[186:187]
	v_pk_mul_f32 v[150:151], v[92:93], v[186:187]
	v_exp_f32_e32 v144, v144
	v_exp_f32_e32 v145, v145
	v_exp_f32_e32 v146, v146
	v_exp_f32_e32 v147, v147
	v_exp_f32_e32 v148, v148
	v_exp_f32_e32 v149, v149
	v_exp_f32_e32 v150, v150
	v_exp_f32_e32 v151, v151
	s_nop 0
	v_pk_add_f32 v[144:145], v[144:145], v[184:185]
	v_pk_add_f32 v[146:147], v[146:147], v[184:185]
	v_pk_add_f32 v[148:149], v[148:149], v[184:185]
	v_pk_add_f32 v[150:151], v[150:151], v[184:185]
	v_rcp_f32_e32 v144, v144
	v_rcp_f32_e32 v145, v145
	v_rcp_f32_e32 v146, v146
	v_rcp_f32_e32 v147, v147
	v_rcp_f32_e32 v148, v148
	v_rcp_f32_e32 v149, v149
	v_rcp_f32_e32 v150, v150
	v_rcp_f32_e32 v151, v151
	s_nop 0
	v_cvt_pk_bf16_f32 v94, v144, v145
	v_cvt_pk_bf16_f32 v95, v146, v147
	v_cvt_pk_bf16_f32 v96, v148, v149
	v_cvt_pk_bf16_f32 v97, v150, v151
	v_pk_mul_f32 v[86:87], v[86:87], v[138:139] op_sel_hi:[1,0]
	v_pk_mul_f32 v[88:89], v[88:89], v[138:139] op_sel_hi:[1,0]
	v_pk_mul_f32 v[82:83], v[82:83], v[138:139] op_sel_hi:[1,0]
	v_pk_mul_f32 v[84:85], v[84:85], v[138:139] op_sel_hi:[1,0]
	v_pk_mul_f32 v[144:145], v[86:87], v[186:187]
	v_pk_mul_f32 v[146:147], v[88:89], v[186:187]
	v_pk_mul_f32 v[148:149], v[82:83], v[186:187]
	v_pk_mul_f32 v[150:151], v[84:85], v[186:187]
	v_exp_f32_e32 v144, v144
	v_exp_f32_e32 v145, v145
	v_exp_f32_e32 v146, v146
	v_exp_f32_e32 v147, v147
	v_exp_f32_e32 v148, v148
	v_exp_f32_e32 v149, v149
	v_exp_f32_e32 v150, v150
	v_exp_f32_e32 v151, v151
	s_nop 0
	v_pk_add_f32 v[144:145], v[144:145], v[184:185]
	v_pk_add_f32 v[146:147], v[146:147], v[184:185]
	v_pk_add_f32 v[148:149], v[148:149], v[184:185]
	v_pk_add_f32 v[150:151], v[150:151], v[184:185]
	v_rcp_f32_e32 v144, v144
	v_rcp_f32_e32 v145, v145
	v_rcp_f32_e32 v146, v146
	v_rcp_f32_e32 v147, v147
	v_rcp_f32_e32 v148, v148
	v_rcp_f32_e32 v149, v149
	v_rcp_f32_e32 v150, v150
	v_rcp_f32_e32 v151, v151
	s_nop 0
	v_cvt_pk_bf16_f32 v86, v144, v145
	v_cvt_pk_bf16_f32 v87, v146, v147
	v_cvt_pk_bf16_f32 v88, v148, v149
	v_cvt_pk_bf16_f32 v89, v150, v151
	v_mov_b32_e32 v158, v86
	v_mov_b32_e32 v159, v87
	v_mov_b32_e32 v160, v88
	v_mov_b32_e32 v161, v89
	v_mov_b32_dpp v86, v94 row_shl:8 row_mask:0xf bank_mask:0x3
	v_mov_b32_dpp v87, v95 row_shl:8 row_mask:0xf bank_mask:0x3
	v_mov_b32_dpp v88, v96 row_shl:8 row_mask:0xf bank_mask:0x3
	v_mov_b32_dpp v89, v97 row_shl:8 row_mask:0xf bank_mask:0x3
	v_mov_b32_dpp v94, v158 row_shr:8 row_mask:0xf bank_mask:0xc
	v_mov_b32_dpp v95, v159 row_shr:8 row_mask:0xf bank_mask:0xc
	v_mov_b32_dpp v96, v160 row_shr:8 row_mask:0xf bank_mask:0xc
	v_mov_b32_dpp v97, v161 row_shr:8 row_mask:0xf bank_mask:0xc
	s_mul_i32 s28, s22, 32
	v_lshl_add_u64 v[180:181], s[28:29], 0, v[178:179]
	global_store_dwordx4 v[180:181], v[94:97], off
	s_mul_i32 s28, s22, 40
	v_lshl_add_u64 v[180:181], s[28:29], 0, v[178:179]
	global_store_dwordx4 v[180:181], v[86:89], off
	v_pk_mul_f32 v[78:79], v[78:79], v[138:139] op_sel:[0,1] op_sel_hi:[1,1]
	v_pk_mul_f32 v[80:81], v[80:81], v[138:139] op_sel:[0,1] op_sel_hi:[1,1]
	v_pk_mul_f32 v[74:75], v[74:75], v[138:139] op_sel:[0,1] op_sel_hi:[1,1]
	v_pk_mul_f32 v[76:77], v[76:77], v[138:139] op_sel:[0,1] op_sel_hi:[1,1]
	v_pk_mul_f32 v[144:145], v[78:79], v[186:187]
	v_pk_mul_f32 v[146:147], v[80:81], v[186:187]
	v_pk_mul_f32 v[148:149], v[74:75], v[186:187]
	v_pk_mul_f32 v[150:151], v[76:77], v[186:187]
	v_exp_f32_e32 v144, v144
	v_exp_f32_e32 v145, v145
	v_exp_f32_e32 v146, v146
	v_exp_f32_e32 v147, v147
	v_exp_f32_e32 v148, v148
	v_exp_f32_e32 v149, v149
	v_exp_f32_e32 v150, v150
	v_exp_f32_e32 v151, v151
	s_nop 0
	v_pk_add_f32 v[144:145], v[144:145], v[184:185]
	v_pk_add_f32 v[146:147], v[146:147], v[184:185]
	v_pk_add_f32 v[148:149], v[148:149], v[184:185]
	v_pk_add_f32 v[150:151], v[150:151], v[184:185]
	v_rcp_f32_e32 v144, v144
	v_rcp_f32_e32 v145, v145
	v_rcp_f32_e32 v146, v146
	v_rcp_f32_e32 v147, v147
	v_rcp_f32_e32 v148, v148
	v_rcp_f32_e32 v149, v149
	v_rcp_f32_e32 v150, v150
	v_rcp_f32_e32 v151, v151
	s_nop 0
	v_cvt_pk_bf16_f32 v78, v144, v145
	v_cvt_pk_bf16_f32 v79, v146, v147
	v_cvt_pk_bf16_f32 v80, v148, v149
	v_cvt_pk_bf16_f32 v81, v150, v151
	v_pk_mul_f32 v[70:71], v[70:71], v[138:139] op_sel:[0,1] op_sel_hi:[1,1]
	v_pk_mul_f32 v[72:73], v[72:73], v[138:139] op_sel:[0,1] op_sel_hi:[1,1]
	v_pk_mul_f32 v[66:67], v[66:67], v[138:139] op_sel:[0,1] op_sel_hi:[1,1]
	v_pk_mul_f32 v[68:69], v[68:69], v[138:139] op_sel:[0,1] op_sel_hi:[1,1]
	v_pk_mul_f32 v[144:145], v[70:71], v[186:187]
	v_pk_mul_f32 v[146:147], v[72:73], v[186:187]
	v_pk_mul_f32 v[148:149], v[66:67], v[186:187]
	v_pk_mul_f32 v[150:151], v[68:69], v[186:187]
	v_exp_f32_e32 v144, v144
	v_exp_f32_e32 v145, v145
	v_exp_f32_e32 v146, v146
	v_exp_f32_e32 v147, v147
	v_exp_f32_e32 v148, v148
	v_exp_f32_e32 v149, v149
	v_exp_f32_e32 v150, v150
	v_exp_f32_e32 v151, v151
	s_nop 0
	v_pk_add_f32 v[144:145], v[144:145], v[184:185]
	v_pk_add_f32 v[146:147], v[146:147], v[184:185]
	v_pk_add_f32 v[148:149], v[148:149], v[184:185]
	v_pk_add_f32 v[150:151], v[150:151], v[184:185]
	v_rcp_f32_e32 v144, v144
	v_rcp_f32_e32 v145, v145
	v_rcp_f32_e32 v146, v146
	v_rcp_f32_e32 v147, v147
	v_rcp_f32_e32 v148, v148
	v_rcp_f32_e32 v149, v149
	v_rcp_f32_e32 v150, v150
	v_rcp_f32_e32 v151, v151
	s_nop 0
	v_cvt_pk_bf16_f32 v70, v144, v145
	v_cvt_pk_bf16_f32 v71, v146, v147
	v_cvt_pk_bf16_f32 v72, v148, v149
	v_cvt_pk_bf16_f32 v73, v150, v151
	v_mov_b32_e32 v158, v70
	v_mov_b32_e32 v159, v71
	v_mov_b32_e32 v160, v72
	v_mov_b32_e32 v161, v73
	v_mov_b32_dpp v70, v78 row_shl:8 row_mask:0xf bank_mask:0x3
	v_mov_b32_dpp v71, v79 row_shl:8 row_mask:0xf bank_mask:0x3
	v_mov_b32_dpp v72, v80 row_shl:8 row_mask:0xf bank_mask:0x3
	v_mov_b32_dpp v73, v81 row_shl:8 row_mask:0xf bank_mask:0x3
	v_mov_b32_dpp v78, v158 row_shr:8 row_mask:0xf bank_mask:0xc
	v_mov_b32_dpp v79, v159 row_shr:8 row_mask:0xf bank_mask:0xc
	v_mov_b32_dpp v80, v160 row_shr:8 row_mask:0xf bank_mask:0xc
	v_mov_b32_dpp v81, v161 row_shr:8 row_mask:0xf bank_mask:0xc
	s_mul_i32 s28, s22, 48
	v_lshl_add_u64 v[180:181], s[28:29], 0, v[178:179]
	global_store_dwordx4 v[180:181], v[78:81], off
	s_mul_i32 s28, s22, 56
	v_lshl_add_u64 v[180:181], s[28:29], 0, v[178:179]
	global_store_dwordx4 v[180:181], v[70:73], off
	v_pk_mul_f32 v[62:63], v[62:63], v[140:141] op_sel_hi:[1,0]
	v_pk_mul_f32 v[64:65], v[64:65], v[140:141] op_sel_hi:[1,0]
	v_pk_mul_f32 v[58:59], v[58:59], v[140:141] op_sel_hi:[1,0]
	v_pk_mul_f32 v[60:61], v[60:61], v[140:141] op_sel_hi:[1,0]
	v_pk_mul_f32 v[144:145], v[62:63], v[186:187]
	v_pk_mul_f32 v[146:147], v[64:65], v[186:187]
	v_pk_mul_f32 v[148:149], v[58:59], v[186:187]
	v_pk_mul_f32 v[150:151], v[60:61], v[186:187]
	v_exp_f32_e32 v144, v144
	v_exp_f32_e32 v145, v145
	v_exp_f32_e32 v146, v146
	v_exp_f32_e32 v147, v147
	v_exp_f32_e32 v148, v148
	v_exp_f32_e32 v149, v149
	v_exp_f32_e32 v150, v150
	v_exp_f32_e32 v151, v151
	s_nop 0
	v_pk_add_f32 v[144:145], v[144:145], v[184:185]
	v_pk_add_f32 v[146:147], v[146:147], v[184:185]
	v_pk_add_f32 v[148:149], v[148:149], v[184:185]
	v_pk_add_f32 v[150:151], v[150:151], v[184:185]
	v_rcp_f32_e32 v144, v144
	v_rcp_f32_e32 v145, v145
	v_rcp_f32_e32 v146, v146
	v_rcp_f32_e32 v147, v147
	v_rcp_f32_e32 v148, v148
	v_rcp_f32_e32 v149, v149
	v_rcp_f32_e32 v150, v150
	v_rcp_f32_e32 v151, v151
	s_nop 0
	v_cvt_pk_bf16_f32 v62, v144, v145
	v_cvt_pk_bf16_f32 v63, v146, v147
	v_cvt_pk_bf16_f32 v64, v148, v149
	v_cvt_pk_bf16_f32 v65, v150, v151
	v_pk_mul_f32 v[54:55], v[54:55], v[140:141] op_sel_hi:[1,0]
	v_pk_mul_f32 v[56:57], v[56:57], v[140:141] op_sel_hi:[1,0]
	v_pk_mul_f32 v[50:51], v[50:51], v[140:141] op_sel_hi:[1,0]
	v_pk_mul_f32 v[52:53], v[52:53], v[140:141] op_sel_hi:[1,0]
	v_pk_mul_f32 v[144:145], v[54:55], v[186:187]
	v_pk_mul_f32 v[146:147], v[56:57], v[186:187]
	v_pk_mul_f32 v[148:149], v[50:51], v[186:187]
	v_pk_mul_f32 v[150:151], v[52:53], v[186:187]
	v_exp_f32_e32 v144, v144
	v_exp_f32_e32 v145, v145
	v_exp_f32_e32 v146, v146
	v_exp_f32_e32 v147, v147
	v_exp_f32_e32 v148, v148
	v_exp_f32_e32 v149, v149
	v_exp_f32_e32 v150, v150
	v_exp_f32_e32 v151, v151
	s_nop 0
	v_pk_add_f32 v[144:145], v[144:145], v[184:185]
	v_pk_add_f32 v[146:147], v[146:147], v[184:185]
	v_pk_add_f32 v[148:149], v[148:149], v[184:185]
	v_pk_add_f32 v[150:151], v[150:151], v[184:185]
	v_rcp_f32_e32 v144, v144
	v_rcp_f32_e32 v145, v145
	v_rcp_f32_e32 v146, v146
	v_rcp_f32_e32 v147, v147
	v_rcp_f32_e32 v148, v148
	v_rcp_f32_e32 v149, v149
	v_rcp_f32_e32 v150, v150
	v_rcp_f32_e32 v151, v151
	s_nop 0
	v_cvt_pk_bf16_f32 v54, v144, v145
	v_cvt_pk_bf16_f32 v55, v146, v147
	v_cvt_pk_bf16_f32 v56, v148, v149
	v_cvt_pk_bf16_f32 v57, v150, v151
	v_mov_b32_e32 v158, v54
	v_mov_b32_e32 v159, v55
	v_mov_b32_e32 v160, v56
	v_mov_b32_e32 v161, v57
	v_mov_b32_dpp v54, v62 row_shl:8 row_mask:0xf bank_mask:0x3
	v_mov_b32_dpp v55, v63 row_shl:8 row_mask:0xf bank_mask:0x3
	v_mov_b32_dpp v56, v64 row_shl:8 row_mask:0xf bank_mask:0x3
	v_mov_b32_dpp v57, v65 row_shl:8 row_mask:0xf bank_mask:0x3
	v_mov_b32_dpp v62, v158 row_shr:8 row_mask:0xf bank_mask:0xc
	v_mov_b32_dpp v63, v159 row_shr:8 row_mask:0xf bank_mask:0xc
	v_mov_b32_dpp v64, v160 row_shr:8 row_mask:0xf bank_mask:0xc
	v_mov_b32_dpp v65, v161 row_shr:8 row_mask:0xf bank_mask:0xc
	s_mul_i32 s28, s22, 128
	v_lshl_add_u64 v[180:181], s[28:29], 0, v[178:179]
	global_store_dwordx4 v[180:181], v[62:65], off
	s_mul_i32 s28, s22, 136
	v_lshl_add_u64 v[180:181], s[28:29], 0, v[178:179]
	global_store_dwordx4 v[180:181], v[54:57], off
	v_pk_mul_f32 v[46:47], v[46:47], v[140:141] op_sel:[0,1] op_sel_hi:[1,1]
	v_pk_mul_f32 v[48:49], v[48:49], v[140:141] op_sel:[0,1] op_sel_hi:[1,1]
	v_pk_mul_f32 v[42:43], v[42:43], v[140:141] op_sel:[0,1] op_sel_hi:[1,1]
	v_pk_mul_f32 v[44:45], v[44:45], v[140:141] op_sel:[0,1] op_sel_hi:[1,1]
	v_pk_mul_f32 v[144:145], v[46:47], v[186:187]
	v_pk_mul_f32 v[146:147], v[48:49], v[186:187]
	v_pk_mul_f32 v[148:149], v[42:43], v[186:187]
	v_pk_mul_f32 v[150:151], v[44:45], v[186:187]
	v_exp_f32_e32 v144, v144
	v_exp_f32_e32 v145, v145
	v_exp_f32_e32 v146, v146
	v_exp_f32_e32 v147, v147
	v_exp_f32_e32 v148, v148
	v_exp_f32_e32 v149, v149
	v_exp_f32_e32 v150, v150
	v_exp_f32_e32 v151, v151
	s_nop 0
	v_pk_add_f32 v[144:145], v[144:145], v[184:185]
	v_pk_add_f32 v[146:147], v[146:147], v[184:185]
	v_pk_add_f32 v[148:149], v[148:149], v[184:185]
	v_pk_add_f32 v[150:151], v[150:151], v[184:185]
	v_rcp_f32_e32 v144, v144
	v_rcp_f32_e32 v145, v145
	v_rcp_f32_e32 v146, v146
	v_rcp_f32_e32 v147, v147
	v_rcp_f32_e32 v148, v148
	v_rcp_f32_e32 v149, v149
	v_rcp_f32_e32 v150, v150
	v_rcp_f32_e32 v151, v151
	s_nop 0
	v_cvt_pk_bf16_f32 v46, v144, v145
	v_cvt_pk_bf16_f32 v47, v146, v147
	v_cvt_pk_bf16_f32 v48, v148, v149
	v_cvt_pk_bf16_f32 v49, v150, v151
	v_pk_mul_f32 v[38:39], v[38:39], v[140:141] op_sel:[0,1] op_sel_hi:[1,1]
	v_pk_mul_f32 v[40:41], v[40:41], v[140:141] op_sel:[0,1] op_sel_hi:[1,1]
	v_pk_mul_f32 v[34:35], v[34:35], v[140:141] op_sel:[0,1] op_sel_hi:[1,1]
	v_pk_mul_f32 v[36:37], v[36:37], v[140:141] op_sel:[0,1] op_sel_hi:[1,1]
	v_pk_mul_f32 v[144:145], v[38:39], v[186:187]
	v_pk_mul_f32 v[146:147], v[40:41], v[186:187]
	v_pk_mul_f32 v[148:149], v[34:35], v[186:187]
	v_pk_mul_f32 v[150:151], v[36:37], v[186:187]
	v_exp_f32_e32 v144, v144
	v_exp_f32_e32 v145, v145
	v_exp_f32_e32 v146, v146
	v_exp_f32_e32 v147, v147
	v_exp_f32_e32 v148, v148
	v_exp_f32_e32 v149, v149
	v_exp_f32_e32 v150, v150
	v_exp_f32_e32 v151, v151
	s_nop 0
	v_pk_add_f32 v[144:145], v[144:145], v[184:185]
	v_pk_add_f32 v[146:147], v[146:147], v[184:185]
	v_pk_add_f32 v[148:149], v[148:149], v[184:185]
	v_pk_add_f32 v[150:151], v[150:151], v[184:185]
	v_rcp_f32_e32 v144, v144
	v_rcp_f32_e32 v145, v145
	v_rcp_f32_e32 v146, v146
	v_rcp_f32_e32 v147, v147
	v_rcp_f32_e32 v148, v148
	v_rcp_f32_e32 v149, v149
	v_rcp_f32_e32 v150, v150
	v_rcp_f32_e32 v151, v151
	s_nop 0
	v_cvt_pk_bf16_f32 v38, v144, v145
	v_cvt_pk_bf16_f32 v39, v146, v147
	v_cvt_pk_bf16_f32 v40, v148, v149
	v_cvt_pk_bf16_f32 v41, v150, v151
	v_mov_b32_e32 v158, v38
	v_mov_b32_e32 v159, v39
	v_mov_b32_e32 v160, v40
	v_mov_b32_e32 v161, v41
	v_mov_b32_dpp v38, v46 row_shl:8 row_mask:0xf bank_mask:0x3
	v_mov_b32_dpp v39, v47 row_shl:8 row_mask:0xf bank_mask:0x3
	v_mov_b32_dpp v40, v48 row_shl:8 row_mask:0xf bank_mask:0x3
	v_mov_b32_dpp v41, v49 row_shl:8 row_mask:0xf bank_mask:0x3
	v_mov_b32_dpp v46, v158 row_shr:8 row_mask:0xf bank_mask:0xc
	v_mov_b32_dpp v47, v159 row_shr:8 row_mask:0xf bank_mask:0xc
	v_mov_b32_dpp v48, v160 row_shr:8 row_mask:0xf bank_mask:0xc
	v_mov_b32_dpp v49, v161 row_shr:8 row_mask:0xf bank_mask:0xc
	s_mul_i32 s28, s22, 144
	v_lshl_add_u64 v[180:181], s[28:29], 0, v[178:179]
	global_store_dwordx4 v[180:181], v[46:49], off
	s_mul_i32 s28, s22, 152
	v_lshl_add_u64 v[180:181], s[28:29], 0, v[178:179]
	global_store_dwordx4 v[180:181], v[38:41], off
	v_pk_mul_f32 v[30:31], v[30:31], v[142:143] op_sel_hi:[1,0]
	v_pk_mul_f32 v[32:33], v[32:33], v[142:143] op_sel_hi:[1,0]
	v_pk_mul_f32 v[26:27], v[26:27], v[142:143] op_sel_hi:[1,0]
	v_pk_mul_f32 v[28:29], v[28:29], v[142:143] op_sel_hi:[1,0]
	v_pk_mul_f32 v[144:145], v[30:31], v[186:187]
	v_pk_mul_f32 v[146:147], v[32:33], v[186:187]
	v_pk_mul_f32 v[148:149], v[26:27], v[186:187]
	v_pk_mul_f32 v[150:151], v[28:29], v[186:187]
	v_exp_f32_e32 v144, v144
	v_exp_f32_e32 v145, v145
	v_exp_f32_e32 v146, v146
	v_exp_f32_e32 v147, v147
	v_exp_f32_e32 v148, v148
	v_exp_f32_e32 v149, v149
	v_exp_f32_e32 v150, v150
	v_exp_f32_e32 v151, v151
	s_nop 0
	v_pk_add_f32 v[144:145], v[144:145], v[184:185]
	v_pk_add_f32 v[146:147], v[146:147], v[184:185]
	v_pk_add_f32 v[148:149], v[148:149], v[184:185]
	v_pk_add_f32 v[150:151], v[150:151], v[184:185]
	v_rcp_f32_e32 v144, v144
	v_rcp_f32_e32 v145, v145
	v_rcp_f32_e32 v146, v146
	v_rcp_f32_e32 v147, v147
	v_rcp_f32_e32 v148, v148
	v_rcp_f32_e32 v149, v149
	v_rcp_f32_e32 v150, v150
	v_rcp_f32_e32 v151, v151
	s_nop 0
	v_cvt_pk_bf16_f32 v30, v144, v145
	v_cvt_pk_bf16_f32 v31, v146, v147
	v_cvt_pk_bf16_f32 v32, v148, v149
	v_cvt_pk_bf16_f32 v33, v150, v151
	v_pk_mul_f32 v[22:23], v[22:23], v[142:143] op_sel_hi:[1,0]
	v_pk_mul_f32 v[24:25], v[24:25], v[142:143] op_sel_hi:[1,0]
	v_pk_mul_f32 v[18:19], v[18:19], v[142:143] op_sel_hi:[1,0]
	v_pk_mul_f32 v[20:21], v[20:21], v[142:143] op_sel_hi:[1,0]
	v_pk_mul_f32 v[144:145], v[22:23], v[186:187]
	v_pk_mul_f32 v[146:147], v[24:25], v[186:187]
	v_pk_mul_f32 v[148:149], v[18:19], v[186:187]
	v_pk_mul_f32 v[150:151], v[20:21], v[186:187]
	v_exp_f32_e32 v144, v144
	v_exp_f32_e32 v145, v145
	v_exp_f32_e32 v146, v146
	v_exp_f32_e32 v147, v147
	v_exp_f32_e32 v148, v148
	v_exp_f32_e32 v149, v149
	v_exp_f32_e32 v150, v150
	v_exp_f32_e32 v151, v151
	s_nop 0
	v_pk_add_f32 v[144:145], v[144:145], v[184:185]
	v_pk_add_f32 v[146:147], v[146:147], v[184:185]
	v_pk_add_f32 v[148:149], v[148:149], v[184:185]
	v_pk_add_f32 v[150:151], v[150:151], v[184:185]
	v_rcp_f32_e32 v144, v144
	v_rcp_f32_e32 v145, v145
	v_rcp_f32_e32 v146, v146
	v_rcp_f32_e32 v147, v147
	v_rcp_f32_e32 v148, v148
	v_rcp_f32_e32 v149, v149
	v_rcp_f32_e32 v150, v150
	v_rcp_f32_e32 v151, v151
	s_nop 0
	v_cvt_pk_bf16_f32 v22, v144, v145
	v_cvt_pk_bf16_f32 v23, v146, v147
	v_cvt_pk_bf16_f32 v24, v148, v149
	v_cvt_pk_bf16_f32 v25, v150, v151
	v_mov_b32_e32 v158, v22
	v_mov_b32_e32 v159, v23
	v_mov_b32_e32 v160, v24
	v_mov_b32_e32 v161, v25
	v_mov_b32_dpp v22, v30 row_shl:8 row_mask:0xf bank_mask:0x3
	v_mov_b32_dpp v23, v31 row_shl:8 row_mask:0xf bank_mask:0x3
	v_mov_b32_dpp v24, v32 row_shl:8 row_mask:0xf bank_mask:0x3
	v_mov_b32_dpp v25, v33 row_shl:8 row_mask:0xf bank_mask:0x3
	v_mov_b32_dpp v30, v158 row_shr:8 row_mask:0xf bank_mask:0xc
	v_mov_b32_dpp v31, v159 row_shr:8 row_mask:0xf bank_mask:0xc
	v_mov_b32_dpp v32, v160 row_shr:8 row_mask:0xf bank_mask:0xc
	v_mov_b32_dpp v33, v161 row_shr:8 row_mask:0xf bank_mask:0xc
	s_mul_i32 s28, s22, 160
	v_lshl_add_u64 v[180:181], s[28:29], 0, v[178:179]
	global_store_dwordx4 v[180:181], v[30:33], off
	s_mul_i32 s28, s22, 168
	v_lshl_add_u64 v[180:181], s[28:29], 0, v[178:179]
	global_store_dwordx4 v[180:181], v[22:25], off
	v_pk_mul_f32 v[14:15], v[14:15], v[142:143] op_sel:[0,1] op_sel_hi:[1,1]
	v_pk_mul_f32 v[16:17], v[16:17], v[142:143] op_sel:[0,1] op_sel_hi:[1,1]
	v_pk_mul_f32 v[10:11], v[10:11], v[142:143] op_sel:[0,1] op_sel_hi:[1,1]
	v_pk_mul_f32 v[12:13], v[12:13], v[142:143] op_sel:[0,1] op_sel_hi:[1,1]
	v_pk_mul_f32 v[144:145], v[14:15], v[186:187]
	v_pk_mul_f32 v[146:147], v[16:17], v[186:187]
	v_pk_mul_f32 v[148:149], v[10:11], v[186:187]
	v_pk_mul_f32 v[150:151], v[12:13], v[186:187]
	v_exp_f32_e32 v144, v144
	v_exp_f32_e32 v145, v145
	v_exp_f32_e32 v146, v146
	v_exp_f32_e32 v147, v147
	v_exp_f32_e32 v148, v148
	v_exp_f32_e32 v149, v149
	v_exp_f32_e32 v150, v150
	v_exp_f32_e32 v151, v151
	s_nop 0
	v_pk_add_f32 v[144:145], v[144:145], v[184:185]
	v_pk_add_f32 v[146:147], v[146:147], v[184:185]
	v_pk_add_f32 v[148:149], v[148:149], v[184:185]
	v_pk_add_f32 v[150:151], v[150:151], v[184:185]
	v_rcp_f32_e32 v144, v144
	v_rcp_f32_e32 v145, v145
	v_rcp_f32_e32 v146, v146
	v_rcp_f32_e32 v147, v147
	v_rcp_f32_e32 v148, v148
	v_rcp_f32_e32 v149, v149
	v_rcp_f32_e32 v150, v150
	v_rcp_f32_e32 v151, v151
	s_nop 0
	v_cvt_pk_bf16_f32 v14, v144, v145
	v_cvt_pk_bf16_f32 v15, v146, v147
	v_cvt_pk_bf16_f32 v16, v148, v149
	v_cvt_pk_bf16_f32 v17, v150, v151
	v_pk_mul_f32 v[6:7], v[6:7], v[142:143] op_sel:[0,1] op_sel_hi:[1,1]
	v_pk_mul_f32 v[8:9], v[8:9], v[142:143] op_sel:[0,1] op_sel_hi:[1,1]
	v_pk_mul_f32 v[2:3], v[2:3], v[142:143] op_sel:[0,1] op_sel_hi:[1,1]
	v_pk_mul_f32 v[4:5], v[4:5], v[142:143] op_sel:[0,1] op_sel_hi:[1,1]
	v_pk_mul_f32 v[144:145], v[6:7], v[186:187]
	v_pk_mul_f32 v[146:147], v[8:9], v[186:187]
	v_pk_mul_f32 v[148:149], v[2:3], v[186:187]
	v_pk_mul_f32 v[150:151], v[4:5], v[186:187]
	v_exp_f32_e32 v144, v144
	v_exp_f32_e32 v145, v145
	v_exp_f32_e32 v146, v146
	v_exp_f32_e32 v147, v147
	v_exp_f32_e32 v148, v148
	v_exp_f32_e32 v149, v149
	v_exp_f32_e32 v150, v150
	v_exp_f32_e32 v151, v151
	s_nop 0
	v_pk_add_f32 v[144:145], v[144:145], v[184:185]
	v_pk_add_f32 v[146:147], v[146:147], v[184:185]
	v_pk_add_f32 v[148:149], v[148:149], v[184:185]
	v_pk_add_f32 v[150:151], v[150:151], v[184:185]
	v_rcp_f32_e32 v144, v144
	v_rcp_f32_e32 v145, v145
	v_rcp_f32_e32 v146, v146
	v_rcp_f32_e32 v147, v147
	v_rcp_f32_e32 v148, v148
	v_rcp_f32_e32 v149, v149
	v_rcp_f32_e32 v150, v150
	v_rcp_f32_e32 v151, v151
	s_nop 0
	v_cvt_pk_bf16_f32 v6, v144, v145
	v_cvt_pk_bf16_f32 v7, v146, v147
	v_cvt_pk_bf16_f32 v8, v148, v149
	v_cvt_pk_bf16_f32 v9, v150, v151
	v_mov_b32_e32 v158, v6
	v_mov_b32_e32 v159, v7
	v_mov_b32_e32 v160, v8
	v_mov_b32_e32 v161, v9
	v_mov_b32_dpp v6, v14 row_shl:8 row_mask:0xf bank_mask:0x3
	v_mov_b32_dpp v7, v15 row_shl:8 row_mask:0xf bank_mask:0x3
	v_mov_b32_dpp v8, v16 row_shl:8 row_mask:0xf bank_mask:0x3
	v_mov_b32_dpp v9, v17 row_shl:8 row_mask:0xf bank_mask:0x3
	v_mov_b32_dpp v14, v158 row_shr:8 row_mask:0xf bank_mask:0xc
	v_mov_b32_dpp v15, v159 row_shr:8 row_mask:0xf bank_mask:0xc
	v_mov_b32_dpp v16, v160 row_shr:8 row_mask:0xf bank_mask:0xc
	v_mov_b32_dpp v17, v161 row_shr:8 row_mask:0xf bank_mask:0xc
	s_mul_i32 s28, s22, 176
	v_lshl_add_u64 v[180:181], s[28:29], 0, v[178:179]
	global_store_dwordx4 v[180:181], v[14:17], off
	s_mul_i32 s28, s22, 184
	v_lshl_add_u64 v[180:181], s[28:29], 0, v[178:179]
	global_store_dwordx4 v[180:181], v[6:9], off
.Lpj_done:
	s_and_b64 vcc, exec, s[2:3]
	s_mov_b64 s[2:3], -1
	s_cbranch_vccnz .LBB0_566
	s_andn2_b64 vcc, exec, s[12:13]
	s_cbranch_vccnz .LBB0_565
	s_barrier
	s_branch .LBB0_565

.LBB0_1465:
	v_and_b32_e32 v224, -9, v186
	v_lshl_add_u32 v224, s70, 8, v224
	v_ashrrev_i32_e32 v225, 31, v224
	v_lshrrev_b32_e32 v226, 5, v188
	v_lshlrev_b32_e32 v226, 6, v226
	v_lshl_or_b32 v226, s71, 8, v226
	v_and_b32_e32 v232, 12, v188
	v_add_u32_e32 v242, v226, v232
	v_lshl_add_u32 v240, s70, 8, v186
	v_ashrrev_i32_e32 v241, 31, v240
	v_and_b32_e32 v232, 4, v188
	v_and_b32_e32 v233, 8, v188
	v_lshl_add_u32 v226, v232, 2, v226
	v_add_u32_e32 v226, v226, v233
	v_and_b32_e32 v232, 8, v186
	v_lshl_add_u32 v226, v232, 2, v226
	v_lshlrev_b32_e32 v226, 1, v226
	v_mov_b32_e32 v227, 0
	s_mov_b32 s5, 0
	v_lshlrev_b64 v[230:231], 11, v[224:225]
	v_lshl_add_u64 v[228:229], s[14:15], 0, v[230:231]
	v_lshl_add_u64 v[228:229], v[228:229], 0, v[226:227]
	s_andn2_b64 vcc, exec, s[22:23]
	s_cbranch_vccnz .Lrf_wout_bf16
	v_lshlrev_b32_e32 v242, 2, v242
	v_mov_b32_e32 v243, 0
	v_lshlrev_b64 v[230:231], 12, v[240:241]
	v_lshl_add_u64 v[244:245], s[16:17], 0, v[230:231]
	v_lshl_add_u64 v[244:245], v[244:245], 0, v[242:243]
	s_mov_b32 s4, 0x0
	v_lshl_add_u64 v[230:231], s[4:5], 0, v[244:245]
	global_load_dwordx4 v[130:133], v[230:231], off
	global_load_dwordx4 v[134:137], v[230:231], off offset:64
	global_load_dwordx4 v[138:141], v[230:231], off offset:128
	global_load_dwordx4 v[142:145], v[230:231], off offset:192
	s_mov_b32 s4, 0x10000
	v_lshl_add_u64 v[230:231], s[4:5], 0, v[244:245]
	global_load_dwordx4 v[146:149], v[230:231], off
	global_load_dwordx4 v[150:153], v[230:231], off offset:64
	global_load_dwordx4 v[154:157], v[230:231], off offset:128
	global_load_dwordx4 v[158:161], v[230:231], off offset:192
	s_mov_b32 s4, 0x20000
	v_lshl_add_u64 v[230:231], s[4:5], 0, v[244:245]
	global_load_dwordx4 v[172:175], v[230:231], off
	global_load_dwordx4 v[176:179], v[230:231], off offset:64
	global_load_dwordx4 v[180:183], v[230:231], off offset:128
	global_load_dwordx4 v[190:193], v[230:231], off offset:192
	s_mov_b32 s4, 0x30000
	v_lshl_add_u64 v[230:231], s[4:5], 0, v[244:245]
	global_load_dwordx4 v[194:197], v[230:231], off
	global_load_dwordx4 v[212:215], v[230:231], off offset:64
	global_load_dwordx4 v[216:219], v[230:231], off offset:128
	global_load_dwordx4 v[220:223], v[230:231], off offset:192
	s_and_b64 vcc, exec, s[20:21]
	s_cbranch_vccz .Lrf_wout_nobarf
	s_barrier
.Lrf_wout_nobarf:
	s_waitcnt vmcnt(15)
	v_pk_fma_f32 v[126:127], v[166:167], v[126:127], v[130:131]
	v_pk_fma_f32 v[128:129], v[166:167], v[128:129], v[132:133]
	s_waitcnt vmcnt(14)
	v_pk_fma_f32 v[122:123], v[166:167], v[122:123], v[134:135]
	v_pk_fma_f32 v[124:125], v[166:167], v[124:125], v[136:137]
	v_cvt_pk_bf16_f32 v126, v126, v127
	v_cvt_pk_bf16_f32 v127, v128, v129
	v_cvt_pk_bf16_f32 v128, v122, v123
	v_cvt_pk_bf16_f32 v129, v124, v125
	s_nop 1
	v_permlane16_swap_b32_e32 v126, v128
	v_permlane16_swap_b32_e32 v127, v129
	s_waitcnt vmcnt(13)
	v_pk_fma_f32 v[118:119], v[166:167], v[118:119], v[138:139]
	v_pk_fma_f32 v[120:121], v[166:167], v[120:121], v[140:141]
	s_waitcnt vmcnt(12)
	v_pk_fma_f32 v[114:115], v[166:167], v[114:115], v[142:143]
	v_pk_fma_f32 v[116:117], v[166:167], v[116:117], v[144:145]
	v_cvt_pk_bf16_f32 v118, v118, v119
	v_cvt_pk_bf16_f32 v119, v120, v121
	v_cvt_pk_bf16_f32 v120, v114, v115
	v_cvt_pk_bf16_f32 v121, v116, v117
	s_nop 1
	v_permlane16_swap_b32_e32 v118, v120
	v_permlane16_swap_b32_e32 v119, v121
	s_waitcnt vmcnt(11)
	v_pk_fma_f32 v[110:111], v[166:167], v[110:111], v[146:147]
	v_pk_fma_f32 v[112:113], v[166:167], v[112:113], v[148:149]
	s_waitcnt vmcnt(10)
	v_pk_fma_f32 v[106:107], v[166:167], v[106:107], v[150:151]
	v_pk_fma_f32 v[108:109], v[166:167], v[108:109], v[152:153]
	v_cvt_pk_bf16_f32 v110, v110, v111
	v_cvt_pk_bf16_f32 v111, v112, v113
	v_cvt_pk_bf16_f32 v112, v106, v107
	v_cvt_pk_bf16_f32 v113, v108, v109
	s_nop 1
	v_permlane16_swap_b32_e32 v110, v112
	v_permlane16_swap_b32_e32 v111, v113
	s_waitcnt vmcnt(9)
	v_pk_fma_f32 v[102:103], v[166:167], v[102:103], v[154:155]
	v_pk_fma_f32 v[104:105], v[166:167], v[104:105], v[156:157]
	s_waitcnt vmcnt(8)
	v_pk_fma_f32 v[98:99], v[166:167], v[98:99], v[158:159]
	v_pk_fma_f32 v[100:101], v[166:167], v[100:101], v[160:161]
	v_cvt_pk_bf16_f32 v102, v102, v103
	v_cvt_pk_bf16_f32 v103, v104, v105
	v_cvt_pk_bf16_f32 v104, v98, v99
	v_cvt_pk_bf16_f32 v105, v100, v101
	s_nop 1
	v_permlane16_swap_b32_e32 v102, v104
	v_permlane16_swap_b32_e32 v103, v105
	s_waitcnt vmcnt(7)
	v_pk_fma_f32 v[94:95], v[166:167], v[94:95], v[172:173]
	v_pk_fma_f32 v[96:97], v[166:167], v[96:97], v[174:175]
	s_waitcnt vmcnt(6)
	v_pk_fma_f32 v[90:91], v[166:167], v[90:91], v[176:177]
	v_pk_fma_f32 v[92:93], v[166:167], v[92:93], v[178:179]
	v_cvt_pk_bf16_f32 v94, v94, v95
	v_cvt_pk_bf16_f32 v95, v96, v97
	v_cvt_pk_bf16_f32 v96, v90, v91
	v_cvt_pk_bf16_f32 v97, v92, v93
	s_nop 1
	v_permlane16_swap_b32_e32 v94, v96
	v_permlane16_swap_b32_e32 v95, v97
	s_waitcnt vmcnt(5)
	v_pk_fma_f32 v[86:87], v[166:167], v[86:87], v[180:181]
	v_pk_fma_f32 v[88:89], v[166:167], v[88:89], v[182:183]
	s_waitcnt vmcnt(4)
	v_pk_fma_f32 v[82:83], v[166:167], v[82:83], v[190:191]
	v_pk_fma_f32 v[84:85], v[166:167], v[84:85], v[192:193]
	v_cvt_pk_bf16_f32 v86, v86, v87
	v_cvt_pk_bf16_f32 v87, v88, v89
	v_cvt_pk_bf16_f32 v88, v82, v83
	v_cvt_pk_bf16_f32 v89, v84, v85
	s_nop 1
	v_permlane16_swap_b32_e32 v86, v88
	v_permlane16_swap_b32_e32 v87, v89
	s_waitcnt vmcnt(3)
	v_pk_fma_f32 v[78:79], v[166:167], v[78:79], v[194:195]
	v_pk_fma_f32 v[80:81], v[166:167], v[80:81], v[196:197]
	s_waitcnt vmcnt(2)
	v_pk_fma_f32 v[74:75], v[166:167], v[74:75], v[212:213]
	v_pk_fma_f32 v[76:77], v[166:167], v[76:77], v[214:215]
	v_cvt_pk_bf16_f32 v78, v78, v79
	v_cvt_pk_bf16_f32 v79, v80, v81
	v_cvt_pk_bf16_f32 v80, v74, v75
	v_cvt_pk_bf16_f32 v81, v76, v77
	s_nop 1
	v_permlane16_swap_b32_e32 v78, v80
	v_permlane16_swap_b32_e32 v79, v81
	s_waitcnt vmcnt(1)
	v_pk_fma_f32 v[70:71], v[166:167], v[70:71], v[216:217]
	v_pk_fma_f32 v[72:73], v[166:167], v[72:73], v[218:219]
	s_waitcnt vmcnt(0)
	v_pk_fma_f32 v[66:67], v[166:167], v[66:67], v[220:221]
	v_pk_fma_f32 v[68:69], v[166:167], v[68:69], v[222:223]
	v_cvt_pk_bf16_f32 v70, v70, v71
	v_cvt_pk_bf16_f32 v71, v72, v73
	v_cvt_pk_bf16_f32 v72, v66, v67
	v_cvt_pk_bf16_f32 v73, v68, v69
	s_nop 1
	v_permlane16_swap_b32_e32 v70, v72
	v_permlane16_swap_b32_e32 v71, v73
	s_mov_b32 s4, 0x80000
	v_lshl_add_u64 v[230:231], s[4:5], 0, v[244:245]
	global_load_dwordx4 v[130:133], v[230:231], off
	global_load_dwordx4 v[134:137], v[230:231], off offset:64
	global_load_dwordx4 v[138:141], v[230:231], off offset:128
	global_load_dwordx4 v[142:145], v[230:231], off offset:192
	s_mov_b32 s4, 0x90000
	v_lshl_add_u64 v[230:231], s[4:5], 0, v[244:245]
	global_load_dwordx4 v[146:149], v[230:231], off
	global_load_dwordx4 v[150:153], v[230:231], off offset:64
	global_load_dwordx4 v[154:157], v[230:231], off offset:128
	global_load_dwordx4 v[158:161], v[230:231], off offset:192
	s_mov_b32 s4, 0xa0000
	v_lshl_add_u64 v[230:231], s[4:5], 0, v[244:245]
	global_load_dwordx4 v[172:175], v[230:231], off
	global_load_dwordx4 v[176:179], v[230:231], off offset:64
	global_load_dwordx4 v[180:183], v[230:231], off offset:128
	global_load_dwordx4 v[190:193], v[230:231], off offset:192
	s_mov_b32 s4, 0xb0000
	v_lshl_add_u64 v[230:231], s[4:5], 0, v[244:245]
	global_load_dwordx4 v[194:197], v[230:231], off
	global_load_dwordx4 v[212:215], v[230:231], off offset:64
	global_load_dwordx4 v[216:219], v[230:231], off offset:128
	global_load_dwordx4 v[220:223], v[230:231], off offset:192
	s_waitcnt vmcnt(15)
	v_pk_fma_f32 v[62:63], v[166:167], v[62:63], v[130:131]
	v_pk_fma_f32 v[64:65], v[166:167], v[64:65], v[132:133]
	s_waitcnt vmcnt(14)
	v_pk_fma_f32 v[58:59], v[166:167], v[58:59], v[134:135]
	v_pk_fma_f32 v[60:61], v[166:167], v[60:61], v[136:137]
	v_cvt_pk_bf16_f32 v62, v62, v63
	v_cvt_pk_bf16_f32 v63, v64, v65
	v_cvt_pk_bf16_f32 v64, v58, v59
	v_cvt_pk_bf16_f32 v65, v60, v61
	s_nop 1
	v_permlane16_swap_b32_e32 v62, v64
	v_permlane16_swap_b32_e32 v63, v65
	s_waitcnt vmcnt(13)
	v_pk_fma_f32 v[54:55], v[166:167], v[54:55], v[138:139]
	v_pk_fma_f32 v[56:57], v[166:167], v[56:57], v[140:141]
	s_waitcnt vmcnt(12)
	v_pk_fma_f32 v[50:51], v[166:167], v[50:51], v[142:143]
	v_pk_fma_f32 v[52:53], v[166:167], v[52:53], v[144:145]
	v_cvt_pk_bf16_f32 v54, v54, v55
	v_cvt_pk_bf16_f32 v55, v56, v57
	v_cvt_pk_bf16_f32 v56, v50, v51
	v_cvt_pk_bf16_f32 v57, v52, v53
	s_nop 1
	v_permlane16_swap_b32_e32 v54, v56
	v_permlane16_swap_b32_e32 v55, v57
	s_waitcnt vmcnt(11)
	v_pk_fma_f32 v[46:47], v[166:167], v[46:47], v[146:147]
	v_pk_fma_f32 v[48:49], v[166:167], v[48:49], v[148:149]
	s_waitcnt vmcnt(10)
	v_pk_fma_f32 v[42:43], v[166:167], v[42:43], v[150:151]
	v_pk_fma_f32 v[44:45], v[166:167], v[44:45], v[152:153]
	v_cvt_pk_bf16_f32 v46, v46, v47
	v_cvt_pk_bf16_f32 v47, v48, v49
	v_cvt_pk_bf16_f32 v48, v42, v43
	v_cvt_pk_bf16_f32 v49, v44, v45
	s_nop 1
	v_permlane16_swap_b32_e32 v46, v48
	v_permlane16_swap_b32_e32 v47, v49
	s_waitcnt vmcnt(9)
	v_pk_fma_f32 v[38:39], v[166:167], v[38:39], v[154:155]
	v_pk_fma_f32 v[40:41], v[166:167], v[40:41], v[156:157]
	s_waitcnt vmcnt(8)
	v_pk_fma_f32 v[34:35], v[166:167], v[34:35], v[158:159]
	v_pk_fma_f32 v[36:37], v[166:167], v[36:37], v[160:161]
	v_cvt_pk_bf16_f32 v38, v38, v39
	v_cvt_pk_bf16_f32 v39, v40, v41
	v_cvt_pk_bf16_f32 v40, v34, v35
	v_cvt_pk_bf16_f32 v41, v36, v37
	s_nop 1
	v_permlane16_swap_b32_e32 v38, v40
	v_permlane16_swap_b32_e32 v39, v41
	s_waitcnt vmcnt(7)
	v_pk_fma_f32 v[30:31], v[166:167], v[30:31], v[172:173]
	v_pk_fma_f32 v[32:33], v[166:167], v[32:33], v[174:175]
	s_waitcnt vmcnt(6)
	v_pk_fma_f32 v[26:27], v[166:167], v[26:27], v[176:177]
	v_pk_fma_f32 v[28:29], v[166:167], v[28:29], v[178:179]
	v_cvt_pk_bf16_f32 v30, v30, v31
	v_cvt_pk_bf16_f32 v31, v32, v33
	v_cvt_pk_bf16_f32 v32, v26, v27
	v_cvt_pk_bf16_f32 v33, v28, v29
	s_nop 1
	v_permlane16_swap_b32_e32 v30, v32
	v_permlane16_swap_b32_e32 v31, v33
	s_waitcnt vmcnt(5)
	v_pk_fma_f32 v[22:23], v[166:167], v[22:23], v[180:181]
	v_pk_fma_f32 v[24:25], v[166:167], v[24:25], v[182:183]
	s_waitcnt vmcnt(4)
	v_pk_fma_f32 v[18:19], v[166:167], v[18:19], v[190:191]
	v_pk_fma_f32 v[20:21], v[166:167], v[20:21], v[192:193]
	v_cvt_pk_bf16_f32 v22, v22, v23
	v_cvt_pk_bf16_f32 v23, v24, v25
	v_cvt_pk_bf16_f32 v24, v18, v19
	v_cvt_pk_bf16_f32 v25, v20, v21
	s_nop 1
	v_permlane16_swap_b32_e32 v22, v24
	v_permlane16_swap_b32_e32 v23, v25
	s_waitcnt vmcnt(3)
	v_pk_fma_f32 v[14:15], v[166:167], v[14:15], v[194:195]
	v_pk_fma_f32 v[16:17], v[166:167], v[16:17], v[196:197]
	s_waitcnt vmcnt(2)
	v_pk_fma_f32 v[10:11], v[166:167], v[10:11], v[212:213]
	v_pk_fma_f32 v[12:13], v[166:167], v[12:13], v[214:215]
	v_cvt_pk_bf16_f32 v14, v14, v15
	v_cvt_pk_bf16_f32 v15, v16, v17
	v_cvt_pk_bf16_f32 v16, v10, v11
	v_cvt_pk_bf16_f32 v17, v12, v13
	s_nop 1
	v_permlane16_swap_b32_e32 v14, v16
	v_permlane16_swap_b32_e32 v15, v17
	s_waitcnt vmcnt(1)
	v_pk_fma_f32 v[6:7], v[166:167], v[6:7], v[216:217]
	v_pk_fma_f32 v[8:9], v[166:167], v[8:9], v[218:219]
	s_waitcnt vmcnt(0)
	v_pk_fma_f32 v[2:3], v[166:167], v[2:3], v[220:221]
	v_pk_fma_f32 v[4:5], v[166:167], v[4:5], v[222:223]
	v_cvt_pk_bf16_f32 v6, v6, v7
	v_cvt_pk_bf16_f32 v7, v8, v9
	v_cvt_pk_bf16_f32 v8, v2, v3
	v_cvt_pk_bf16_f32 v9, v4, v5
	s_nop 1
	v_permlane16_swap_b32_e32 v6, v8
	v_permlane16_swap_b32_e32 v7, v9
	s_branch .Lrf_wout_store
.Lrf_wout_bf16:
	s_mov_b32 s4, 0x0
	v_lshl_add_u64 v[230:231], s[4:5], 0, v[228:229]
	global_load_dwordx4 v[130:133], v[230:231], off
	s_mov_b32 s4, 0x4000
	v_lshl_add_u64 v[230:231], s[4:5], 0, v[228:229]
	global_load_dwordx4 v[134:137], v[230:231], off
	s_mov_b32 s4, 0x8000
	v_lshl_add_u64 v[230:231], s[4:5], 0, v[228:229]
	global_load_dwordx4 v[138:141], v[230:231], off
	s_mov_b32 s4, 0xc000
	v_lshl_add_u64 v[230:231], s[4:5], 0, v[228:229]
	global_load_dwordx4 v[142:145], v[230:231], off
	s_mov_b32 s4, 0x10000
	v_lshl_add_u64 v[230:231], s[4:5], 0, v[228:229]
	global_load_dwordx4 v[146:149], v[230:231], off
	s_mov_b32 s4, 0x14000
	v_lshl_add_u64 v[230:231], s[4:5], 0, v[228:229]
	global_load_dwordx4 v[150:153], v[230:231], off
	s_mov_b32 s4, 0x18000
	v_lshl_add_u64 v[230:231], s[4:5], 0, v[228:229]
	global_load_dwordx4 v[154:157], v[230:231], off
	s_mov_b32 s4, 0x1c000
	v_lshl_add_u64 v[230:231], s[4:5], 0, v[228:229]
	global_load_dwordx4 v[158:161], v[230:231], off
	s_mov_b32 s4, 0x40000
	v_lshl_add_u64 v[230:231], s[4:5], 0, v[228:229]
	global_load_dwordx4 v[172:175], v[230:231], off
	s_mov_b32 s4, 0x44000
	v_lshl_add_u64 v[230:231], s[4:5], 0, v[228:229]
	global_load_dwordx4 v[176:179], v[230:231], off
	s_mov_b32 s4, 0x48000
	v_lshl_add_u64 v[230:231], s[4:5], 0, v[228:229]
	global_load_dwordx4 v[180:183], v[230:231], off
	s_mov_b32 s4, 0x4c000
	v_lshl_add_u64 v[230:231], s[4:5], 0, v[228:229]
	global_load_dwordx4 v[190:193], v[230:231], off
	s_mov_b32 s4, 0x50000
	v_lshl_add_u64 v[230:231], s[4:5], 0, v[228:229]
	global_load_dwordx4 v[194:197], v[230:231], off
	s_mov_b32 s4, 0x54000
	v_lshl_add_u64 v[230:231], s[4:5], 0, v[228:229]
	global_load_dwordx4 v[212:215], v[230:231], off
	s_mov_b32 s4, 0x58000
	v_lshl_add_u64 v[230:231], s[4:5], 0, v[228:229]
	global_load_dwordx4 v[216:219], v[230:231], off
	s_mov_b32 s4, 0x5c000
	v_lshl_add_u64 v[230:231], s[4:5], 0, v[228:229]
	global_load_dwordx4 v[220:223], v[230:231], off
	s_and_b64 vcc, exec, s[20:21]
	s_cbranch_vccz .Lrf_wout_nobarb
	s_barrier
.Lrf_wout_nobarb:
	s_waitcnt vmcnt(14)
	v_mov_b32_e32 v232, v130
	v_mov_b32_e32 v233, v131
	v_mov_b32_e32 v234, v132
	v_mov_b32_e32 v235, v133
	v_mov_b32_dpp v130, v134 row_shr:8 row_mask:0xf bank_mask:0xc
	v_mov_b32_dpp v131, v135 row_shr:8 row_mask:0xf bank_mask:0xc
	v_mov_b32_dpp v132, v136 row_shr:8 row_mask:0xf bank_mask:0xc
	v_mov_b32_dpp v133, v137 row_shr:8 row_mask:0xf bank_mask:0xc
	v_mov_b32_dpp v134, v232 row_shl:8 row_mask:0xf bank_mask:0x3
	v_mov_b32_dpp v135, v233 row_shl:8 row_mask:0xf bank_mask:0x3
	v_mov_b32_dpp v136, v234 row_shl:8 row_mask:0xf bank_mask:0x3
	v_mov_b32_dpp v137, v235 row_shl:8 row_mask:0xf bank_mask:0x3
	s_nop 1
	v_permlane16_swap_b32_e32 v130, v132
	v_permlane16_swap_b32_e32 v131, v133
	v_lshlrev_b32_e32 v236, 16, v130
	v_and_b32_e32 v237, 0xffff0000, v130
	v_pk_fma_f32 v[126:127], v[166:167], v[126:127], v[236:237]
	v_lshlrev_b32_e32 v238, 16, v131
	v_and_b32_e32 v239, 0xffff0000, v131
	v_pk_fma_f32 v[128:129], v[166:167], v[128:129], v[238:239]
	v_lshlrev_b32_e32 v236, 16, v132
	v_and_b32_e32 v237, 0xffff0000, v132
	v_pk_fma_f32 v[122:123], v[166:167], v[122:123], v[236:237]
	v_lshlrev_b32_e32 v238, 16, v133
	v_and_b32_e32 v239, 0xffff0000, v133
	v_pk_fma_f32 v[124:125], v[166:167], v[124:125], v[238:239]
	v_cvt_pk_bf16_f32 v126, v126, v127
	v_cvt_pk_bf16_f32 v127, v128, v129
	v_cvt_pk_bf16_f32 v128, v122, v123
	v_cvt_pk_bf16_f32 v129, v124, v125
	s_nop 1
	v_permlane16_swap_b32_e32 v126, v128
	v_permlane16_swap_b32_e32 v127, v129
	v_permlane16_swap_b32_e32 v134, v136
	v_permlane16_swap_b32_e32 v135, v137
	v_lshlrev_b32_e32 v236, 16, v134
	v_and_b32_e32 v237, 0xffff0000, v134
	v_pk_fma_f32 v[118:119], v[166:167], v[118:119], v[236:237]
	v_lshlrev_b32_e32 v238, 16, v135
	v_and_b32_e32 v239, 0xffff0000, v135
	v_pk_fma_f32 v[120:121], v[166:167], v[120:121], v[238:239]
	v_lshlrev_b32_e32 v236, 16, v136
	v_and_b32_e32 v237, 0xffff0000, v136
	v_pk_fma_f32 v[114:115], v[166:167], v[114:115], v[236:237]
	v_lshlrev_b32_e32 v238, 16, v137
	v_and_b32_e32 v239, 0xffff0000, v137
	v_pk_fma_f32 v[116:117], v[166:167], v[116:117], v[238:239]
	v_cvt_pk_bf16_f32 v118, v118, v119
	v_cvt_pk_bf16_f32 v119, v120, v121
	v_cvt_pk_bf16_f32 v120, v114, v115
	v_cvt_pk_bf16_f32 v121, v116, v117
	s_nop 1
	v_permlane16_swap_b32_e32 v118, v120
	v_permlane16_swap_b32_e32 v119, v121
	s_waitcnt vmcnt(12)
	v_mov_b32_e32 v232, v138
	v_mov_b32_e32 v233, v139
	v_mov_b32_e32 v234, v140
	v_mov_b32_e32 v235, v141
	v_mov_b32_dpp v138, v142 row_shr:8 row_mask:0xf bank_mask:0xc
	v_mov_b32_dpp v139, v143 row_shr:8 row_mask:0xf bank_mask:0xc
	v_mov_b32_dpp v140, v144 row_shr:8 row_mask:0xf bank_mask:0xc
	v_mov_b32_dpp v141, v145 row_shr:8 row_mask:0xf bank_mask:0xc
	v_mov_b32_dpp v142, v232 row_shl:8 row_mask:0xf bank_mask:0x3
	v_mov_b32_dpp v143, v233 row_shl:8 row_mask:0xf bank_mask:0x3
	v_mov_b32_dpp v144, v234 row_shl:8 row_mask:0xf bank_mask:0x3
	v_mov_b32_dpp v145, v235 row_shl:8 row_mask:0xf bank_mask:0x3
	s_nop 1
	v_permlane16_swap_b32_e32 v138, v140
	v_permlane16_swap_b32_e32 v139, v141
	v_lshlrev_b32_e32 v236, 16, v138
	v_and_b32_e32 v237, 0xffff0000, v138
	v_pk_fma_f32 v[110:111], v[166:167], v[110:111], v[236:237]
	v_lshlrev_b32_e32 v238, 16, v139
	v_and_b32_e32 v239, 0xffff0000, v139
	v_pk_fma_f32 v[112:113], v[166:167], v[112:113], v[238:239]
	v_lshlrev_b32_e32 v236, 16, v140
	v_and_b32_e32 v237, 0xffff0000, v140
	v_pk_fma_f32 v[106:107], v[166:167], v[106:107], v[236:237]
	v_lshlrev_b32_e32 v238, 16, v141
	v_and_b32_e32 v239, 0xffff0000, v141
	v_pk_fma_f32 v[108:109], v[166:167], v[108:109], v[238:239]
	v_cvt_pk_bf16_f32 v110, v110, v111
	v_cvt_pk_bf16_f32 v111, v112, v113
	v_cvt_pk_bf16_f32 v112, v106, v107
	v_cvt_pk_bf16_f32 v113, v108, v109
	s_nop 1
	v_permlane16_swap_b32_e32 v110, v112
	v_permlane16_swap_b32_e32 v111, v113
	v_permlane16_swap_b32_e32 v142, v144
	v_permlane16_swap_b32_e32 v143, v145
	v_lshlrev_b32_e32 v236, 16, v142
	v_and_b32_e32 v237, 0xffff0000, v142
	v_pk_fma_f32 v[102:103], v[166:167], v[102:103], v[236:237]
	v_lshlrev_b32_e32 v238, 16, v143
	v_and_b32_e32 v239, 0xffff0000, v143
	v_pk_fma_f32 v[104:105], v[166:167], v[104:105], v[238:239]
	v_lshlrev_b32_e32 v236, 16, v144
	v_and_b32_e32 v237, 0xffff0000, v144
	v_pk_fma_f32 v[98:99], v[166:167], v[98:99], v[236:237]
	v_lshlrev_b32_e32 v238, 16, v145
	v_and_b32_e32 v239, 0xffff0000, v145
	v_pk_fma_f32 v[100:101], v[166:167], v[100:101], v[238:239]
	v_cvt_pk_bf16_f32 v102, v102, v103
	v_cvt_pk_bf16_f32 v103, v104, v105
	v_cvt_pk_bf16_f32 v104, v98, v99
	v_cvt_pk_bf16_f32 v105, v100, v101
	s_nop 1
	v_permlane16_swap_b32_e32 v102, v104
	v_permlane16_swap_b32_e32 v103, v105
	s_waitcnt vmcnt(10)
	v_mov_b32_e32 v232, v146
	v_mov_b32_e32 v233, v147
	v_mov_b32_e32 v234, v148
	v_mov_b32_e32 v235, v149
	v_mov_b32_dpp v146, v150 row_shr:8 row_mask:0xf bank_mask:0xc
	v_mov_b32_dpp v147, v151 row_shr:8 row_mask:0xf bank_mask:0xc
	v_mov_b32_dpp v148, v152 row_shr:8 row_mask:0xf bank_mask:0xc
	v_mov_b32_dpp v149, v153 row_shr:8 row_mask:0xf bank_mask:0xc
	v_mov_b32_dpp v150, v232 row_shl:8 row_mask:0xf bank_mask:0x3
	v_mov_b32_dpp v151, v233 row_shl:8 row_mask:0xf bank_mask:0x3
	v_mov_b32_dpp v152, v234 row_shl:8 row_mask:0xf bank_mask:0x3
	v_mov_b32_dpp v153, v235 row_shl:8 row_mask:0xf bank_mask:0x3
	s_nop 1
	v_permlane16_swap_b32_e32 v146, v148
	v_permlane16_swap_b32_e32 v147, v149
	v_lshlrev_b32_e32 v236, 16, v146
	v_and_b32_e32 v237, 0xffff0000, v146
	v_pk_fma_f32 v[94:95], v[166:167], v[94:95], v[236:237]
	v_lshlrev_b32_e32 v238, 16, v147
	v_and_b32_e32 v239, 0xffff0000, v147
	v_pk_fma_f32 v[96:97], v[166:167], v[96:97], v[238:239]
	v_lshlrev_b32_e32 v236, 16, v148
	v_and_b32_e32 v237, 0xffff0000, v148
	v_pk_fma_f32 v[90:91], v[166:167], v[90:91], v[236:237]
	v_lshlrev_b32_e32 v238, 16, v149
	v_and_b32_e32 v239, 0xffff0000, v149
	v_pk_fma_f32 v[92:93], v[166:167], v[92:93], v[238:239]
	v_cvt_pk_bf16_f32 v94, v94, v95
	v_cvt_pk_bf16_f32 v95, v96, v97
	v_cvt_pk_bf16_f32 v96, v90, v91
	v_cvt_pk_bf16_f32 v97, v92, v93
	s_nop 1
	v_permlane16_swap_b32_e32 v94, v96
	v_permlane16_swap_b32_e32 v95, v97
	v_permlane16_swap_b32_e32 v150, v152
	v_permlane16_swap_b32_e32 v151, v153
	v_lshlrev_b32_e32 v236, 16, v150
	v_and_b32_e32 v237, 0xffff0000, v150
	v_pk_fma_f32 v[86:87], v[166:167], v[86:87], v[236:237]
	v_lshlrev_b32_e32 v238, 16, v151
	v_and_b32_e32 v239, 0xffff0000, v151
	v_pk_fma_f32 v[88:89], v[166:167], v[88:89], v[238:239]
	v_lshlrev_b32_e32 v236, 16, v152
	v_and_b32_e32 v237, 0xffff0000, v152
	v_pk_fma_f32 v[82:83], v[166:167], v[82:83], v[236:237]
	v_lshlrev_b32_e32 v238, 16, v153
	v_and_b32_e32 v239, 0xffff0000, v153
	v_pk_fma_f32 v[84:85], v[166:167], v[84:85], v[238:239]
	v_cvt_pk_bf16_f32 v86, v86, v87
	v_cvt_pk_bf16_f32 v87, v88, v89
	v_cvt_pk_bf16_f32 v88, v82, v83
	v_cvt_pk_bf16_f32 v89, v84, v85
	s_nop 1
	v_permlane16_swap_b32_e32 v86, v88
	v_permlane16_swap_b32_e32 v87, v89
	s_waitcnt vmcnt(8)
	v_mov_b32_e32 v232, v154
	v_mov_b32_e32 v233, v155
	v_mov_b32_e32 v234, v156
	v_mov_b32_e32 v235, v157
	v_mov_b32_dpp v154, v158 row_shr:8 row_mask:0xf bank_mask:0xc
	v_mov_b32_dpp v155, v159 row_shr:8 row_mask:0xf bank_mask:0xc
	v_mov_b32_dpp v156, v160 row_shr:8 row_mask:0xf bank_mask:0xc
	v_mov_b32_dpp v157, v161 row_shr:8 row_mask:0xf bank_mask:0xc
	v_mov_b32_dpp v158, v232 row_shl:8 row_mask:0xf bank_mask:0x3
	v_mov_b32_dpp v159, v233 row_shl:8 row_mask:0xf bank_mask:0x3
	v_mov_b32_dpp v160, v234 row_shl:8 row_mask:0xf bank_mask:0x3
	v_mov_b32_dpp v161, v235 row_shl:8 row_mask:0xf bank_mask:0x3
	s_nop 1
	v_permlane16_swap_b32_e32 v154, v156
	v_permlane16_swap_b32_e32 v155, v157
	v_lshlrev_b32_e32 v236, 16, v154
	v_and_b32_e32 v237, 0xffff0000, v154
	v_pk_fma_f32 v[78:79], v[166:167], v[78:79], v[236:237]
	v_lshlrev_b32_e32 v238, 16, v155
	v_and_b32_e32 v239, 0xffff0000, v155
	v_pk_fma_f32 v[80:81], v[166:167], v[80:81], v[238:239]
	v_lshlrev_b32_e32 v236, 16, v156
	v_and_b32_e32 v237, 0xffff0000, v156
	v_pk_fma_f32 v[74:75], v[166:167], v[74:75], v[236:237]
	v_lshlrev_b32_e32 v238, 16, v157
	v_and_b32_e32 v239, 0xffff0000, v157
	v_pk_fma_f32 v[76:77], v[166:167], v[76:77], v[238:239]
	v_cvt_pk_bf16_f32 v78, v78, v79
	v_cvt_pk_bf16_f32 v79, v80, v81
	v_cvt_pk_bf16_f32 v80, v74, v75
	v_cvt_pk_bf16_f32 v81, v76, v77
	s_nop 1
	v_permlane16_swap_b32_e32 v78, v80
	v_permlane16_swap_b32_e32 v79, v81
	v_permlane16_swap_b32_e32 v158, v160
	v_permlane16_swap_b32_e32 v159, v161
	v_lshlrev_b32_e32 v236, 16, v158
	v_and_b32_e32 v237, 0xffff0000, v158
	v_pk_fma_f32 v[70:71], v[166:167], v[70:71], v[236:237]
	v_lshlrev_b32_e32 v238, 16, v159
	v_and_b32_e32 v239, 0xffff0000, v159
	v_pk_fma_f32 v[72:73], v[166:167], v[72:73], v[238:239]
	v_lshlrev_b32_e32 v236, 16, v160
	v_and_b32_e32 v237, 0xffff0000, v160
	v_pk_fma_f32 v[66:67], v[166:167], v[66:67], v[236:237]
	v_lshlrev_b32_e32 v238, 16, v161
	v_and_b32_e32 v239, 0xffff0000, v161
	v_pk_fma_f32 v[68:69], v[166:167], v[68:69], v[238:239]
	v_cvt_pk_bf16_f32 v70, v70, v71
	v_cvt_pk_bf16_f32 v71, v72, v73
	v_cvt_pk_bf16_f32 v72, v66, v67
	v_cvt_pk_bf16_f32 v73, v68, v69
	s_nop 1
	v_permlane16_swap_b32_e32 v70, v72
	v_permlane16_swap_b32_e32 v71, v73
	s_waitcnt vmcnt(6)
	v_mov_b32_e32 v232, v172
	v_mov_b32_e32 v233, v173
	v_mov_b32_e32 v234, v174
	v_mov_b32_e32 v235, v175
	v_mov_b32_dpp v172, v176 row_shr:8 row_mask:0xf bank_mask:0xc
	v_mov_b32_dpp v173, v177 row_shr:8 row_mask:0xf bank_mask:0xc
	v_mov_b32_dpp v174, v178 row_shr:8 row_mask:0xf bank_mask:0xc
	v_mov_b32_dpp v175, v179 row_shr:8 row_mask:0xf bank_mask:0xc
	v_mov_b32_dpp v176, v232 row_shl:8 row_mask:0xf bank_mask:0x3
	v_mov_b32_dpp v177, v233 row_shl:8 row_mask:0xf bank_mask:0x3
	v_mov_b32_dpp v178, v234 row_shl:8 row_mask:0xf bank_mask:0x3
	v_mov_b32_dpp v179, v235 row_shl:8 row_mask:0xf bank_mask:0x3
	s_nop 1
	v_permlane16_swap_b32_e32 v172, v174
	v_permlane16_swap_b32_e32 v173, v175
	v_lshlrev_b32_e32 v236, 16, v172
	v_and_b32_e32 v237, 0xffff0000, v172
	v_pk_fma_f32 v[62:63], v[166:167], v[62:63], v[236:237]
	v_lshlrev_b32_e32 v238, 16, v173
	v_and_b32_e32 v239, 0xffff0000, v173
	v_pk_fma_f32 v[64:65], v[166:167], v[64:65], v[238:239]
	v_lshlrev_b32_e32 v236, 16, v174
	v_and_b32_e32 v237, 0xffff0000, v174
	v_pk_fma_f32 v[58:59], v[166:167], v[58:59], v[236:237]
	v_lshlrev_b32_e32 v238, 16, v175
	v_and_b32_e32 v239, 0xffff0000, v175
	v_pk_fma_f32 v[60:61], v[166:167], v[60:61], v[238:239]
	v_cvt_pk_bf16_f32 v62, v62, v63
	v_cvt_pk_bf16_f32 v63, v64, v65
	v_cvt_pk_bf16_f32 v64, v58, v59
	v_cvt_pk_bf16_f32 v65, v60, v61
	s_nop 1
	v_permlane16_swap_b32_e32 v62, v64
	v_permlane16_swap_b32_e32 v63, v65
	v_permlane16_swap_b32_e32 v176, v178
	v_permlane16_swap_b32_e32 v177, v179
	v_lshlrev_b32_e32 v236, 16, v176
	v_and_b32_e32 v237, 0xffff0000, v176
	v_pk_fma_f32 v[54:55], v[166:167], v[54:55], v[236:237]
	v_lshlrev_b32_e32 v238, 16, v177
	v_and_b32_e32 v239, 0xffff0000, v177
	v_pk_fma_f32 v[56:57], v[166:167], v[56:57], v[238:239]
	v_lshlrev_b32_e32 v236, 16, v178
	v_and_b32_e32 v237, 0xffff0000, v178
	v_pk_fma_f32 v[50:51], v[166:167], v[50:51], v[236:237]
	v_lshlrev_b32_e32 v238, 16, v179
	v_and_b32_e32 v239, 0xffff0000, v179
	v_pk_fma_f32 v[52:53], v[166:167], v[52:53], v[238:239]
	v_cvt_pk_bf16_f32 v54, v54, v55
	v_cvt_pk_bf16_f32 v55, v56, v57
	v_cvt_pk_bf16_f32 v56, v50, v51
	v_cvt_pk_bf16_f32 v57, v52, v53
	s_nop 1
	v_permlane16_swap_b32_e32 v54, v56
	v_permlane16_swap_b32_e32 v55, v57
	s_waitcnt vmcnt(4)
	v_mov_b32_e32 v232, v180
	v_mov_b32_e32 v233, v181
	v_mov_b32_e32 v234, v182
	v_mov_b32_e32 v235, v183
	v_mov_b32_dpp v180, v190 row_shr:8 row_mask:0xf bank_mask:0xc
	v_mov_b32_dpp v181, v191 row_shr:8 row_mask:0xf bank_mask:0xc
	v_mov_b32_dpp v182, v192 row_shr:8 row_mask:0xf bank_mask:0xc
	v_mov_b32_dpp v183, v193 row_shr:8 row_mask:0xf bank_mask:0xc
	v_mov_b32_dpp v190, v232 row_shl:8 row_mask:0xf bank_mask:0x3
	v_mov_b32_dpp v191, v233 row_shl:8 row_mask:0xf bank_mask:0x3
	v_mov_b32_dpp v192, v234 row_shl:8 row_mask:0xf bank_mask:0x3
	v_mov_b32_dpp v193, v235 row_shl:8 row_mask:0xf bank_mask:0x3
	s_nop 1
	v_permlane16_swap_b32_e32 v180, v182
	v_permlane16_swap_b32_e32 v181, v183
	v_lshlrev_b32_e32 v236, 16, v180
	v_and_b32_e32 v237, 0xffff0000, v180
	v_pk_fma_f32 v[46:47], v[166:167], v[46:47], v[236:237]
	v_lshlrev_b32_e32 v238, 16, v181
	v_and_b32_e32 v239, 0xffff0000, v181
	v_pk_fma_f32 v[48:49], v[166:167], v[48:49], v[238:239]
	v_lshlrev_b32_e32 v236, 16, v182
	v_and_b32_e32 v237, 0xffff0000, v182
	v_pk_fma_f32 v[42:43], v[166:167], v[42:43], v[236:237]
	v_lshlrev_b32_e32 v238, 16, v183
	v_and_b32_e32 v239, 0xffff0000, v183
	v_pk_fma_f32 v[44:45], v[166:167], v[44:45], v[238:239]
	v_cvt_pk_bf16_f32 v46, v46, v47
	v_cvt_pk_bf16_f32 v47, v48, v49
	v_cvt_pk_bf16_f32 v48, v42, v43
	v_cvt_pk_bf16_f32 v49, v44, v45
	s_nop 1
	v_permlane16_swap_b32_e32 v46, v48
	v_permlane16_swap_b32_e32 v47, v49
	v_permlane16_swap_b32_e32 v190, v192
	v_permlane16_swap_b32_e32 v191, v193
	v_lshlrev_b32_e32 v236, 16, v190
	v_and_b32_e32 v237, 0xffff0000, v190
	v_pk_fma_f32 v[38:39], v[166:167], v[38:39], v[236:237]
	v_lshlrev_b32_e32 v238, 16, v191
	v_and_b32_e32 v239, 0xffff0000, v191
	v_pk_fma_f32 v[40:41], v[166:167], v[40:41], v[238:239]
	v_lshlrev_b32_e32 v236, 16, v192
	v_and_b32_e32 v237, 0xffff0000, v192
	v_pk_fma_f32 v[34:35], v[166:167], v[34:35], v[236:237]
	v_lshlrev_b32_e32 v238, 16, v193
	v_and_b32_e32 v239, 0xffff0000, v193
	v_pk_fma_f32 v[36:37], v[166:167], v[36:37], v[238:239]
	v_cvt_pk_bf16_f32 v38, v38, v39
	v_cvt_pk_bf16_f32 v39, v40, v41
	v_cvt_pk_bf16_f32 v40, v34, v35
	v_cvt_pk_bf16_f32 v41, v36, v37
	s_nop 1
	v_permlane16_swap_b32_e32 v38, v40
	v_permlane16_swap_b32_e32 v39, v41
	s_waitcnt vmcnt(2)
	v_mov_b32_e32 v232, v194
	v_mov_b32_e32 v233, v195
	v_mov_b32_e32 v234, v196
	v_mov_b32_e32 v235, v197
	v_mov_b32_dpp v194, v212 row_shr:8 row_mask:0xf bank_mask:0xc
	v_mov_b32_dpp v195, v213 row_shr:8 row_mask:0xf bank_mask:0xc
	v_mov_b32_dpp v196, v214 row_shr:8 row_mask:0xf bank_mask:0xc
	v_mov_b32_dpp v197, v215 row_shr:8 row_mask:0xf bank_mask:0xc
	v_mov_b32_dpp v212, v232 row_shl:8 row_mask:0xf bank_mask:0x3
	v_mov_b32_dpp v213, v233 row_shl:8 row_mask:0xf bank_mask:0x3
	v_mov_b32_dpp v214, v234 row_shl:8 row_mask:0xf bank_mask:0x3
	v_mov_b32_dpp v215, v235 row_shl:8 row_mask:0xf bank_mask:0x3
	s_nop 1
	v_permlane16_swap_b32_e32 v194, v196
	v_permlane16_swap_b32_e32 v195, v197
	v_lshlrev_b32_e32 v236, 16, v194
	v_and_b32_e32 v237, 0xffff0000, v194
	v_pk_fma_f32 v[30:31], v[166:167], v[30:31], v[236:237]
	v_lshlrev_b32_e32 v238, 16, v195
	v_and_b32_e32 v239, 0xffff0000, v195
	v_pk_fma_f32 v[32:33], v[166:167], v[32:33], v[238:239]
	v_lshlrev_b32_e32 v236, 16, v196
	v_and_b32_e32 v237, 0xffff0000, v196
	v_pk_fma_f32 v[26:27], v[166:167], v[26:27], v[236:237]
	v_lshlrev_b32_e32 v238, 16, v197
	v_and_b32_e32 v239, 0xffff0000, v197
	v_pk_fma_f32 v[28:29], v[166:167], v[28:29], v[238:239]
	v_cvt_pk_bf16_f32 v30, v30, v31
	v_cvt_pk_bf16_f32 v31, v32, v33
	v_cvt_pk_bf16_f32 v32, v26, v27
	v_cvt_pk_bf16_f32 v33, v28, v29
	s_nop 1
	v_permlane16_swap_b32_e32 v30, v32
	v_permlane16_swap_b32_e32 v31, v33
	v_permlane16_swap_b32_e32 v212, v214
	v_permlane16_swap_b32_e32 v213, v215
	v_lshlrev_b32_e32 v236, 16, v212
	v_and_b32_e32 v237, 0xffff0000, v212
	v_pk_fma_f32 v[22:23], v[166:167], v[22:23], v[236:237]
	v_lshlrev_b32_e32 v238, 16, v213
	v_and_b32_e32 v239, 0xffff0000, v213
	v_pk_fma_f32 v[24:25], v[166:167], v[24:25], v[238:239]
	v_lshlrev_b32_e32 v236, 16, v214
	v_and_b32_e32 v237, 0xffff0000, v214
	v_pk_fma_f32 v[18:19], v[166:167], v[18:19], v[236:237]
	v_lshlrev_b32_e32 v238, 16, v215
	v_and_b32_e32 v239, 0xffff0000, v215
	v_pk_fma_f32 v[20:21], v[166:167], v[20:21], v[238:239]
	v_cvt_pk_bf16_f32 v22, v22, v23
	v_cvt_pk_bf16_f32 v23, v24, v25
	v_cvt_pk_bf16_f32 v24, v18, v19
	v_cvt_pk_bf16_f32 v25, v20, v21
	s_nop 1
	v_permlane16_swap_b32_e32 v22, v24
	v_permlane16_swap_b32_e32 v23, v25
	s_waitcnt vmcnt(0)
	v_mov_b32_e32 v232, v216
	v_mov_b32_e32 v233, v217
	v_mov_b32_e32 v234, v218
	v_mov_b32_e32 v235, v219
	v_mov_b32_dpp v216, v220 row_shr:8 row_mask:0xf bank_mask:0xc
	v_mov_b32_dpp v217, v221 row_shr:8 row_mask:0xf bank_mask:0xc
	v_mov_b32_dpp v218, v222 row_shr:8 row_mask:0xf bank_mask:0xc
	v_mov_b32_dpp v219, v223 row_shr:8 row_mask:0xf bank_mask:0xc
	v_mov_b32_dpp v220, v232 row_shl:8 row_mask:0xf bank_mask:0x3
	v_mov_b32_dpp v221, v233 row_shl:8 row_mask:0xf bank_mask:0x3
	v_mov_b32_dpp v222, v234 row_shl:8 row_mask:0xf bank_mask:0x3
	v_mov_b32_dpp v223, v235 row_shl:8 row_mask:0xf bank_mask:0x3
	s_nop 1
	v_permlane16_swap_b32_e32 v216, v218
	v_permlane16_swap_b32_e32 v217, v219
	v_lshlrev_b32_e32 v236, 16, v216
	v_and_b32_e32 v237, 0xffff0000, v216
	v_pk_fma_f32 v[14:15], v[166:167], v[14:15], v[236:237]
	v_lshlrev_b32_e32 v238, 16, v217
	v_and_b32_e32 v239, 0xffff0000, v217
	v_pk_fma_f32 v[16:17], v[166:167], v[16:17], v[238:239]
	v_lshlrev_b32_e32 v236, 16, v218
	v_and_b32_e32 v237, 0xffff0000, v218
	v_pk_fma_f32 v[10:11], v[166:167], v[10:11], v[236:237]
	v_lshlrev_b32_e32 v238, 16, v219
	v_and_b32_e32 v239, 0xffff0000, v219
	v_pk_fma_f32 v[12:13], v[166:167], v[12:13], v[238:239]
	v_cvt_pk_bf16_f32 v14, v14, v15
	v_cvt_pk_bf16_f32 v15, v16, v17
	v_cvt_pk_bf16_f32 v16, v10, v11
	v_cvt_pk_bf16_f32 v17, v12, v13
	s_nop 1
	v_permlane16_swap_b32_e32 v14, v16
	v_permlane16_swap_b32_e32 v15, v17
	v_permlane16_swap_b32_e32 v220, v222
	v_permlane16_swap_b32_e32 v221, v223
	v_lshlrev_b32_e32 v236, 16, v220
	v_and_b32_e32 v237, 0xffff0000, v220
	v_pk_fma_f32 v[6:7], v[166:167], v[6:7], v[236:237]
	v_lshlrev_b32_e32 v238, 16, v221
	v_and_b32_e32 v239, 0xffff0000, v221
	v_pk_fma_f32 v[8:9], v[166:167], v[8:9], v[238:239]
	v_lshlrev_b32_e32 v236, 16, v222
	v_and_b32_e32 v237, 0xffff0000, v222
	v_pk_fma_f32 v[2:3], v[166:167], v[2:3], v[236:237]
	v_lshlrev_b32_e32 v238, 16, v223
	v_and_b32_e32 v239, 0xffff0000, v223
	v_pk_fma_f32 v[4:5], v[166:167], v[4:5], v[238:239]
	v_cvt_pk_bf16_f32 v6, v6, v7
	v_cvt_pk_bf16_f32 v7, v8, v9
	v_cvt_pk_bf16_f32 v8, v2, v3
	v_cvt_pk_bf16_f32 v9, v4, v5
	s_nop 1
	v_permlane16_swap_b32_e32 v6, v8
	v_permlane16_swap_b32_e32 v7, v9
.Lrf_wout_store:
	v_mov_b32_e32 v232, v118
	v_mov_b32_e32 v233, v119
	v_mov_b32_e32 v234, v120
	v_mov_b32_e32 v235, v121
	v_mov_b32_dpp v118, v126 row_shl:8 row_mask:0xf bank_mask:0x3
	v_mov_b32_dpp v119, v127 row_shl:8 row_mask:0xf bank_mask:0x3
	v_mov_b32_dpp v120, v128 row_shl:8 row_mask:0xf bank_mask:0x3
	v_mov_b32_dpp v121, v129 row_shl:8 row_mask:0xf bank_mask:0x3
	v_mov_b32_dpp v126, v232 row_shr:8 row_mask:0xf bank_mask:0xc
	v_mov_b32_dpp v127, v233 row_shr:8 row_mask:0xf bank_mask:0xc
	v_mov_b32_dpp v128, v234 row_shr:8 row_mask:0xf bank_mask:0xc
	v_mov_b32_dpp v129, v235 row_shr:8 row_mask:0xf bank_mask:0xc
	s_mov_b32 s4, 0x0
	v_lshl_add_u64 v[230:231], s[4:5], 0, v[228:229]
	global_store_dwordx4 v[230:231], v[126:129], off
	s_mov_b32 s4, 0x4000
	v_lshl_add_u64 v[230:231], s[4:5], 0, v[228:229]
	global_store_dwordx4 v[230:231], v[118:121], off
	v_mov_b32_e32 v232, v102
	v_mov_b32_e32 v233, v103
	v_mov_b32_e32 v234, v104
	v_mov_b32_e32 v235, v105
	v_mov_b32_dpp v102, v110 row_shl:8 row_mask:0xf bank_mask:0x3
	v_mov_b32_dpp v103, v111 row_shl:8 row_mask:0xf bank_mask:0x3
	v_mov_b32_dpp v104, v112 row_shl:8 row_mask:0xf bank_mask:0x3
	v_mov_b32_dpp v105, v113 row_shl:8 row_mask:0xf bank_mask:0x3
	v_mov_b32_dpp v110, v232 row_shr:8 row_mask:0xf bank_mask:0xc
	v_mov_b32_dpp v111, v233 row_shr:8 row_mask:0xf bank_mask:0xc
	v_mov_b32_dpp v112, v234 row_shr:8 row_mask:0xf bank_mask:0xc
	v_mov_b32_dpp v113, v235 row_shr:8 row_mask:0xf bank_mask:0xc
	s_mov_b32 s4, 0x8000
	v_lshl_add_u64 v[230:231], s[4:5], 0, v[228:229]
	global_store_dwordx4 v[230:231], v[110:113], off
	s_mov_b32 s4, 0xc000
	v_lshl_add_u64 v[230:231], s[4:5], 0, v[228:229]
	global_store_dwordx4 v[230:231], v[102:105], off
	v_mov_b32_e32 v232, v86
	v_mov_b32_e32 v233, v87
	v_mov_b32_e32 v234, v88
	v_mov_b32_e32 v235, v89
	v_mov_b32_dpp v86, v94 row_shl:8 row_mask:0xf bank_mask:0x3
	v_mov_b32_dpp v87, v95 row_shl:8 row_mask:0xf bank_mask:0x3
	v_mov_b32_dpp v88, v96 row_shl:8 row_mask:0xf bank_mask:0x3
	v_mov_b32_dpp v89, v97 row_shl:8 row_mask:0xf bank_mask:0x3
	v_mov_b32_dpp v94, v232 row_shr:8 row_mask:0xf bank_mask:0xc
	v_mov_b32_dpp v95, v233 row_shr:8 row_mask:0xf bank_mask:0xc
	v_mov_b32_dpp v96, v234 row_shr:8 row_mask:0xf bank_mask:0xc
	v_mov_b32_dpp v97, v235 row_shr:8 row_mask:0xf bank_mask:0xc
	s_mov_b32 s4, 0x10000
	v_lshl_add_u64 v[230:231], s[4:5], 0, v[228:229]
	global_store_dwordx4 v[230:231], v[94:97], off
	s_mov_b32 s4, 0x14000
	v_lshl_add_u64 v[230:231], s[4:5], 0, v[228:229]
	global_store_dwordx4 v[230:231], v[86:89], off
	v_mov_b32_e32 v232, v70
	v_mov_b32_e32 v233, v71
	v_mov_b32_e32 v234, v72
	v_mov_b32_e32 v235, v73
	v_mov_b32_dpp v70, v78 row_shl:8 row_mask:0xf bank_mask:0x3
	v_mov_b32_dpp v71, v79 row_shl:8 row_mask:0xf bank_mask:0x3
	v_mov_b32_dpp v72, v80 row_shl:8 row_mask:0xf bank_mask:0x3
	v_mov_b32_dpp v73, v81 row_shl:8 row_mask:0xf bank_mask:0x3
	v_mov_b32_dpp v78, v232 row_shr:8 row_mask:0xf bank_mask:0xc
	v_mov_b32_dpp v79, v233 row_shr:8 row_mask:0xf bank_mask:0xc
	v_mov_b32_dpp v80, v234 row_shr:8 row_mask:0xf bank_mask:0xc
	v_mov_b32_dpp v81, v235 row_shr:8 row_mask:0xf bank_mask:0xc
	s_mov_b32 s4, 0x18000
	v_lshl_add_u64 v[230:231], s[4:5], 0, v[228:229]
	global_store_dwordx4 v[230:231], v[78:81], off
	s_mov_b32 s4, 0x1c000
	v_lshl_add_u64 v[230:231], s[4:5], 0, v[228:229]
	global_store_dwordx4 v[230:231], v[70:73], off
	v_mov_b32_e32 v232, v54
	v_mov_b32_e32 v233, v55
	v_mov_b32_e32 v234, v56
	v_mov_b32_e32 v235, v57
	v_mov_b32_dpp v54, v62 row_shl:8 row_mask:0xf bank_mask:0x3
	v_mov_b32_dpp v55, v63 row_shl:8 row_mask:0xf bank_mask:0x3
	v_mov_b32_dpp v56, v64 row_shl:8 row_mask:0xf bank_mask:0x3
	v_mov_b32_dpp v57, v65 row_shl:8 row_mask:0xf bank_mask:0x3
	v_mov_b32_dpp v62, v232 row_shr:8 row_mask:0xf bank_mask:0xc
	v_mov_b32_dpp v63, v233 row_shr:8 row_mask:0xf bank_mask:0xc
	v_mov_b32_dpp v64, v234 row_shr:8 row_mask:0xf bank_mask:0xc
	v_mov_b32_dpp v65, v235 row_shr:8 row_mask:0xf bank_mask:0xc
	s_mov_b32 s4, 0x40000
	v_lshl_add_u64 v[230:231], s[4:5], 0, v[228:229]
	global_store_dwordx4 v[230:231], v[62:65], off
	s_mov_b32 s4, 0x44000
	v_lshl_add_u64 v[230:231], s[4:5], 0, v[228:229]
	global_store_dwordx4 v[230:231], v[54:57], off
	v_mov_b32_e32 v232, v38
	v_mov_b32_e32 v233, v39
	v_mov_b32_e32 v234, v40
	v_mov_b32_e32 v235, v41
	v_mov_b32_dpp v38, v46 row_shl:8 row_mask:0xf bank_mask:0x3
	v_mov_b32_dpp v39, v47 row_shl:8 row_mask:0xf bank_mask:0x3
	v_mov_b32_dpp v40, v48 row_shl:8 row_mask:0xf bank_mask:0x3
	v_mov_b32_dpp v41, v49 row_shl:8 row_mask:0xf bank_mask:0x3
	v_mov_b32_dpp v46, v232 row_shr:8 row_mask:0xf bank_mask:0xc
	v_mov_b32_dpp v47, v233 row_shr:8 row_mask:0xf bank_mask:0xc
	v_mov_b32_dpp v48, v234 row_shr:8 row_mask:0xf bank_mask:0xc
	v_mov_b32_dpp v49, v235 row_shr:8 row_mask:0xf bank_mask:0xc
	s_mov_b32 s4, 0x48000
	v_lshl_add_u64 v[230:231], s[4:5], 0, v[228:229]
	global_store_dwordx4 v[230:231], v[46:49], off
	s_mov_b32 s4, 0x4c000
	v_lshl_add_u64 v[230:231], s[4:5], 0, v[228:229]
	global_store_dwordx4 v[230:231], v[38:41], off
	v_mov_b32_e32 v232, v22
	v_mov_b32_e32 v233, v23
	v_mov_b32_e32 v234, v24
	v_mov_b32_e32 v235, v25
	v_mov_b32_dpp v22, v30 row_shl:8 row_mask:0xf bank_mask:0x3
	v_mov_b32_dpp v23, v31 row_shl:8 row_mask:0xf bank_mask:0x3
	v_mov_b32_dpp v24, v32 row_shl:8 row_mask:0xf bank_mask:0x3
	v_mov_b32_dpp v25, v33 row_shl:8 row_mask:0xf bank_mask:0x3
	v_mov_b32_dpp v30, v232 row_shr:8 row_mask:0xf bank_mask:0xc
	v_mov_b32_dpp v31, v233 row_shr:8 row_mask:0xf bank_mask:0xc
	v_mov_b32_dpp v32, v234 row_shr:8 row_mask:0xf bank_mask:0xc
	v_mov_b32_dpp v33, v235 row_shr:8 row_mask:0xf bank_mask:0xc
	s_mov_b32 s4, 0x50000
	v_lshl_add_u64 v[230:231], s[4:5], 0, v[228:229]
	global_store_dwordx4 v[230:231], v[30:33], off
	s_mov_b32 s4, 0x54000
	v_lshl_add_u64 v[230:231], s[4:5], 0, v[228:229]
	global_store_dwordx4 v[230:231], v[22:25], off
	v_mov_b32_e32 v232, v6
	v_mov_b32_e32 v233, v7
	v_mov_b32_e32 v234, v8
	v_mov_b32_e32 v235, v9
	v_mov_b32_dpp v6, v14 row_shl:8 row_mask:0xf bank_mask:0x3
	v_mov_b32_dpp v7, v15 row_shl:8 row_mask:0xf bank_mask:0x3
	v_mov_b32_dpp v8, v16 row_shl:8 row_mask:0xf bank_mask:0x3
	v_mov_b32_dpp v9, v17 row_shl:8 row_mask:0xf bank_mask:0x3
	v_mov_b32_dpp v14, v232 row_shr:8 row_mask:0xf bank_mask:0xc
	v_mov_b32_dpp v15, v233 row_shr:8 row_mask:0xf bank_mask:0xc
	v_mov_b32_dpp v16, v234 row_shr:8 row_mask:0xf bank_mask:0xc
	v_mov_b32_dpp v17, v235 row_shr:8 row_mask:0xf bank_mask:0xc
	s_mov_b32 s4, 0x58000
	v_lshl_add_u64 v[230:231], s[4:5], 0, v[228:229]
	global_store_dwordx4 v[230:231], v[14:17], off
	s_mov_b32 s4, 0x5c000
	v_lshl_add_u64 v[230:231], s[4:5], 0, v[228:229]
	global_store_dwordx4 v[230:231], v[6:9], off
	s_and_b64 vcc, exec, s[2:3]
	s_mov_b64 s[2:3], -1
	s_cbranch_vccnz .LBB0_1451
	s_andn2_b64 vcc, exec, s[12:13]
	s_cbranch_vccnz .LBB0_1450
	s_barrier
	s_branch .LBB0_1450

.LBB0_2887:
	v_and_b32_e32 v224, -9, v154
	v_lshl_add_u32 v224, s65, 8, v224
	v_ashrrev_i32_e32 v225, 31, v224
	v_lshrrev_b32_e32 v226, 5, v156
	v_lshlrev_b32_e32 v226, 6, v226
	v_lshl_or_b32 v226, s66, 8, v226
	v_and_b32_e32 v232, 4, v156
	v_and_b32_e32 v233, 8, v156
	v_lshl_add_u32 v226, v232, 2, v226
	v_add_u32_e32 v226, v226, v233
	v_and_b32_e32 v232, 8, v154
	v_lshl_add_u32 v226, v232, 2, v226
	v_lshlrev_b32_e32 v226, 1, v226
	v_mov_b32_e32 v227, 0
	s_mov_b32 s21, 0
	v_lshlrev_b64 v[230:231], 11, v[224:225]
	v_lshl_add_u64 v[228:229], s[12:13], 0, v[230:231]
	v_lshl_add_u64 v[228:229], v[228:229], 0, v[226:227]
	s_mov_b32 s20, 0x0
	v_lshl_add_u64 v[230:231], s[20:21], 0, v[228:229]
	global_load_dwordx4 v[132:135], v[230:231], off
	s_mov_b32 s20, 0x4000
	v_lshl_add_u64 v[230:231], s[20:21], 0, v[228:229]
	global_load_dwordx4 v[136:139], v[230:231], off
	s_mov_b32 s20, 0x8000
	v_lshl_add_u64 v[230:231], s[20:21], 0, v[228:229]
	global_load_dwordx4 v[140:143], v[230:231], off
	s_mov_b32 s20, 0xc000
	v_lshl_add_u64 v[230:231], s[20:21], 0, v[228:229]
	global_load_dwordx4 v[144:147], v[230:231], off
	s_mov_b32 s20, 0x10000
	v_lshl_add_u64 v[230:231], s[20:21], 0, v[228:229]
	global_load_dwordx4 v[148:151], v[230:231], off
	s_mov_b32 s20, 0x14000
	v_lshl_add_u64 v[230:231], s[20:21], 0, v[228:229]
	global_load_dwordx4 v[158:161], v[230:231], off
	s_mov_b32 s20, 0x18000
	v_lshl_add_u64 v[230:231], s[20:21], 0, v[228:229]
	global_load_dwordx4 v[172:175], v[230:231], off
	s_mov_b32 s20, 0x1c000
	v_lshl_add_u64 v[230:231], s[20:21], 0, v[228:229]
	global_load_dwordx4 v[176:179], v[230:231], off
	s_mov_b32 s20, 0x40000
	v_lshl_add_u64 v[230:231], s[20:21], 0, v[228:229]
	global_load_dwordx4 v[180:183], v[230:231], off
	s_mov_b32 s20, 0x44000
	v_lshl_add_u64 v[230:231], s[20:21], 0, v[228:229]
	global_load_dwordx4 v[184:187], v[230:231], off
	s_mov_b32 s20, 0x48000
	v_lshl_add_u64 v[230:231], s[20:21], 0, v[228:229]
	global_load_dwordx4 v[188:191], v[230:231], off
	s_mov_b32 s20, 0x4c000
	v_lshl_add_u64 v[230:231], s[20:21], 0, v[228:229]
	global_load_dwordx4 v[192:195], v[230:231], off
	s_mov_b32 s20, 0x50000
	v_lshl_add_u64 v[230:231], s[20:21], 0, v[228:229]
	global_load_dwordx4 v[196:199], v[230:231], off
	s_mov_b32 s20, 0x54000
	v_lshl_add_u64 v[230:231], s[20:21], 0, v[228:229]
	global_load_dwordx4 v[212:215], v[230:231], off
	s_mov_b32 s20, 0x58000
	v_lshl_add_u64 v[230:231], s[20:21], 0, v[228:229]
	global_load_dwordx4 v[216:219], v[230:231], off
	s_mov_b32 s20, 0x5c000
	v_lshl_add_u64 v[230:231], s[20:21], 0, v[228:229]
	global_load_dwordx4 v[220:223], v[230:231], off
	s_and_b64 vcc, exec, s[16:17]
	s_cbranch_vccz .Lrf_ffn2_nobarb
	s_barrier
.Lrf_ffn2_nobarb:
	s_waitcnt vmcnt(14)
	v_mov_b32_e32 v232, v132
	v_mov_b32_e32 v233, v133
	v_mov_b32_e32 v234, v134
	v_mov_b32_e32 v235, v135
	v_mov_b32_dpp v132, v136 row_shr:8 row_mask:0xf bank_mask:0xc
	v_mov_b32_dpp v133, v137 row_shr:8 row_mask:0xf bank_mask:0xc
	v_mov_b32_dpp v134, v138 row_shr:8 row_mask:0xf bank_mask:0xc
	v_mov_b32_dpp v135, v139 row_shr:8 row_mask:0xf bank_mask:0xc
	v_mov_b32_dpp v136, v232 row_shl:8 row_mask:0xf bank_mask:0x3
	v_mov_b32_dpp v137, v233 row_shl:8 row_mask:0xf bank_mask:0x3
	v_mov_b32_dpp v138, v234 row_shl:8 row_mask:0xf bank_mask:0x3
	v_mov_b32_dpp v139, v235 row_shl:8 row_mask:0xf bank_mask:0x3
	s_nop 1
	v_permlane16_swap_b32_e32 v132, v134
	v_permlane16_swap_b32_e32 v133, v135
	v_lshlrev_b32_e32 v236, 16, v132
	v_and_b32_e32 v237, 0xffff0000, v132
	v_pk_fma_f32 v[126:127], v[166:167], v[126:127], v[236:237]
	v_lshlrev_b32_e32 v238, 16, v133
	v_and_b32_e32 v239, 0xffff0000, v133
	v_pk_fma_f32 v[128:129], v[166:167], v[128:129], v[238:239]
	v_lshlrev_b32_e32 v236, 16, v134
	v_and_b32_e32 v237, 0xffff0000, v134
	v_pk_fma_f32 v[122:123], v[166:167], v[122:123], v[236:237]
	v_lshlrev_b32_e32 v238, 16, v135
	v_and_b32_e32 v239, 0xffff0000, v135
	v_pk_fma_f32 v[124:125], v[166:167], v[124:125], v[238:239]
	v_cvt_pk_bf16_f32 v126, v126, v127
	v_cvt_pk_bf16_f32 v127, v128, v129
	v_cvt_pk_bf16_f32 v128, v122, v123
	v_cvt_pk_bf16_f32 v129, v124, v125
	s_nop 1
	v_permlane16_swap_b32_e32 v126, v128
	v_permlane16_swap_b32_e32 v127, v129
	v_permlane16_swap_b32_e32 v136, v138
	v_permlane16_swap_b32_e32 v137, v139
	v_lshlrev_b32_e32 v236, 16, v136
	v_and_b32_e32 v237, 0xffff0000, v136
	v_pk_fma_f32 v[118:119], v[166:167], v[118:119], v[236:237]
	v_lshlrev_b32_e32 v238, 16, v137
	v_and_b32_e32 v239, 0xffff0000, v137
	v_pk_fma_f32 v[120:121], v[166:167], v[120:121], v[238:239]
	v_lshlrev_b32_e32 v236, 16, v138
	v_and_b32_e32 v237, 0xffff0000, v138
	v_pk_fma_f32 v[114:115], v[166:167], v[114:115], v[236:237]
	v_lshlrev_b32_e32 v238, 16, v139
	v_and_b32_e32 v239, 0xffff0000, v139
	v_pk_fma_f32 v[116:117], v[166:167], v[116:117], v[238:239]
	v_cvt_pk_bf16_f32 v118, v118, v119
	v_cvt_pk_bf16_f32 v119, v120, v121
	v_cvt_pk_bf16_f32 v120, v114, v115
	v_cvt_pk_bf16_f32 v121, v116, v117
	s_nop 1
	v_permlane16_swap_b32_e32 v118, v120
	v_permlane16_swap_b32_e32 v119, v121
	s_waitcnt vmcnt(12)
	v_mov_b32_e32 v232, v140
	v_mov_b32_e32 v233, v141
	v_mov_b32_e32 v234, v142
	v_mov_b32_e32 v235, v143
	v_mov_b32_dpp v140, v144 row_shr:8 row_mask:0xf bank_mask:0xc
	v_mov_b32_dpp v141, v145 row_shr:8 row_mask:0xf bank_mask:0xc
	v_mov_b32_dpp v142, v146 row_shr:8 row_mask:0xf bank_mask:0xc
	v_mov_b32_dpp v143, v147 row_shr:8 row_mask:0xf bank_mask:0xc
	v_mov_b32_dpp v144, v232 row_shl:8 row_mask:0xf bank_mask:0x3
	v_mov_b32_dpp v145, v233 row_shl:8 row_mask:0xf bank_mask:0x3
	v_mov_b32_dpp v146, v234 row_shl:8 row_mask:0xf bank_mask:0x3
	v_mov_b32_dpp v147, v235 row_shl:8 row_mask:0xf bank_mask:0x3
	s_nop 1
	v_permlane16_swap_b32_e32 v140, v142
	v_permlane16_swap_b32_e32 v141, v143
	v_lshlrev_b32_e32 v236, 16, v140
	v_and_b32_e32 v237, 0xffff0000, v140
	v_pk_fma_f32 v[110:111], v[166:167], v[110:111], v[236:237]
	v_lshlrev_b32_e32 v238, 16, v141
	v_and_b32_e32 v239, 0xffff0000, v141
	v_pk_fma_f32 v[112:113], v[166:167], v[112:113], v[238:239]
	v_lshlrev_b32_e32 v236, 16, v142
	v_and_b32_e32 v237, 0xffff0000, v142
	v_pk_fma_f32 v[106:107], v[166:167], v[106:107], v[236:237]
	v_lshlrev_b32_e32 v238, 16, v143
	v_and_b32_e32 v239, 0xffff0000, v143
	v_pk_fma_f32 v[108:109], v[166:167], v[108:109], v[238:239]
	v_cvt_pk_bf16_f32 v110, v110, v111
	v_cvt_pk_bf16_f32 v111, v112, v113
	v_cvt_pk_bf16_f32 v112, v106, v107
	v_cvt_pk_bf16_f32 v113, v108, v109
	s_nop 1
	v_permlane16_swap_b32_e32 v110, v112
	v_permlane16_swap_b32_e32 v111, v113
	v_permlane16_swap_b32_e32 v144, v146
	v_permlane16_swap_b32_e32 v145, v147
	v_lshlrev_b32_e32 v236, 16, v144
	v_and_b32_e32 v237, 0xffff0000, v144
	v_pk_fma_f32 v[102:103], v[166:167], v[102:103], v[236:237]
	v_lshlrev_b32_e32 v238, 16, v145
	v_and_b32_e32 v239, 0xffff0000, v145
	v_pk_fma_f32 v[104:105], v[166:167], v[104:105], v[238:239]
	v_lshlrev_b32_e32 v236, 16, v146
	v_and_b32_e32 v237, 0xffff0000, v146
	v_pk_fma_f32 v[98:99], v[166:167], v[98:99], v[236:237]
	v_lshlrev_b32_e32 v238, 16, v147
	v_and_b32_e32 v239, 0xffff0000, v147
	v_pk_fma_f32 v[100:101], v[166:167], v[100:101], v[238:239]
	v_cvt_pk_bf16_f32 v102, v102, v103
	v_cvt_pk_bf16_f32 v103, v104, v105
	v_cvt_pk_bf16_f32 v104, v98, v99
	v_cvt_pk_bf16_f32 v105, v100, v101
	s_nop 1
	v_permlane16_swap_b32_e32 v102, v104
	v_permlane16_swap_b32_e32 v103, v105
	s_waitcnt vmcnt(10)
	v_mov_b32_e32 v232, v148
	v_mov_b32_e32 v233, v149
	v_mov_b32_e32 v234, v150
	v_mov_b32_e32 v235, v151
	v_mov_b32_dpp v148, v158 row_shr:8 row_mask:0xf bank_mask:0xc
	v_mov_b32_dpp v149, v159 row_shr:8 row_mask:0xf bank_mask:0xc
	v_mov_b32_dpp v150, v160 row_shr:8 row_mask:0xf bank_mask:0xc
	v_mov_b32_dpp v151, v161 row_shr:8 row_mask:0xf bank_mask:0xc
	v_mov_b32_dpp v158, v232 row_shl:8 row_mask:0xf bank_mask:0x3
	v_mov_b32_dpp v159, v233 row_shl:8 row_mask:0xf bank_mask:0x3
	v_mov_b32_dpp v160, v234 row_shl:8 row_mask:0xf bank_mask:0x3
	v_mov_b32_dpp v161, v235 row_shl:8 row_mask:0xf bank_mask:0x3
	s_nop 1
	v_permlane16_swap_b32_e32 v148, v150
	v_permlane16_swap_b32_e32 v149, v151
	v_lshlrev_b32_e32 v236, 16, v148
	v_and_b32_e32 v237, 0xffff0000, v148
	v_pk_fma_f32 v[94:95], v[166:167], v[94:95], v[236:237]
	v_lshlrev_b32_e32 v238, 16, v149
	v_and_b32_e32 v239, 0xffff0000, v149
	v_pk_fma_f32 v[96:97], v[166:167], v[96:97], v[238:239]
	v_lshlrev_b32_e32 v236, 16, v150
	v_and_b32_e32 v237, 0xffff0000, v150
	v_pk_fma_f32 v[90:91], v[166:167], v[90:91], v[236:237]
	v_lshlrev_b32_e32 v238, 16, v151
	v_and_b32_e32 v239, 0xffff0000, v151
	v_pk_fma_f32 v[92:93], v[166:167], v[92:93], v[238:239]
	v_cvt_pk_bf16_f32 v94, v94, v95
	v_cvt_pk_bf16_f32 v95, v96, v97
	v_cvt_pk_bf16_f32 v96, v90, v91
	v_cvt_pk_bf16_f32 v97, v92, v93
	s_nop 1
	v_permlane16_swap_b32_e32 v94, v96
	v_permlane16_swap_b32_e32 v95, v97
	v_permlane16_swap_b32_e32 v158, v160
	v_permlane16_swap_b32_e32 v159, v161
	v_lshlrev_b32_e32 v236, 16, v158
	v_and_b32_e32 v237, 0xffff0000, v158
	v_pk_fma_f32 v[86:87], v[166:167], v[86:87], v[236:237]
	v_lshlrev_b32_e32 v238, 16, v159
	v_and_b32_e32 v239, 0xffff0000, v159
	v_pk_fma_f32 v[88:89], v[166:167], v[88:89], v[238:239]
	v_lshlrev_b32_e32 v236, 16, v160
	v_and_b32_e32 v237, 0xffff0000, v160
	v_pk_fma_f32 v[82:83], v[166:167], v[82:83], v[236:237]
	v_lshlrev_b32_e32 v238, 16, v161
	v_and_b32_e32 v239, 0xffff0000, v161
	v_pk_fma_f32 v[84:85], v[166:167], v[84:85], v[238:239]
	v_cvt_pk_bf16_f32 v86, v86, v87
	v_cvt_pk_bf16_f32 v87, v88, v89
	v_cvt_pk_bf16_f32 v88, v82, v83
	v_cvt_pk_bf16_f32 v89, v84, v85
	s_nop 1
	v_permlane16_swap_b32_e32 v86, v88
	v_permlane16_swap_b32_e32 v87, v89
	s_waitcnt vmcnt(8)
	v_mov_b32_e32 v232, v172
	v_mov_b32_e32 v233, v173
	v_mov_b32_e32 v234, v174
	v_mov_b32_e32 v235, v175
	v_mov_b32_dpp v172, v176 row_shr:8 row_mask:0xf bank_mask:0xc
	v_mov_b32_dpp v173, v177 row_shr:8 row_mask:0xf bank_mask:0xc
	v_mov_b32_dpp v174, v178 row_shr:8 row_mask:0xf bank_mask:0xc
	v_mov_b32_dpp v175, v179 row_shr:8 row_mask:0xf bank_mask:0xc
	v_mov_b32_dpp v176, v232 row_shl:8 row_mask:0xf bank_mask:0x3
	v_mov_b32_dpp v177, v233 row_shl:8 row_mask:0xf bank_mask:0x3
	v_mov_b32_dpp v178, v234 row_shl:8 row_mask:0xf bank_mask:0x3
	v_mov_b32_dpp v179, v235 row_shl:8 row_mask:0xf bank_mask:0x3
	s_nop 1
	v_permlane16_swap_b32_e32 v172, v174
	v_permlane16_swap_b32_e32 v173, v175
	v_lshlrev_b32_e32 v236, 16, v172
	v_and_b32_e32 v237, 0xffff0000, v172
	v_pk_fma_f32 v[78:79], v[166:167], v[78:79], v[236:237]
	v_lshlrev_b32_e32 v238, 16, v173
	v_and_b32_e32 v239, 0xffff0000, v173
	v_pk_fma_f32 v[80:81], v[166:167], v[80:81], v[238:239]
	v_lshlrev_b32_e32 v236, 16, v174
	v_and_b32_e32 v237, 0xffff0000, v174
	v_pk_fma_f32 v[74:75], v[166:167], v[74:75], v[236:237]
	v_lshlrev_b32_e32 v238, 16, v175
	v_and_b32_e32 v239, 0xffff0000, v175
	v_pk_fma_f32 v[76:77], v[166:167], v[76:77], v[238:239]
	v_cvt_pk_bf16_f32 v78, v78, v79
	v_cvt_pk_bf16_f32 v79, v80, v81
	v_cvt_pk_bf16_f32 v80, v74, v75
	v_cvt_pk_bf16_f32 v81, v76, v77
	s_nop 1
	v_permlane16_swap_b32_e32 v78, v80
	v_permlane16_swap_b32_e32 v79, v81
	v_permlane16_swap_b32_e32 v176, v178
	v_permlane16_swap_b32_e32 v177, v179
	v_lshlrev_b32_e32 v236, 16, v176
	v_and_b32_e32 v237, 0xffff0000, v176
	v_pk_fma_f32 v[70:71], v[166:167], v[70:71], v[236:237]
	v_lshlrev_b32_e32 v238, 16, v177
	v_and_b32_e32 v239, 0xffff0000, v177
	v_pk_fma_f32 v[72:73], v[166:167], v[72:73], v[238:239]
	v_lshlrev_b32_e32 v236, 16, v178
	v_and_b32_e32 v237, 0xffff0000, v178
	v_pk_fma_f32 v[66:67], v[166:167], v[66:67], v[236:237]
	v_lshlrev_b32_e32 v238, 16, v179
	v_and_b32_e32 v239, 0xffff0000, v179
	v_pk_fma_f32 v[68:69], v[166:167], v[68:69], v[238:239]
	v_cvt_pk_bf16_f32 v70, v70, v71
	v_cvt_pk_bf16_f32 v71, v72, v73
	v_cvt_pk_bf16_f32 v72, v66, v67
	v_cvt_pk_bf16_f32 v73, v68, v69
	s_nop 1
	v_permlane16_swap_b32_e32 v70, v72
	v_permlane16_swap_b32_e32 v71, v73
	s_waitcnt vmcnt(6)
	v_mov_b32_e32 v232, v180
	v_mov_b32_e32 v233, v181
	v_mov_b32_e32 v234, v182
	v_mov_b32_e32 v235, v183
	v_mov_b32_dpp v180, v184 row_shr:8 row_mask:0xf bank_mask:0xc
	v_mov_b32_dpp v181, v185 row_shr:8 row_mask:0xf bank_mask:0xc
	v_mov_b32_dpp v182, v186 row_shr:8 row_mask:0xf bank_mask:0xc
	v_mov_b32_dpp v183, v187 row_shr:8 row_mask:0xf bank_mask:0xc
	v_mov_b32_dpp v184, v232 row_shl:8 row_mask:0xf bank_mask:0x3
	v_mov_b32_dpp v185, v233 row_shl:8 row_mask:0xf bank_mask:0x3
	v_mov_b32_dpp v186, v234 row_shl:8 row_mask:0xf bank_mask:0x3
	v_mov_b32_dpp v187, v235 row_shl:8 row_mask:0xf bank_mask:0x3
	s_nop 1
	v_permlane16_swap_b32_e32 v180, v182
	v_permlane16_swap_b32_e32 v181, v183
	v_lshlrev_b32_e32 v236, 16, v180
	v_and_b32_e32 v237, 0xffff0000, v180
	v_pk_fma_f32 v[62:63], v[166:167], v[62:63], v[236:237]
	v_lshlrev_b32_e32 v238, 16, v181
	v_and_b32_e32 v239, 0xffff0000, v181
	v_pk_fma_f32 v[64:65], v[166:167], v[64:65], v[238:239]
	v_lshlrev_b32_e32 v236, 16, v182
	v_and_b32_e32 v237, 0xffff0000, v182
	v_pk_fma_f32 v[58:59], v[166:167], v[58:59], v[236:237]
	v_lshlrev_b32_e32 v238, 16, v183
	v_and_b32_e32 v239, 0xffff0000, v183
	v_pk_fma_f32 v[60:61], v[166:167], v[60:61], v[238:239]
	v_cvt_pk_bf16_f32 v62, v62, v63
	v_cvt_pk_bf16_f32 v63, v64, v65
	v_cvt_pk_bf16_f32 v64, v58, v59
	v_cvt_pk_bf16_f32 v65, v60, v61
	s_nop 1
	v_permlane16_swap_b32_e32 v62, v64
	v_permlane16_swap_b32_e32 v63, v65
	v_permlane16_swap_b32_e32 v184, v186
	v_permlane16_swap_b32_e32 v185, v187
	v_lshlrev_b32_e32 v236, 16, v184
	v_and_b32_e32 v237, 0xffff0000, v184
	v_pk_fma_f32 v[54:55], v[166:167], v[54:55], v[236:237]
	v_lshlrev_b32_e32 v238, 16, v185
	v_and_b32_e32 v239, 0xffff0000, v185
	v_pk_fma_f32 v[56:57], v[166:167], v[56:57], v[238:239]
	v_lshlrev_b32_e32 v236, 16, v186
	v_and_b32_e32 v237, 0xffff0000, v186
	v_pk_fma_f32 v[50:51], v[166:167], v[50:51], v[236:237]
	v_lshlrev_b32_e32 v238, 16, v187
	v_and_b32_e32 v239, 0xffff0000, v187
	v_pk_fma_f32 v[52:53], v[166:167], v[52:53], v[238:239]
	v_cvt_pk_bf16_f32 v54, v54, v55
	v_cvt_pk_bf16_f32 v55, v56, v57
	v_cvt_pk_bf16_f32 v56, v50, v51
	v_cvt_pk_bf16_f32 v57, v52, v53
	s_nop 1
	v_permlane16_swap_b32_e32 v54, v56
	v_permlane16_swap_b32_e32 v55, v57
	s_waitcnt vmcnt(4)
	v_mov_b32_e32 v232, v188
	v_mov_b32_e32 v233, v189
	v_mov_b32_e32 v234, v190
	v_mov_b32_e32 v235, v191
	v_mov_b32_dpp v188, v192 row_shr:8 row_mask:0xf bank_mask:0xc
	v_mov_b32_dpp v189, v193 row_shr:8 row_mask:0xf bank_mask:0xc
	v_mov_b32_dpp v190, v194 row_shr:8 row_mask:0xf bank_mask:0xc
	v_mov_b32_dpp v191, v195 row_shr:8 row_mask:0xf bank_mask:0xc
	v_mov_b32_dpp v192, v232 row_shl:8 row_mask:0xf bank_mask:0x3
	v_mov_b32_dpp v193, v233 row_shl:8 row_mask:0xf bank_mask:0x3
	v_mov_b32_dpp v194, v234 row_shl:8 row_mask:0xf bank_mask:0x3
	v_mov_b32_dpp v195, v235 row_shl:8 row_mask:0xf bank_mask:0x3
	s_nop 1
	v_permlane16_swap_b32_e32 v188, v190
	v_permlane16_swap_b32_e32 v189, v191
	v_lshlrev_b32_e32 v236, 16, v188
	v_and_b32_e32 v237, 0xffff0000, v188
	v_pk_fma_f32 v[46:47], v[166:167], v[46:47], v[236:237]
	v_lshlrev_b32_e32 v238, 16, v189
	v_and_b32_e32 v239, 0xffff0000, v189
	v_pk_fma_f32 v[48:49], v[166:167], v[48:49], v[238:239]
	v_lshlrev_b32_e32 v236, 16, v190
	v_and_b32_e32 v237, 0xffff0000, v190
	v_pk_fma_f32 v[42:43], v[166:167], v[42:43], v[236:237]
	v_lshlrev_b32_e32 v238, 16, v191
	v_and_b32_e32 v239, 0xffff0000, v191
	v_pk_fma_f32 v[44:45], v[166:167], v[44:45], v[238:239]
	v_cvt_pk_bf16_f32 v46, v46, v47
	v_cvt_pk_bf16_f32 v47, v48, v49
	v_cvt_pk_bf16_f32 v48, v42, v43
	v_cvt_pk_bf16_f32 v49, v44, v45
	s_nop 1
	v_permlane16_swap_b32_e32 v46, v48
	v_permlane16_swap_b32_e32 v47, v49
	v_permlane16_swap_b32_e32 v192, v194
	v_permlane16_swap_b32_e32 v193, v195
	v_lshlrev_b32_e32 v236, 16, v192
	v_and_b32_e32 v237, 0xffff0000, v192
	v_pk_fma_f32 v[38:39], v[166:167], v[38:39], v[236:237]
	v_lshlrev_b32_e32 v238, 16, v193
	v_and_b32_e32 v239, 0xffff0000, v193
	v_pk_fma_f32 v[40:41], v[166:167], v[40:41], v[238:239]
	v_lshlrev_b32_e32 v236, 16, v194
	v_and_b32_e32 v237, 0xffff0000, v194
	v_pk_fma_f32 v[34:35], v[166:167], v[34:35], v[236:237]
	v_lshlrev_b32_e32 v238, 16, v195
	v_and_b32_e32 v239, 0xffff0000, v195
	v_pk_fma_f32 v[36:37], v[166:167], v[36:37], v[238:239]
	v_cvt_pk_bf16_f32 v38, v38, v39
	v_cvt_pk_bf16_f32 v39, v40, v41
	v_cvt_pk_bf16_f32 v40, v34, v35
	v_cvt_pk_bf16_f32 v41, v36, v37
	s_nop 1
	v_permlane16_swap_b32_e32 v38, v40
	v_permlane16_swap_b32_e32 v39, v41
	s_waitcnt vmcnt(2)
	v_mov_b32_e32 v232, v196
	v_mov_b32_e32 v233, v197
	v_mov_b32_e32 v234, v198
	v_mov_b32_e32 v235, v199
	v_mov_b32_dpp v196, v212 row_shr:8 row_mask:0xf bank_mask:0xc
	v_mov_b32_dpp v197, v213 row_shr:8 row_mask:0xf bank_mask:0xc
	v_mov_b32_dpp v198, v214 row_shr:8 row_mask:0xf bank_mask:0xc
	v_mov_b32_dpp v199, v215 row_shr:8 row_mask:0xf bank_mask:0xc
	v_mov_b32_dpp v212, v232 row_shl:8 row_mask:0xf bank_mask:0x3
	v_mov_b32_dpp v213, v233 row_shl:8 row_mask:0xf bank_mask:0x3
	v_mov_b32_dpp v214, v234 row_shl:8 row_mask:0xf bank_mask:0x3
	v_mov_b32_dpp v215, v235 row_shl:8 row_mask:0xf bank_mask:0x3
	s_nop 1
	v_permlane16_swap_b32_e32 v196, v198
	v_permlane16_swap_b32_e32 v197, v199
	v_lshlrev_b32_e32 v236, 16, v196
	v_and_b32_e32 v237, 0xffff0000, v196
	v_pk_fma_f32 v[30:31], v[166:167], v[30:31], v[236:237]
	v_lshlrev_b32_e32 v238, 16, v197
	v_and_b32_e32 v239, 0xffff0000, v197
	v_pk_fma_f32 v[32:33], v[166:167], v[32:33], v[238:239]
	v_lshlrev_b32_e32 v236, 16, v198
	v_and_b32_e32 v237, 0xffff0000, v198
	v_pk_fma_f32 v[26:27], v[166:167], v[26:27], v[236:237]
	v_lshlrev_b32_e32 v238, 16, v199
	v_and_b32_e32 v239, 0xffff0000, v199
	v_pk_fma_f32 v[28:29], v[166:167], v[28:29], v[238:239]
	v_cvt_pk_bf16_f32 v30, v30, v31
	v_cvt_pk_bf16_f32 v31, v32, v33
	v_cvt_pk_bf16_f32 v32, v26, v27
	v_cvt_pk_bf16_f32 v33, v28, v29
	s_nop 1
	v_permlane16_swap_b32_e32 v30, v32
	v_permlane16_swap_b32_e32 v31, v33
	v_permlane16_swap_b32_e32 v212, v214
	v_permlane16_swap_b32_e32 v213, v215
	v_lshlrev_b32_e32 v236, 16, v212
	v_and_b32_e32 v237, 0xffff0000, v212
	v_pk_fma_f32 v[22:23], v[166:167], v[22:23], v[236:237]
	v_lshlrev_b32_e32 v238, 16, v213
	v_and_b32_e32 v239, 0xffff0000, v213
	v_pk_fma_f32 v[24:25], v[166:167], v[24:25], v[238:239]
	v_lshlrev_b32_e32 v236, 16, v214
	v_and_b32_e32 v237, 0xffff0000, v214
	v_pk_fma_f32 v[18:19], v[166:167], v[18:19], v[236:237]
	v_lshlrev_b32_e32 v238, 16, v215
	v_and_b32_e32 v239, 0xffff0000, v215
	v_pk_fma_f32 v[20:21], v[166:167], v[20:21], v[238:239]
	v_cvt_pk_bf16_f32 v22, v22, v23
	v_cvt_pk_bf16_f32 v23, v24, v25
	v_cvt_pk_bf16_f32 v24, v18, v19
	v_cvt_pk_bf16_f32 v25, v20, v21
	s_nop 1
	v_permlane16_swap_b32_e32 v22, v24
	v_permlane16_swap_b32_e32 v23, v25
	s_waitcnt vmcnt(0)
	v_mov_b32_e32 v232, v216
	v_mov_b32_e32 v233, v217
	v_mov_b32_e32 v234, v218
	v_mov_b32_e32 v235, v219
	v_mov_b32_dpp v216, v220 row_shr:8 row_mask:0xf bank_mask:0xc
	v_mov_b32_dpp v217, v221 row_shr:8 row_mask:0xf bank_mask:0xc
	v_mov_b32_dpp v218, v222 row_shr:8 row_mask:0xf bank_mask:0xc
	v_mov_b32_dpp v219, v223 row_shr:8 row_mask:0xf bank_mask:0xc
	v_mov_b32_dpp v220, v232 row_shl:8 row_mask:0xf bank_mask:0x3
	v_mov_b32_dpp v221, v233 row_shl:8 row_mask:0xf bank_mask:0x3
	v_mov_b32_dpp v222, v234 row_shl:8 row_mask:0xf bank_mask:0x3
	v_mov_b32_dpp v223, v235 row_shl:8 row_mask:0xf bank_mask:0x3
	s_nop 1
	v_permlane16_swap_b32_e32 v216, v218
	v_permlane16_swap_b32_e32 v217, v219
	v_lshlrev_b32_e32 v236, 16, v216
	v_and_b32_e32 v237, 0xffff0000, v216
	v_pk_fma_f32 v[14:15], v[166:167], v[14:15], v[236:237]
	v_lshlrev_b32_e32 v238, 16, v217
	v_and_b32_e32 v239, 0xffff0000, v217
	v_pk_fma_f32 v[16:17], v[166:167], v[16:17], v[238:239]
	v_lshlrev_b32_e32 v236, 16, v218
	v_and_b32_e32 v237, 0xffff0000, v218
	v_pk_fma_f32 v[10:11], v[166:167], v[10:11], v[236:237]
	v_lshlrev_b32_e32 v238, 16, v219
	v_and_b32_e32 v239, 0xffff0000, v219
	v_pk_fma_f32 v[12:13], v[166:167], v[12:13], v[238:239]
	v_cvt_pk_bf16_f32 v14, v14, v15
	v_cvt_pk_bf16_f32 v15, v16, v17
	v_cvt_pk_bf16_f32 v16, v10, v11
	v_cvt_pk_bf16_f32 v17, v12, v13
	s_nop 1
	v_permlane16_swap_b32_e32 v14, v16
	v_permlane16_swap_b32_e32 v15, v17
	v_permlane16_swap_b32_e32 v220, v222
	v_permlane16_swap_b32_e32 v221, v223
	v_lshlrev_b32_e32 v236, 16, v220
	v_and_b32_e32 v237, 0xffff0000, v220
	v_pk_fma_f32 v[6:7], v[166:167], v[6:7], v[236:237]
	v_lshlrev_b32_e32 v238, 16, v221
	v_and_b32_e32 v239, 0xffff0000, v221
	v_pk_fma_f32 v[8:9], v[166:167], v[8:9], v[238:239]
	v_lshlrev_b32_e32 v236, 16, v222
	v_and_b32_e32 v237, 0xffff0000, v222
	v_pk_fma_f32 v[2:3], v[166:167], v[2:3], v[236:237]
	v_lshlrev_b32_e32 v238, 16, v223
	v_and_b32_e32 v239, 0xffff0000, v223
	v_pk_fma_f32 v[4:5], v[166:167], v[4:5], v[238:239]
	v_cvt_pk_bf16_f32 v6, v6, v7
	v_cvt_pk_bf16_f32 v7, v8, v9
	v_cvt_pk_bf16_f32 v8, v2, v3
	v_cvt_pk_bf16_f32 v9, v4, v5
	s_nop 1
	v_permlane16_swap_b32_e32 v6, v8
	v_permlane16_swap_b32_e32 v7, v9
	v_mov_b32_e32 v232, v118
	v_mov_b32_e32 v233, v119
	v_mov_b32_e32 v234, v120
	v_mov_b32_e32 v235, v121
	v_mov_b32_dpp v118, v126 row_shl:8 row_mask:0xf bank_mask:0x3
	v_mov_b32_dpp v119, v127 row_shl:8 row_mask:0xf bank_mask:0x3
	v_mov_b32_dpp v120, v128 row_shl:8 row_mask:0xf bank_mask:0x3
	v_mov_b32_dpp v121, v129 row_shl:8 row_mask:0xf bank_mask:0x3
	v_mov_b32_dpp v126, v232 row_shr:8 row_mask:0xf bank_mask:0xc
	v_mov_b32_dpp v127, v233 row_shr:8 row_mask:0xf bank_mask:0xc
	v_mov_b32_dpp v128, v234 row_shr:8 row_mask:0xf bank_mask:0xc
	v_mov_b32_dpp v129, v235 row_shr:8 row_mask:0xf bank_mask:0xc
	s_mov_b32 s20, 0x0
	v_lshl_add_u64 v[230:231], s[20:21], 0, v[228:229]
	global_store_dwordx4 v[230:231], v[126:129], off
	s_mov_b32 s20, 0x4000
	v_lshl_add_u64 v[230:231], s[20:21], 0, v[228:229]
	global_store_dwordx4 v[230:231], v[118:121], off
	v_mov_b32_e32 v232, v102
	v_mov_b32_e32 v233, v103
	v_mov_b32_e32 v234, v104
	v_mov_b32_e32 v235, v105
	v_mov_b32_dpp v102, v110 row_shl:8 row_mask:0xf bank_mask:0x3
	v_mov_b32_dpp v103, v111 row_shl:8 row_mask:0xf bank_mask:0x3
	v_mov_b32_dpp v104, v112 row_shl:8 row_mask:0xf bank_mask:0x3
	v_mov_b32_dpp v105, v113 row_shl:8 row_mask:0xf bank_mask:0x3
	v_mov_b32_dpp v110, v232 row_shr:8 row_mask:0xf bank_mask:0xc
	v_mov_b32_dpp v111, v233 row_shr:8 row_mask:0xf bank_mask:0xc
	v_mov_b32_dpp v112, v234 row_shr:8 row_mask:0xf bank_mask:0xc
	v_mov_b32_dpp v113, v235 row_shr:8 row_mask:0xf bank_mask:0xc
	s_mov_b32 s20, 0x8000
	v_lshl_add_u64 v[230:231], s[20:21], 0, v[228:229]
	global_store_dwordx4 v[230:231], v[110:113], off
	s_mov_b32 s20, 0xc000
	v_lshl_add_u64 v[230:231], s[20:21], 0, v[228:229]
	global_store_dwordx4 v[230:231], v[102:105], off
	v_mov_b32_e32 v232, v86
	v_mov_b32_e32 v233, v87
	v_mov_b32_e32 v234, v88
	v_mov_b32_e32 v235, v89
	v_mov_b32_dpp v86, v94 row_shl:8 row_mask:0xf bank_mask:0x3
	v_mov_b32_dpp v87, v95 row_shl:8 row_mask:0xf bank_mask:0x3
	v_mov_b32_dpp v88, v96 row_shl:8 row_mask:0xf bank_mask:0x3
	v_mov_b32_dpp v89, v97 row_shl:8 row_mask:0xf bank_mask:0x3
	v_mov_b32_dpp v94, v232 row_shr:8 row_mask:0xf bank_mask:0xc
	v_mov_b32_dpp v95, v233 row_shr:8 row_mask:0xf bank_mask:0xc
	v_mov_b32_dpp v96, v234 row_shr:8 row_mask:0xf bank_mask:0xc
	v_mov_b32_dpp v97, v235 row_shr:8 row_mask:0xf bank_mask:0xc
	s_mov_b32 s20, 0x10000
	v_lshl_add_u64 v[230:231], s[20:21], 0, v[228:229]
	global_store_dwordx4 v[230:231], v[94:97], off
	s_mov_b32 s20, 0x14000
	v_lshl_add_u64 v[230:231], s[20:21], 0, v[228:229]
	global_store_dwordx4 v[230:231], v[86:89], off
	v_mov_b32_e32 v232, v70
	v_mov_b32_e32 v233, v71
	v_mov_b32_e32 v234, v72
	v_mov_b32_e32 v235, v73
	v_mov_b32_dpp v70, v78 row_shl:8 row_mask:0xf bank_mask:0x3
	v_mov_b32_dpp v71, v79 row_shl:8 row_mask:0xf bank_mask:0x3
	v_mov_b32_dpp v72, v80 row_shl:8 row_mask:0xf bank_mask:0x3
	v_mov_b32_dpp v73, v81 row_shl:8 row_mask:0xf bank_mask:0x3
	v_mov_b32_dpp v78, v232 row_shr:8 row_mask:0xf bank_mask:0xc
	v_mov_b32_dpp v79, v233 row_shr:8 row_mask:0xf bank_mask:0xc
	v_mov_b32_dpp v80, v234 row_shr:8 row_mask:0xf bank_mask:0xc
	v_mov_b32_dpp v81, v235 row_shr:8 row_mask:0xf bank_mask:0xc
	s_mov_b32 s20, 0x18000
	v_lshl_add_u64 v[230:231], s[20:21], 0, v[228:229]
	global_store_dwordx4 v[230:231], v[78:81], off
	s_mov_b32 s20, 0x1c000
	v_lshl_add_u64 v[230:231], s[20:21], 0, v[228:229]
	global_store_dwordx4 v[230:231], v[70:73], off
	v_mov_b32_e32 v232, v54
	v_mov_b32_e32 v233, v55
	v_mov_b32_e32 v234, v56
	v_mov_b32_e32 v235, v57
	v_mov_b32_dpp v54, v62 row_shl:8 row_mask:0xf bank_mask:0x3
	v_mov_b32_dpp v55, v63 row_shl:8 row_mask:0xf bank_mask:0x3
	v_mov_b32_dpp v56, v64 row_shl:8 row_mask:0xf bank_mask:0x3
	v_mov_b32_dpp v57, v65 row_shl:8 row_mask:0xf bank_mask:0x3
	v_mov_b32_dpp v62, v232 row_shr:8 row_mask:0xf bank_mask:0xc
	v_mov_b32_dpp v63, v233 row_shr:8 row_mask:0xf bank_mask:0xc
	v_mov_b32_dpp v64, v234 row_shr:8 row_mask:0xf bank_mask:0xc
	v_mov_b32_dpp v65, v235 row_shr:8 row_mask:0xf bank_mask:0xc
	s_mov_b32 s20, 0x40000
	v_lshl_add_u64 v[230:231], s[20:21], 0, v[228:229]
	global_store_dwordx4 v[230:231], v[62:65], off
	s_mov_b32 s20, 0x44000
	v_lshl_add_u64 v[230:231], s[20:21], 0, v[228:229]
	global_store_dwordx4 v[230:231], v[54:57], off
	v_mov_b32_e32 v232, v38
	v_mov_b32_e32 v233, v39
	v_mov_b32_e32 v234, v40
	v_mov_b32_e32 v235, v41
	v_mov_b32_dpp v38, v46 row_shl:8 row_mask:0xf bank_mask:0x3
	v_mov_b32_dpp v39, v47 row_shl:8 row_mask:0xf bank_mask:0x3
	v_mov_b32_dpp v40, v48 row_shl:8 row_mask:0xf bank_mask:0x3
	v_mov_b32_dpp v41, v49 row_shl:8 row_mask:0xf bank_mask:0x3
	v_mov_b32_dpp v46, v232 row_shr:8 row_mask:0xf bank_mask:0xc
	v_mov_b32_dpp v47, v233 row_shr:8 row_mask:0xf bank_mask:0xc
	v_mov_b32_dpp v48, v234 row_shr:8 row_mask:0xf bank_mask:0xc
	v_mov_b32_dpp v49, v235 row_shr:8 row_mask:0xf bank_mask:0xc
	s_mov_b32 s20, 0x48000
	v_lshl_add_u64 v[230:231], s[20:21], 0, v[228:229]
	global_store_dwordx4 v[230:231], v[46:49], off
	s_mov_b32 s20, 0x4c000
	v_lshl_add_u64 v[230:231], s[20:21], 0, v[228:229]
	global_store_dwordx4 v[230:231], v[38:41], off
	v_mov_b32_e32 v232, v22
	v_mov_b32_e32 v233, v23
	v_mov_b32_e32 v234, v24
	v_mov_b32_e32 v235, v25
	v_mov_b32_dpp v22, v30 row_shl:8 row_mask:0xf bank_mask:0x3
	v_mov_b32_dpp v23, v31 row_shl:8 row_mask:0xf bank_mask:0x3
	v_mov_b32_dpp v24, v32 row_shl:8 row_mask:0xf bank_mask:0x3
	v_mov_b32_dpp v25, v33 row_shl:8 row_mask:0xf bank_mask:0x3
	v_mov_b32_dpp v30, v232 row_shr:8 row_mask:0xf bank_mask:0xc
	v_mov_b32_dpp v31, v233 row_shr:8 row_mask:0xf bank_mask:0xc
	v_mov_b32_dpp v32, v234 row_shr:8 row_mask:0xf bank_mask:0xc
	v_mov_b32_dpp v33, v235 row_shr:8 row_mask:0xf bank_mask:0xc
	s_mov_b32 s20, 0x50000
	v_lshl_add_u64 v[230:231], s[20:21], 0, v[228:229]
	global_store_dwordx4 v[230:231], v[30:33], off
	s_mov_b32 s20, 0x54000
	v_lshl_add_u64 v[230:231], s[20:21], 0, v[228:229]
	global_store_dwordx4 v[230:231], v[22:25], off
	v_mov_b32_e32 v232, v6
	v_mov_b32_e32 v233, v7
	v_mov_b32_e32 v234, v8
	v_mov_b32_e32 v235, v9
	v_mov_b32_dpp v6, v14 row_shl:8 row_mask:0xf bank_mask:0x3
	v_mov_b32_dpp v7, v15 row_shl:8 row_mask:0xf bank_mask:0x3
	v_mov_b32_dpp v8, v16 row_shl:8 row_mask:0xf bank_mask:0x3
	v_mov_b32_dpp v9, v17 row_shl:8 row_mask:0xf bank_mask:0x3
	v_mov_b32_dpp v14, v232 row_shr:8 row_mask:0xf bank_mask:0xc
	v_mov_b32_dpp v15, v233 row_shr:8 row_mask:0xf bank_mask:0xc
	v_mov_b32_dpp v16, v234 row_shr:8 row_mask:0xf bank_mask:0xc
	v_mov_b32_dpp v17, v235 row_shr:8 row_mask:0xf bank_mask:0xc
	s_mov_b32 s20, 0x58000
	v_lshl_add_u64 v[230:231], s[20:21], 0, v[228:229]
	global_store_dwordx4 v[230:231], v[14:17], off
	s_mov_b32 s20, 0x5c000
	v_lshl_add_u64 v[230:231], s[20:21], 0, v[228:229]
	global_store_dwordx4 v[230:231], v[6:9], off
	s_mov_b64 s[20:21], -1
	s_and_b64 vcc, exec, s[2:3]
	s_cbranch_vccnz .LBB0_2873
	s_andn2_b64 vcc, exec, s[10:11]
	s_cbranch_vccnz .LBB0_2872
	s_barrier
	s_branch .LBB0_2872
